# EpiGate epilogues (P5a, P6): gate/tmp loads hoisted and kept 6-10 deep in flight in dead fragment registers; IEEE division expansions replaced by v_rcp_f32 in P5/P6/P10 epilogues and ret_unit; counted
# baseline (speedup 1.0000x reference)
.LBB0_937:
	s_or_b64 exec, exec, s[94:95]
	s_add_i32 s0, 0, 0x23800
	v_add_u32_e32 v66, s0, v122
	s_waitcnt lgkmcnt(0)
	s_barrier
	ds_read_b64 v[66:67], v66
	s_lshl_b32 s94, s84, 2
	v_lshl_add_u64 v[138:139], v[138:139], 0, s[88:89]
	s_waitcnt lgkmcnt(0)
	v_sub_f32_e32 v42, v42, v66
	v_sub_f32_e32 v43, v43, v66
	v_sub_f32_e32 v58, v58, v66
	v_sub_f32_e32 v59, v59, v66
	v_mul_f32_e32 v42, v67, v42
	v_mul_f32_e32 v43, v67, v43
	v_mul_f32_e32 v58, v67, v58
	v_mul_f32_e32 v59, v67, v59
	v_cvt_pk_bf16_f32 v42, v42, v43
	v_sub_f32_e32 v43, v44, v66
	v_sub_f32_e32 v44, v45, v66
	v_cvt_pk_bf16_f32 v58, v58, v59
	v_sub_f32_e32 v59, v60, v66
	v_mul_f32_e32 v43, v67, v43
	v_mul_f32_e32 v44, v67, v44
	v_mul_f32_e32 v59, v67, v59
	v_sub_f32_e32 v60, v61, v66
	v_cvt_pk_bf16_f32 v43, v43, v44
	v_add_u32_e32 v44, 0x8800, v206
	v_mul_f32_e32 v60, v67, v60
	v_cvt_pk_bf16_f32 v59, v59, v60
	ds_write2_b64 v44, v[58:59], v[42:43] offset1:4
	v_add_u32_e32 v42, s0, v182
	ds_read_b64 v[42:43], v42
	s_waitcnt lgkmcnt(0)
	v_sub_f32_e32 v14, v14, v42
	v_sub_f32_e32 v15, v15, v42
	v_sub_f32_e32 v30, v30, v42
	v_sub_f32_e32 v31, v31, v42
	v_mul_f32_e32 v14, v43, v14
	v_mul_f32_e32 v15, v43, v15
	v_mul_f32_e32 v30, v43, v30
	v_mul_f32_e32 v31, v43, v31
	v_cvt_pk_bf16_f32 v14, v14, v15
	v_sub_f32_e32 v15, v16, v42
	v_sub_f32_e32 v16, v17, v42
	v_cvt_pk_bf16_f32 v30, v30, v31
	v_sub_f32_e32 v31, v32, v42
	v_mul_f32_e32 v15, v43, v15
	v_mul_f32_e32 v16, v43, v16
	v_mul_f32_e32 v31, v43, v31
	v_sub_f32_e32 v32, v33, v42
	v_cvt_pk_bf16_f32 v15, v15, v16
	v_add_u32_e32 v16, 0xa800, v206
	v_mul_f32_e32 v32, v43, v32
	v_cvt_pk_bf16_f32 v31, v31, v32
	ds_write2_b64 v16, v[30:31], v[14:15] offset0:32 offset1:36
	v_add_u32_e32 v14, s0, v183
	ds_read_b64 v[14:15], v14
	s_waitcnt lgkmcnt(0)
	v_sub_f32_e32 v16, v62, v14
	v_sub_f32_e32 v17, v63, v14
	v_mul_f32_e32 v16, v15, v16
	v_mul_f32_e32 v17, v15, v17
	v_cvt_pk_bf16_f32 v16, v16, v17
	v_sub_f32_e32 v17, v64, v14
	v_sub_f32_e32 v30, v65, v14
	v_mul_f32_e32 v17, v15, v17
	v_mul_f32_e32 v30, v15, v30
	v_cvt_pk_bf16_f32 v17, v17, v30
	v_sub_f32_e32 v30, v46, v14
	v_sub_f32_e32 v31, v47, v14
	v_mul_f32_e32 v30, v15, v30
	v_mul_f32_e32 v31, v15, v31
	v_cvt_pk_bf16_f32 v30, v30, v31
	v_sub_f32_e32 v31, v48, v14
	v_sub_f32_e32 v14, v49, v14
	v_mul_f32_e32 v31, v15, v31
	v_mul_f32_e32 v14, v15, v14
	v_cvt_pk_bf16_f32 v31, v31, v14
	v_add_u32_e32 v14, 0xc800, v206
	ds_write2_b64 v14, v[16:17], v[30:31] offset0:64 offset1:68
	v_add_u32_e32 v14, s0, v184
	ds_read_b64 v[14:15], v14
	s_waitcnt lgkmcnt(0)
	v_sub_f32_e32 v16, v34, v14
	v_sub_f32_e32 v17, v35, v14
	v_sub_f32_e32 v18, v18, v14
	v_sub_f32_e32 v19, v19, v14
	v_mul_f32_e32 v16, v15, v16
	v_mul_f32_e32 v17, v15, v17
	v_mul_f32_e32 v18, v15, v18
	v_mul_f32_e32 v19, v15, v19
	v_cvt_pk_bf16_f32 v16, v16, v17
	v_sub_f32_e32 v17, v36, v14
	v_sub_f32_e32 v30, v37, v14
	v_cvt_pk_bf16_f32 v18, v18, v19
	v_sub_f32_e32 v19, v20, v14
	v_sub_f32_e32 v14, v21, v14
	v_mul_f32_e32 v19, v15, v19
	v_mul_f32_e32 v14, v15, v14
	v_mul_f32_e32 v17, v15, v17
	v_cvt_pk_bf16_f32 v19, v19, v14
	v_add_u32_e32 v14, 0xe800, v206
	v_mul_f32_e32 v30, v15, v30
	v_cvt_pk_bf16_f32 v17, v17, v30
	ds_write2_b64 v14, v[16:17], v[18:19] offset0:96 offset1:100
	v_add_u32_e32 v14, s0, v185
	ds_read_b64 v[14:15], v14
	s_waitcnt lgkmcnt(0)
	v_sub_f32_e32 v16, v54, v14
	v_sub_f32_e32 v17, v55, v14
	v_mul_f32_e32 v16, v15, v16
	v_mul_f32_e32 v17, v15, v17
	v_cvt_pk_bf16_f32 v16, v16, v17
	v_sub_f32_e32 v17, v56, v14
	v_sub_f32_e32 v18, v57, v14
	v_mul_f32_e32 v17, v15, v17
	v_mul_f32_e32 v18, v15, v18
	v_cvt_pk_bf16_f32 v17, v17, v18
	v_sub_f32_e32 v18, v38, v14
	v_sub_f32_e32 v19, v39, v14
	v_mul_f32_e32 v18, v15, v18
	v_mul_f32_e32 v19, v15, v19
	v_cvt_pk_bf16_f32 v18, v18, v19
	v_sub_f32_e32 v19, v40, v14
	v_sub_f32_e32 v14, v41, v14
	v_mul_f32_e32 v19, v15, v19
	v_mul_f32_e32 v14, v15, v14
	v_cvt_pk_bf16_f32 v19, v19, v14
	v_add_u32_e32 v14, 0x8800, v207
	ds_write2_b64 v14, v[16:17], v[18:19] offset1:4
	v_add_u32_e32 v14, s0, v186
	ds_read_b64 v[14:15], v14
	v_or_b32_e32 v38, s11, v167
	v_mul_lo_u32 v124, v38, s96
	s_waitcnt lgkmcnt(0)
	v_sub_f32_e32 v6, v6, v14
	v_sub_f32_e32 v7, v7, v14
	v_sub_f32_e32 v16, v22, v14
	v_sub_f32_e32 v17, v23, v14
	v_mul_f32_e32 v6, v15, v6
	v_mul_f32_e32 v7, v15, v7
	v_mul_f32_e32 v16, v15, v16
	v_mul_f32_e32 v17, v15, v17
	v_cvt_pk_bf16_f32 v6, v6, v7
	v_sub_f32_e32 v7, v8, v14
	v_sub_f32_e32 v8, v9, v14
	v_cvt_pk_bf16_f32 v16, v16, v17
	v_sub_f32_e32 v17, v24, v14
	v_mul_f32_e32 v7, v15, v7
	v_mul_f32_e32 v8, v15, v8
	v_mul_f32_e32 v17, v15, v17
	v_sub_f32_e32 v18, v25, v14
	v_cvt_pk_bf16_f32 v7, v7, v8
	v_add_u32_e32 v8, 0xa800, v207
	v_mul_f32_e32 v18, v15, v18
	v_cvt_pk_bf16_f32 v17, v17, v18
	ds_write2_b64 v8, v[16:17], v[6:7] offset0:32 offset1:36
	v_add_u32_e32 v6, s0, v187
	ds_read_b64 v[6:7], v6
	s_waitcnt lgkmcnt(0)
	v_sub_f32_e32 v8, v26, v6
	v_sub_f32_e32 v9, v27, v6
	v_sub_f32_e32 v10, v10, v6
	v_sub_f32_e32 v11, v11, v6
	v_mul_f32_e32 v8, v7, v8
	v_mul_f32_e32 v9, v7, v9
	v_mul_f32_e32 v10, v7, v10
	v_mul_f32_e32 v11, v7, v11
	v_cvt_pk_bf16_f32 v8, v8, v9
	v_sub_f32_e32 v9, v28, v6
	v_sub_f32_e32 v14, v29, v6
	v_cvt_pk_bf16_f32 v10, v10, v11
	v_sub_f32_e32 v11, v12, v6
	v_sub_f32_e32 v6, v13, v6
	v_mul_f32_e32 v11, v7, v11
	v_mul_f32_e32 v6, v7, v6
	v_mul_f32_e32 v9, v7, v9
	v_cvt_pk_bf16_f32 v11, v11, v6
	v_add_u32_e32 v6, 0xc800, v207
	v_mul_f32_e32 v14, v7, v14
	v_cvt_pk_bf16_f32 v9, v9, v14
	ds_write2_b64 v6, v[8:9], v[10:11] offset0:64 offset1:68
	v_add_u32_e32 v6, s0, v188
	ds_read_b64 v[6:7], v6
	s_waitcnt lgkmcnt(0)
	v_sub_f32_e32 v2, v2, v6
	v_sub_f32_e32 v3, v3, v6
	v_mul_f32_e32 v2, v7, v2
	v_mul_f32_e32 v3, v7, v3
	v_cvt_pk_bf16_f32 v2, v2, v3
	v_sub_f32_e32 v3, v4, v6
	v_sub_f32_e32 v4, v5, v6
	v_mul_f32_e32 v3, v7, v3
	v_mul_f32_e32 v4, v7, v4
	v_cvt_pk_bf16_f32 v3, v3, v4
	v_sub_f32_e32 v4, v50, v6
	v_sub_f32_e32 v5, v51, v6
	v_mul_f32_e32 v4, v7, v4
	v_mul_f32_e32 v5, v7, v5
	v_cvt_pk_bf16_f32 v4, v4, v5
	v_sub_f32_e32 v5, v52, v6
	v_sub_f32_e32 v6, v53, v6
	v_mul_f32_e32 v5, v7, v5
	v_mul_f32_e32 v6, v7, v6
	v_cvt_pk_bf16_f32 v5, v5, v6
	v_add_u32_e32 v6, 0xe800, v207
	ds_write2_b64 v6, v[2:3], v[4:5] offset0:96 offset1:100
	v_mov_b32_e32 v2, s80
	s_waitcnt lgkmcnt(0)
	s_barrier
	ds_read_b64 v[2:3], v2
	v_lshlrev_b32_e32 v4, 1, v136
	v_mov_b32_e32 v5, v125
	s_waitcnt lgkmcnt(0)
	v_readfirstlane_b32 s0, v2
	v_readfirstlane_b32 s1, v3
	s_add_u32 s0, s0, s94
	s_addc_u32 s1, s1, 0
	v_lshlrev_b32_e32 v2, 2, v136
	s_nop 1
	global_load_dwordx4 v[34:37], v2, s[0:1] offset:16
	global_load_dwordx4 v[40:43], v2, s[0:1]
	v_lshl_add_u64 v[2:3], v[124:125], 1, s[82:83]
	s_lshl_b32 s0, s84, 1
	s_mov_b32 s1, s85
	v_lshl_add_u64 v[2:3], v[2:3], 0, s[0:1]
	v_lshl_add_u64 v[2:3], v[2:3], 0, v[4:5]
	v_add_co_u32_e32 v2, vcc, s8, v2
	s_add_i32 s10, s10, s52
	s_nop 0
	v_addc_co_u32_e32 v3, vcc, 0, v3, vcc
	global_load_dwordx4 v[30:33], v[2:3], off offset:2048
	v_add_u32_e32 v2, 0x4c000, v124
	v_mov_b32_e32 v3, v125
	v_lshl_add_u64 v[2:3], v[2:3], 1, s[82:83]
	v_lshl_add_u64 v[2:3], v[2:3], 0, s[0:1]
	v_lshl_add_u64 v[2:3], v[2:3], 0, v[4:5]
	v_add_co_u32_e32 v2, vcc, s8, v2
	s_add_i32 s81, s81, s33
	s_nop 0
	v_addc_co_u32_e32 v3, vcc, 0, v3, vcc
	global_load_dwordx4 v[26:29], v[2:3], off offset:2048
	v_add_u32_e32 v2, 0x98000, v124
	v_mov_b32_e32 v3, v125
	v_lshl_add_u64 v[2:3], v[2:3], 1, s[82:83]
	v_lshl_add_u64 v[2:3], v[2:3], 0, s[0:1]
	v_lshl_add_u64 v[2:3], v[2:3], 0, v[4:5]
	v_add_co_u32_e32 v2, vcc, s8, v2
	s_cmpk_lt_i32 s10, 0x200
	s_nop 0
	v_addc_co_u32_e32 v3, vcc, 0, v3, vcc
	global_load_dwordx4 v[22:25], v[2:3], off offset:2048
	v_add_u32_e32 v2, 0xe4000, v124
	v_mov_b32_e32 v3, v125
	v_lshl_add_u64 v[2:3], v[2:3], 1, s[82:83]
	v_lshl_add_u64 v[2:3], v[2:3], 0, s[0:1]
	v_lshl_add_u64 v[2:3], v[2:3], 0, v[4:5]
	v_add_co_u32_e32 v2, vcc, s8, v2
	s_waitcnt vmcnt(3)
	v_mul_f32_e32 v47, 0x41800000, v40
	v_addc_co_u32_e32 v3, vcc, 0, v3, vcc
	global_load_dwordx4 v[18:21], v[2:3], off offset:2048
	v_add_u32_e32 v2, 0x130000, v124
	v_mov_b32_e32 v3, v125
	v_lshl_add_u64 v[2:3], v[2:3], 1, s[82:83]
	v_lshl_add_u64 v[2:3], v[2:3], 0, s[0:1]
	v_lshl_add_u64 v[2:3], v[2:3], 0, v[4:5]
	v_add_co_u32_e32 v2, vcc, s8, v2
	s_waitcnt vmcnt(3)
	v_lshlrev_b32_e32 v48, 16, v30
	v_addc_co_u32_e32 v3, vcc, 0, v3, vcc
	global_load_dwordx4 v[14:17], v[2:3], off offset:2048
	v_add_u32_e32 v2, 0x17c000, v124
	v_mov_b32_e32 v3, v125
	v_lshl_add_u64 v[2:3], v[2:3], 1, s[82:83]
	v_lshl_add_u64 v[2:3], v[2:3], 0, s[0:1]
	v_lshl_add_u64 v[2:3], v[2:3], 0, v[4:5]
	v_add_co_u32_e32 v2, vcc, s8, v2
	v_mul_f32_e32 v49, 0xbfb8aa3b, v48
	s_nop 0
	v_addc_co_u32_e32 v3, vcc, 0, v3, vcc
	global_load_dwordx4 v[10:13], v[2:3], off offset:2048
	v_add_u32_e32 v2, 0x1c8000, v124
	v_mov_b32_e32 v3, v125
	v_lshl_add_u64 v[2:3], v[2:3], 1, s[82:83]
	v_lshl_add_u64 v[2:3], v[2:3], 0, s[0:1]
	v_exp_f32_e32 v49, v49
	v_lshl_add_u64 v[2:3], v[2:3], 0, v[4:5]
	v_add_co_u32_e32 v2, vcc, s8, v2
	v_add_u32_e32 v124, 0x214000, v124
	s_nop 0
	v_addc_co_u32_e32 v3, vcc, 0, v3, vcc
	global_load_dwordx4 v[6:9], v[2:3], off offset:2048
	v_lshl_add_u64 v[2:3], v[124:125], 1, s[82:83]
	v_add_f32_e32 v49, 1.0, v49
	v_lshl_add_u64 v[2:3], v[2:3], 0, s[0:1]
	v_lshl_add_u64 v[2:3], v[2:3], 0, v[4:5]
	v_add_co_u32_e32 v2, vcc, s8, v2
	s_nop 0
	s_nop 0
	v_addc_co_u32_e32 v3, vcc, 0, v3, vcc
	v_mul_f32_e32 v46, 0x41800000, v41
	v_mul_f32_e32 v45, 0x41800000, v42
	v_mul_f32_e32 v44, 0x41800000, v43
	v_mul_f32_e32 v43, 0x41800000, v34
	v_mul_f32_e32 v42, 0x41800000, v35
	v_mul_f32_e32 v41, 0x41800000, v36
	v_mul_f32_e32 v40, 0x41800000, v37
	ds_read_b128 v[34:37], v208 offset:34816
	s_waitcnt lgkmcnt(0)
	v_lshlrev_b32_e32 v39, 16, v34
	v_mul_f32_e32 v39, v47, v39
	v_rcp_f32_e32 v50, v49
	s_nop 0
	v_mul_f32_e32 v48, v48, v50
	v_and_b32_e32 v30, 0xffff0000, v30
	v_mul_f32_e32 v39, v48, v39
	v_mul_f32_e32 v48, 0xbfb8aa3b, v30
	v_exp_f32_e32 v48, v48
	v_and_b32_e32 v34, 0xffff0000, v34
	v_mul_f32_e32 v34, v46, v34
	global_load_dwordx4 v[2:5], v[2:3], off offset:2048
	v_add_f32_e32 v48, 1.0, v48
	v_or_b32_e32 v124, s11, v189
	v_rcp_f32_e32 v49, v48
	s_nop 0
	v_mul_f32_e32 v30, v30, v49
	v_lshlrev_b32_e32 v48, 16, v31
	v_mul_f32_e32 v49, 0xbfb8aa3b, v48
	v_exp_f32_e32 v49, v49
	v_mul_f32_e32 v30, v30, v34
	v_lshlrev_b32_e32 v34, 16, v35
	v_mul_f32_e32 v34, v45, v34
	v_add_f32_e32 v49, 1.0, v49
	v_and_b32_e32 v31, 0xffff0000, v31
	v_and_b32_e32 v35, 0xffff0000, v35
	v_mul_f32_e32 v35, v44, v35
	v_rcp_f32_e32 v50, v49
	s_nop 0
	v_mul_f32_e32 v48, v48, v50
	v_mul_f32_e32 v34, v48, v34
	v_mul_f32_e32 v48, 0xbfb8aa3b, v31
	v_exp_f32_e32 v48, v48
	v_med3_f32 v34, v34, s9, v214
	v_add_f32_e32 v48, 1.0, v48
	s_nop 0
	v_rcp_f32_e32 v49, v48
	s_nop 0
	v_mul_f32_e32 v31, v31, v49
	v_mul_f32_e32 v31, v31, v35
	v_med3_f32 v35, v39, s9, v214
	v_med3_f32 v39, v30, s9, v214
	v_mov_b32_e32 v30, v125
	v_cvt_pk_fp8_f32 v30, v35, v39
	v_med3_f32 v31, v31, s9, v214
	v_cvt_pk_fp8_f32 v30, v34, v31 op_sel:[0,0,1]
	v_lshlrev_b32_e32 v34, 16, v32
	v_mul_f32_e32 v35, 0xbfb8aa3b, v34
	v_exp_f32_e32 v35, v35
	v_and_b32_e32 v32, 0xffff0000, v32
	v_lshlrev_b32_e32 v31, 16, v36
	v_mul_f32_e32 v31, v43, v31
	v_add_f32_e32 v35, 1.0, v35
	s_nop 0
	v_rcp_f32_e32 v39, v35
	s_nop 0
	v_mul_f32_e32 v34, v34, v39
	v_mul_f32_e32 v35, 0xbfb8aa3b, v32
	v_exp_f32_e32 v35, v35
	v_mul_f32_e32 v31, v34, v31
	v_and_b32_e32 v34, 0xffff0000, v36
	v_mul_f32_e32 v34, v42, v34
	v_add_f32_e32 v35, 1.0, v35
	s_nop 0
	v_rcp_f32_e32 v36, v35
	s_nop 0
	v_mul_f32_e32 v32, v32, v36
	v_lshlrev_b32_e32 v35, 16, v33
	v_mul_f32_e32 v36, 0xbfb8aa3b, v35
	v_exp_f32_e32 v36, v36
	v_and_b32_e32 v33, 0xffff0000, v33
	v_mul_f32_e32 v32, v32, v34
	v_lshlrev_b32_e32 v34, 16, v37
	v_add_f32_e32 v36, 1.0, v36
	v_mul_f32_e32 v34, v41, v34
	v_med3_f32 v32, v32, s9, v214
	v_rcp_f32_e32 v39, v36
	s_nop 0
	v_mul_f32_e32 v35, v35, v39
	v_mul_f32_e32 v36, 0xbfb8aa3b, v33
	v_exp_f32_e32 v36, v36
	v_mul_f32_e32 v34, v35, v34
	v_and_b32_e32 v35, 0xffff0000, v37
	v_mul_f32_e32 v35, v40, v35
	v_add_f32_e32 v36, 1.0, v36
	v_med3_f32 v34, v34, s9, v214
	v_rcp_f32_e32 v37, v36
	s_nop 0
	v_mul_f32_e32 v33, v33, v37
	v_mul_f32_e32 v33, v33, v35
	v_med3_f32 v35, v31, s9, v214
	v_mov_b32_e32 v31, v125
	v_cvt_pk_fp8_f32 v31, v35, v32
	s_waitcnt vmcnt(6)
	v_lshlrev_b32_e32 v35, 16, v26
	v_mul_f32_e32 v36, 0xbfb8aa3b, v35
	v_exp_f32_e32 v36, v36
	v_med3_f32 v33, v33, s9, v214
	v_mov_b32_e32 v39, v125
	v_cvt_pk_fp8_f32 v31, v34, v33 op_sel:[0,0,1]
	v_add_f32_e32 v36, 1.0, v36
	v_lshlrev_b64 v[32:33], 11, v[38:39]
	v_lshl_add_u64 v[32:33], s[86:87], 0, v[32:33]
	v_lshl_add_u64 v[32:33], v[32:33], 0, s[84:85]
	v_lshl_add_u64 v[32:33], v[32:33], 0, v[136:137]
	global_store_dwordx2 v[32:33], v[30:31], off
	ds_read_b128 v[30:33], v208 offset:43264
	s_waitcnt lgkmcnt(0)
	v_lshlrev_b32_e32 v34, 16, v30
	v_mul_f32_e32 v34, v47, v34
	v_rcp_f32_e32 v37, v36
	s_nop 0
	v_mul_f32_e32 v35, v35, v37
	v_and_b32_e32 v26, 0xffff0000, v26
	v_mul_f32_e32 v34, v35, v34
	v_mul_f32_e32 v35, 0xbfb8aa3b, v26
	v_exp_f32_e32 v35, v35
	v_and_b32_e32 v30, 0xffff0000, v30
	v_mul_f32_e32 v30, v46, v30
	v_add_f32_e32 v35, 1.0, v35
	s_nop 0
	v_rcp_f32_e32 v36, v35
	s_nop 0
	v_mul_f32_e32 v26, v26, v36
	v_lshlrev_b32_e32 v35, 16, v27
	v_mul_f32_e32 v36, 0xbfb8aa3b, v35
	v_exp_f32_e32 v36, v36
	v_mul_f32_e32 v26, v26, v30
	v_lshlrev_b32_e32 v30, 16, v31
	v_mul_f32_e32 v30, v45, v30
	v_add_f32_e32 v36, 1.0, v36
	v_and_b32_e32 v27, 0xffff0000, v27
	v_and_b32_e32 v31, 0xffff0000, v31
	v_mul_f32_e32 v31, v44, v31
	v_rcp_f32_e32 v37, v36
	s_nop 0
	v_mul_f32_e32 v35, v35, v37
	v_mul_f32_e32 v30, v35, v30
	v_mul_f32_e32 v35, 0xbfb8aa3b, v27
	v_exp_f32_e32 v35, v35
	v_med3_f32 v30, v30, s9, v214
	v_add_f32_e32 v35, 1.0, v35
	s_nop 0
	v_rcp_f32_e32 v36, v35
	s_nop 0
	v_mul_f32_e32 v27, v27, v36
	v_mul_f32_e32 v27, v27, v31
	v_med3_f32 v31, v34, s9, v214
	v_med3_f32 v34, v26, s9, v214
	v_mov_b32_e32 v26, v125
	v_cvt_pk_fp8_f32 v26, v31, v34
	v_med3_f32 v27, v27, s9, v214
	v_cvt_pk_fp8_f32 v26, v30, v27 op_sel:[0,0,1]
	v_lshlrev_b32_e32 v30, 16, v28
	v_mul_f32_e32 v31, 0xbfb8aa3b, v30
	v_exp_f32_e32 v31, v31
	v_and_b32_e32 v28, 0xffff0000, v28
	v_lshlrev_b32_e32 v27, 16, v32
	v_mul_f32_e32 v27, v43, v27
	v_add_f32_e32 v31, 1.0, v31
	s_nop 0
	v_rcp_f32_e32 v34, v31
	s_nop 0
	v_mul_f32_e32 v30, v30, v34
	v_mul_f32_e32 v31, 0xbfb8aa3b, v28
	v_exp_f32_e32 v31, v31
	v_mul_f32_e32 v27, v30, v27
	v_and_b32_e32 v30, 0xffff0000, v32
	v_mul_f32_e32 v30, v42, v30
	v_add_f32_e32 v31, 1.0, v31
	s_nop 0
	v_rcp_f32_e32 v32, v31
	s_nop 0
	v_mul_f32_e32 v28, v28, v32
	v_lshlrev_b32_e32 v31, 16, v29
	v_mul_f32_e32 v32, 0xbfb8aa3b, v31
	v_exp_f32_e32 v32, v32
	v_and_b32_e32 v29, 0xffff0000, v29
	v_mul_f32_e32 v28, v28, v30
	v_lshlrev_b32_e32 v30, 16, v33
	v_add_f32_e32 v32, 1.0, v32
	v_mul_f32_e32 v30, v41, v30
	v_med3_f32 v28, v28, s9, v214
	v_rcp_f32_e32 v34, v32
	s_nop 0
	v_mul_f32_e32 v31, v31, v34
	v_mul_f32_e32 v32, 0xbfb8aa3b, v29
	v_exp_f32_e32 v32, v32
	v_mul_f32_e32 v30, v31, v30
	v_and_b32_e32 v31, 0xffff0000, v33
	v_mul_f32_e32 v31, v40, v31
	v_add_f32_e32 v32, 1.0, v32
	v_med3_f32 v30, v30, s9, v214
	v_rcp_f32_e32 v33, v32
	s_nop 0
	v_mul_f32_e32 v29, v29, v33
	v_mul_f32_e32 v29, v29, v31
	v_med3_f32 v31, v27, s9, v214
	v_mov_b32_e32 v27, v125
	v_cvt_pk_fp8_f32 v27, v31, v28
	s_waitcnt vmcnt(6)
	v_lshlrev_b32_e32 v31, 16, v22
	v_mul_f32_e32 v32, 0xbfb8aa3b, v31
	v_exp_f32_e32 v32, v32
	v_med3_f32 v29, v29, s9, v214
	v_cvt_pk_fp8_f32 v27, v30, v29 op_sel:[0,0,1]
	v_lshlrev_b64 v[28:29], 11, v[124:125]
	v_add_f32_e32 v32, 1.0, v32
	v_lshl_add_u64 v[28:29], s[86:87], 0, v[28:29]
	v_lshl_add_u64 v[28:29], v[28:29], 0, s[84:85]
	v_lshl_add_u64 v[28:29], v[28:29], 0, v[136:137]
	global_store_dwordx2 v[28:29], v[26:27], off
	ds_read_b128 v[26:29], v208 offset:51712
	s_waitcnt lgkmcnt(0)
	v_lshlrev_b32_e32 v30, 16, v26
	v_mul_f32_e32 v30, v47, v30
	v_rcp_f32_e32 v33, v32
	s_nop 0
	v_mul_f32_e32 v31, v31, v33
	v_and_b32_e32 v22, 0xffff0000, v22
	v_mul_f32_e32 v30, v31, v30
	v_mul_f32_e32 v31, 0xbfb8aa3b, v22
	v_exp_f32_e32 v31, v31
	v_and_b32_e32 v26, 0xffff0000, v26
	v_mul_f32_e32 v26, v46, v26
	v_or_b32_e32 v124, s11, v190
	v_add_f32_e32 v31, 1.0, v31
	s_nop 0
	v_rcp_f32_e32 v32, v31
	s_nop 0
	v_mul_f32_e32 v22, v22, v32
	v_lshlrev_b32_e32 v31, 16, v23
	v_mul_f32_e32 v32, 0xbfb8aa3b, v31
	v_exp_f32_e32 v32, v32
	v_mul_f32_e32 v22, v22, v26
	v_lshlrev_b32_e32 v26, 16, v27
	v_mul_f32_e32 v26, v45, v26
	v_add_f32_e32 v32, 1.0, v32
	v_and_b32_e32 v23, 0xffff0000, v23
	v_and_b32_e32 v27, 0xffff0000, v27
	v_mul_f32_e32 v27, v44, v27
	v_rcp_f32_e32 v33, v32
	s_nop 0
	v_mul_f32_e32 v31, v31, v33
	v_mul_f32_e32 v26, v31, v26
	v_mul_f32_e32 v31, 0xbfb8aa3b, v23
	v_exp_f32_e32 v31, v31
	v_med3_f32 v26, v26, s9, v214
	v_add_f32_e32 v31, 1.0, v31
	s_nop 0
	v_rcp_f32_e32 v32, v31
	s_nop 0
	v_mul_f32_e32 v23, v23, v32
	v_mul_f32_e32 v23, v23, v27
	v_med3_f32 v27, v30, s9, v214
	v_med3_f32 v30, v22, s9, v214
	v_mov_b32_e32 v22, v125
	v_cvt_pk_fp8_f32 v22, v27, v30
	v_med3_f32 v23, v23, s9, v214
	v_cvt_pk_fp8_f32 v22, v26, v23 op_sel:[0,0,1]
	v_lshlrev_b32_e32 v26, 16, v24
	v_mul_f32_e32 v27, 0xbfb8aa3b, v26
	v_exp_f32_e32 v27, v27
	v_and_b32_e32 v24, 0xffff0000, v24
	v_lshlrev_b32_e32 v23, 16, v28
	v_mul_f32_e32 v23, v43, v23
	v_add_f32_e32 v27, 1.0, v27
	s_nop 0
	v_rcp_f32_e32 v30, v27
	s_nop 0
	v_mul_f32_e32 v26, v26, v30
	v_mul_f32_e32 v27, 0xbfb8aa3b, v24
	v_exp_f32_e32 v27, v27
	v_mul_f32_e32 v23, v26, v23
	v_and_b32_e32 v26, 0xffff0000, v28
	v_mul_f32_e32 v26, v42, v26
	v_add_f32_e32 v27, 1.0, v27
	s_nop 0
	v_rcp_f32_e32 v28, v27
	s_nop 0
	v_mul_f32_e32 v24, v24, v28
	v_lshlrev_b32_e32 v27, 16, v25
	v_mul_f32_e32 v28, 0xbfb8aa3b, v27
	v_exp_f32_e32 v28, v28
	v_and_b32_e32 v25, 0xffff0000, v25
	v_mul_f32_e32 v24, v24, v26
	v_lshlrev_b32_e32 v26, 16, v29
	v_add_f32_e32 v28, 1.0, v28
	v_mul_f32_e32 v26, v41, v26
	v_med3_f32 v24, v24, s9, v214
	v_rcp_f32_e32 v30, v28
	s_nop 0
	v_mul_f32_e32 v27, v27, v30
	v_mul_f32_e32 v28, 0xbfb8aa3b, v25
	v_exp_f32_e32 v28, v28
	v_mul_f32_e32 v26, v27, v26
	v_and_b32_e32 v27, 0xffff0000, v29
	v_mul_f32_e32 v27, v40, v27
	v_add_f32_e32 v28, 1.0, v28
	v_med3_f32 v26, v26, s9, v214
	v_rcp_f32_e32 v29, v28
	s_nop 0
	v_mul_f32_e32 v25, v25, v29
	v_mul_f32_e32 v25, v25, v27
	v_med3_f32 v27, v23, s9, v214
	v_mov_b32_e32 v23, v125
	v_cvt_pk_fp8_f32 v23, v27, v24
	s_waitcnt vmcnt(6)
	v_lshlrev_b32_e32 v27, 16, v18
	v_mul_f32_e32 v28, 0xbfb8aa3b, v27
	v_exp_f32_e32 v28, v28
	v_med3_f32 v25, v25, s9, v214
	v_cvt_pk_fp8_f32 v23, v26, v25 op_sel:[0,0,1]
	v_lshlrev_b64 v[24:25], 11, v[124:125]
	v_add_f32_e32 v28, 1.0, v28
	v_lshl_add_u64 v[24:25], s[86:87], 0, v[24:25]
	v_lshl_add_u64 v[24:25], v[24:25], 0, s[84:85]
	v_lshl_add_u64 v[24:25], v[24:25], 0, v[136:137]
	global_store_dwordx2 v[24:25], v[22:23], off
	ds_read_b128 v[22:25], v208 offset:60160
	s_waitcnt lgkmcnt(0)
	v_lshlrev_b32_e32 v26, 16, v22
	v_mul_f32_e32 v26, v47, v26
	v_rcp_f32_e32 v29, v28
	s_nop 0
	v_mul_f32_e32 v27, v27, v29
	v_and_b32_e32 v18, 0xffff0000, v18
	v_mul_f32_e32 v26, v27, v26
	v_mul_f32_e32 v27, 0xbfb8aa3b, v18
	v_exp_f32_e32 v27, v27
	v_and_b32_e32 v22, 0xffff0000, v22
	v_mul_f32_e32 v22, v46, v22
	v_or_b32_e32 v124, s11, v191
	v_add_f32_e32 v27, 1.0, v27
	s_nop 0
	v_rcp_f32_e32 v28, v27
	s_nop 0
	v_mul_f32_e32 v18, v18, v28
	v_lshlrev_b32_e32 v27, 16, v19
	v_mul_f32_e32 v28, 0xbfb8aa3b, v27
	v_exp_f32_e32 v28, v28
	v_mul_f32_e32 v18, v18, v22
	v_lshlrev_b32_e32 v22, 16, v23
	v_mul_f32_e32 v22, v45, v22
	v_add_f32_e32 v28, 1.0, v28
	v_and_b32_e32 v19, 0xffff0000, v19
	v_and_b32_e32 v23, 0xffff0000, v23
	v_mul_f32_e32 v23, v44, v23
	v_rcp_f32_e32 v29, v28
	s_nop 0
	v_mul_f32_e32 v27, v27, v29
	v_mul_f32_e32 v22, v27, v22
	v_mul_f32_e32 v27, 0xbfb8aa3b, v19
	v_exp_f32_e32 v27, v27
	v_med3_f32 v22, v22, s9, v214
	v_add_f32_e32 v27, 1.0, v27
	s_nop 0
	v_rcp_f32_e32 v28, v27
	s_nop 0
	v_mul_f32_e32 v19, v19, v28
	v_mul_f32_e32 v19, v19, v23
	v_med3_f32 v23, v26, s9, v214
	v_med3_f32 v26, v18, s9, v214
	v_mov_b32_e32 v18, v125
	v_cvt_pk_fp8_f32 v18, v23, v26
	v_med3_f32 v19, v19, s9, v214
	v_cvt_pk_fp8_f32 v18, v22, v19 op_sel:[0,0,1]
	v_lshlrev_b32_e32 v22, 16, v20
	v_mul_f32_e32 v23, 0xbfb8aa3b, v22
	v_exp_f32_e32 v23, v23
	v_and_b32_e32 v20, 0xffff0000, v20
	v_lshlrev_b32_e32 v19, 16, v24
	v_mul_f32_e32 v19, v43, v19
	v_add_f32_e32 v23, 1.0, v23
	s_nop 0
	v_rcp_f32_e32 v26, v23
	s_nop 0
	v_mul_f32_e32 v22, v22, v26
	v_mul_f32_e32 v23, 0xbfb8aa3b, v20
	v_exp_f32_e32 v23, v23
	v_mul_f32_e32 v19, v22, v19
	v_and_b32_e32 v22, 0xffff0000, v24
	v_mul_f32_e32 v22, v42, v22
	v_add_f32_e32 v23, 1.0, v23
	s_nop 0
	v_rcp_f32_e32 v24, v23
	s_nop 0
	v_mul_f32_e32 v20, v20, v24
	v_lshlrev_b32_e32 v23, 16, v21
	v_mul_f32_e32 v24, 0xbfb8aa3b, v23
	v_exp_f32_e32 v24, v24
	v_and_b32_e32 v21, 0xffff0000, v21
	v_mul_f32_e32 v20, v20, v22
	v_lshlrev_b32_e32 v22, 16, v25
	v_add_f32_e32 v24, 1.0, v24
	v_mul_f32_e32 v22, v41, v22
	v_med3_f32 v20, v20, s9, v214
	v_rcp_f32_e32 v26, v24
	s_nop 0
	v_mul_f32_e32 v23, v23, v26
	v_mul_f32_e32 v24, 0xbfb8aa3b, v21
	v_exp_f32_e32 v24, v24
	v_mul_f32_e32 v22, v23, v22
	v_and_b32_e32 v23, 0xffff0000, v25
	v_mul_f32_e32 v23, v40, v23
	v_add_f32_e32 v24, 1.0, v24
	v_med3_f32 v22, v22, s9, v214
	v_rcp_f32_e32 v25, v24
	s_nop 0
	v_mul_f32_e32 v21, v21, v25
	v_mul_f32_e32 v21, v21, v23
	v_med3_f32 v23, v19, s9, v214
	v_mov_b32_e32 v19, v125
	v_cvt_pk_fp8_f32 v19, v23, v20
	s_waitcnt vmcnt(6)
	v_lshlrev_b32_e32 v23, 16, v14
	v_mul_f32_e32 v24, 0xbfb8aa3b, v23
	v_exp_f32_e32 v24, v24
	v_med3_f32 v21, v21, s9, v214
	v_cvt_pk_fp8_f32 v19, v22, v21 op_sel:[0,0,1]
	v_lshlrev_b64 v[20:21], 11, v[124:125]
	v_add_f32_e32 v24, 1.0, v24
	v_lshl_add_u64 v[20:21], s[86:87], 0, v[20:21]
	v_lshl_add_u64 v[20:21], v[20:21], 0, s[84:85]
	v_lshl_add_u64 v[20:21], v[20:21], 0, v[136:137]
	global_store_dwordx2 v[20:21], v[18:19], off
	ds_read_b128 v[18:21], v209 offset:34816
	s_waitcnt lgkmcnt(0)
	v_lshlrev_b32_e32 v22, 16, v18
	v_mul_f32_e32 v22, v47, v22
	v_rcp_f32_e32 v25, v24
	s_nop 0
	v_mul_f32_e32 v23, v23, v25
	v_and_b32_e32 v14, 0xffff0000, v14
	v_mul_f32_e32 v22, v23, v22
	v_mul_f32_e32 v23, 0xbfb8aa3b, v14
	v_exp_f32_e32 v23, v23
	v_and_b32_e32 v18, 0xffff0000, v18
	v_mul_f32_e32 v18, v46, v18
	v_or_b32_e32 v124, s11, v192
	v_add_f32_e32 v23, 1.0, v23
	s_nop 0
	v_rcp_f32_e32 v24, v23
	s_nop 0
	v_mul_f32_e32 v14, v14, v24
	v_lshlrev_b32_e32 v23, 16, v15
	v_mul_f32_e32 v24, 0xbfb8aa3b, v23
	v_exp_f32_e32 v24, v24
	v_mul_f32_e32 v14, v14, v18
	v_lshlrev_b32_e32 v18, 16, v19
	v_mul_f32_e32 v18, v45, v18
	v_add_f32_e32 v24, 1.0, v24
	v_and_b32_e32 v15, 0xffff0000, v15
	v_and_b32_e32 v19, 0xffff0000, v19
	v_mul_f32_e32 v19, v44, v19
	v_rcp_f32_e32 v25, v24
	s_nop 0
	v_mul_f32_e32 v23, v23, v25
	v_mul_f32_e32 v18, v23, v18
	v_mul_f32_e32 v23, 0xbfb8aa3b, v15
	v_exp_f32_e32 v23, v23
	v_med3_f32 v18, v18, s9, v214
	v_add_f32_e32 v23, 1.0, v23
	s_nop 0
	v_rcp_f32_e32 v24, v23
	s_nop 0
	v_mul_f32_e32 v15, v15, v24
	v_mul_f32_e32 v15, v15, v19
	v_med3_f32 v19, v22, s9, v214
	v_med3_f32 v22, v14, s9, v214
	v_mov_b32_e32 v14, v125
	v_cvt_pk_fp8_f32 v14, v19, v22
	v_med3_f32 v15, v15, s9, v214
	v_cvt_pk_fp8_f32 v14, v18, v15 op_sel:[0,0,1]
	v_lshlrev_b32_e32 v18, 16, v16
	v_mul_f32_e32 v19, 0xbfb8aa3b, v18
	v_exp_f32_e32 v19, v19
	v_and_b32_e32 v16, 0xffff0000, v16
	v_lshlrev_b32_e32 v15, 16, v20
	v_mul_f32_e32 v15, v43, v15
	v_add_f32_e32 v19, 1.0, v19
	s_nop 0
	v_rcp_f32_e32 v22, v19
	s_nop 0
	v_mul_f32_e32 v18, v18, v22
	v_mul_f32_e32 v19, 0xbfb8aa3b, v16
	v_exp_f32_e32 v19, v19
	v_mul_f32_e32 v15, v18, v15
	v_and_b32_e32 v18, 0xffff0000, v20
	v_mul_f32_e32 v18, v42, v18
	v_add_f32_e32 v19, 1.0, v19
	s_nop 0
	v_rcp_f32_e32 v20, v19
	s_nop 0
	v_mul_f32_e32 v16, v16, v20
	v_lshlrev_b32_e32 v19, 16, v17
	v_mul_f32_e32 v20, 0xbfb8aa3b, v19
	v_exp_f32_e32 v20, v20
	v_and_b32_e32 v17, 0xffff0000, v17
	v_mul_f32_e32 v16, v16, v18
	v_lshlrev_b32_e32 v18, 16, v21
	v_add_f32_e32 v20, 1.0, v20
	v_mul_f32_e32 v18, v41, v18
	v_med3_f32 v16, v16, s9, v214
	v_rcp_f32_e32 v22, v20
	s_nop 0
	v_mul_f32_e32 v19, v19, v22
	v_mul_f32_e32 v20, 0xbfb8aa3b, v17
	v_exp_f32_e32 v20, v20
	v_mul_f32_e32 v18, v19, v18
	v_and_b32_e32 v19, 0xffff0000, v21
	v_mul_f32_e32 v19, v40, v19
	v_add_f32_e32 v20, 1.0, v20
	v_med3_f32 v18, v18, s9, v214
	v_rcp_f32_e32 v21, v20
	s_nop 0
	v_mul_f32_e32 v17, v17, v21
	v_mul_f32_e32 v17, v17, v19
	v_med3_f32 v19, v15, s9, v214
	v_mov_b32_e32 v15, v125
	v_cvt_pk_fp8_f32 v15, v19, v16
	s_waitcnt vmcnt(6)
	v_lshlrev_b32_e32 v19, 16, v10
	v_mul_f32_e32 v20, 0xbfb8aa3b, v19
	v_exp_f32_e32 v20, v20
	v_med3_f32 v17, v17, s9, v214
	v_cvt_pk_fp8_f32 v15, v18, v17 op_sel:[0,0,1]
	v_lshlrev_b64 v[16:17], 11, v[124:125]
	v_add_f32_e32 v20, 1.0, v20
	v_lshl_add_u64 v[16:17], s[86:87], 0, v[16:17]
	v_lshl_add_u64 v[16:17], v[16:17], 0, s[84:85]
	v_lshl_add_u64 v[16:17], v[16:17], 0, v[136:137]
	global_store_dwordx2 v[16:17], v[14:15], off
	ds_read_b128 v[14:17], v209 offset:43264
	s_waitcnt lgkmcnt(0)
	v_lshlrev_b32_e32 v18, 16, v14
	v_mul_f32_e32 v18, v47, v18
	v_rcp_f32_e32 v21, v20
	s_nop 0
	v_mul_f32_e32 v19, v19, v21
	v_and_b32_e32 v10, 0xffff0000, v10
	v_mul_f32_e32 v18, v19, v18
	v_mul_f32_e32 v19, 0xbfb8aa3b, v10
	v_exp_f32_e32 v19, v19
	v_and_b32_e32 v14, 0xffff0000, v14
	v_mul_f32_e32 v14, v46, v14
	v_or_b32_e32 v124, s11, v193
	v_add_f32_e32 v19, 1.0, v19
	s_nop 0
	v_rcp_f32_e32 v20, v19
	s_nop 0
	v_mul_f32_e32 v10, v10, v20
	v_lshlrev_b32_e32 v19, 16, v11
	v_mul_f32_e32 v20, 0xbfb8aa3b, v19
	v_exp_f32_e32 v20, v20
	v_mul_f32_e32 v10, v10, v14
	v_lshlrev_b32_e32 v14, 16, v15
	v_mul_f32_e32 v14, v45, v14
	v_add_f32_e32 v20, 1.0, v20
	v_and_b32_e32 v11, 0xffff0000, v11
	v_and_b32_e32 v15, 0xffff0000, v15
	v_mul_f32_e32 v15, v44, v15
	v_rcp_f32_e32 v21, v20
	s_nop 0
	v_mul_f32_e32 v19, v19, v21
	v_mul_f32_e32 v14, v19, v14
	v_mul_f32_e32 v19, 0xbfb8aa3b, v11
	v_exp_f32_e32 v19, v19
	v_med3_f32 v14, v14, s9, v214
	v_add_f32_e32 v19, 1.0, v19
	s_nop 0
	v_rcp_f32_e32 v20, v19
	s_nop 0
	v_mul_f32_e32 v11, v11, v20
	v_mul_f32_e32 v11, v11, v15
	v_med3_f32 v15, v18, s9, v214
	v_med3_f32 v18, v10, s9, v214
	v_mov_b32_e32 v10, v125
	v_cvt_pk_fp8_f32 v10, v15, v18
	v_med3_f32 v11, v11, s9, v214
	v_cvt_pk_fp8_f32 v10, v14, v11 op_sel:[0,0,1]
	v_lshlrev_b32_e32 v14, 16, v12
	v_mul_f32_e32 v15, 0xbfb8aa3b, v14
	v_exp_f32_e32 v15, v15
	v_and_b32_e32 v12, 0xffff0000, v12
	v_lshlrev_b32_e32 v11, 16, v16
	v_mul_f32_e32 v11, v43, v11
	v_add_f32_e32 v15, 1.0, v15
	s_nop 0
	v_rcp_f32_e32 v18, v15
	s_nop 0
	v_mul_f32_e32 v14, v14, v18
	v_mul_f32_e32 v15, 0xbfb8aa3b, v12
	v_exp_f32_e32 v15, v15
	v_mul_f32_e32 v11, v14, v11
	v_and_b32_e32 v14, 0xffff0000, v16
	v_mul_f32_e32 v14, v42, v14
	v_add_f32_e32 v15, 1.0, v15
	s_nop 0
	v_rcp_f32_e32 v16, v15
	s_nop 0
	v_mul_f32_e32 v12, v12, v16
	v_lshlrev_b32_e32 v15, 16, v13
	v_mul_f32_e32 v16, 0xbfb8aa3b, v15
	v_exp_f32_e32 v16, v16
	v_and_b32_e32 v13, 0xffff0000, v13
	v_mul_f32_e32 v12, v12, v14
	v_lshlrev_b32_e32 v14, 16, v17
	v_add_f32_e32 v16, 1.0, v16
	v_mul_f32_e32 v14, v41, v14
	v_med3_f32 v12, v12, s9, v214
	v_rcp_f32_e32 v18, v16
	s_nop 0
	v_mul_f32_e32 v15, v15, v18
	v_mul_f32_e32 v16, 0xbfb8aa3b, v13
	v_exp_f32_e32 v16, v16
	v_mul_f32_e32 v14, v15, v14
	v_and_b32_e32 v15, 0xffff0000, v17
	v_mul_f32_e32 v15, v40, v15
	v_add_f32_e32 v16, 1.0, v16
	v_med3_f32 v14, v14, s9, v214
	v_rcp_f32_e32 v17, v16
	s_nop 0
	v_mul_f32_e32 v13, v13, v17
	v_mul_f32_e32 v13, v13, v15
	v_med3_f32 v15, v11, s9, v214
	v_mov_b32_e32 v11, v125
	v_cvt_pk_fp8_f32 v11, v15, v12
	s_waitcnt vmcnt(6)
	v_lshlrev_b32_e32 v15, 16, v6
	v_mul_f32_e32 v16, 0xbfb8aa3b, v15
	v_exp_f32_e32 v16, v16
	v_med3_f32 v13, v13, s9, v214
	v_cvt_pk_fp8_f32 v11, v14, v13 op_sel:[0,0,1]
	v_lshlrev_b64 v[12:13], 11, v[124:125]
	v_add_f32_e32 v16, 1.0, v16
	v_lshl_add_u64 v[12:13], s[86:87], 0, v[12:13]
	v_lshl_add_u64 v[12:13], v[12:13], 0, s[84:85]
	v_lshl_add_u64 v[12:13], v[12:13], 0, v[136:137]
	global_store_dwordx2 v[12:13], v[10:11], off
	ds_read_b128 v[10:13], v209 offset:51712
	s_waitcnt lgkmcnt(0)
	v_lshlrev_b32_e32 v14, 16, v10
	v_mul_f32_e32 v14, v47, v14
	v_rcp_f32_e32 v17, v16
	s_nop 0
	v_mul_f32_e32 v15, v15, v17
	v_and_b32_e32 v6, 0xffff0000, v6
	v_mul_f32_e32 v14, v15, v14
	v_mul_f32_e32 v15, 0xbfb8aa3b, v6
	v_exp_f32_e32 v15, v15
	v_and_b32_e32 v10, 0xffff0000, v10
	v_mul_f32_e32 v10, v46, v10
	v_or_b32_e32 v124, s11, v195
	v_add_f32_e32 v15, 1.0, v15
	s_nop 0
	v_rcp_f32_e32 v16, v15
	s_nop 0
	v_mul_f32_e32 v6, v6, v16
	v_lshlrev_b32_e32 v15, 16, v7
	v_mul_f32_e32 v16, 0xbfb8aa3b, v15
	v_exp_f32_e32 v16, v16
	v_mul_f32_e32 v6, v6, v10
	v_lshlrev_b32_e32 v10, 16, v11
	v_mul_f32_e32 v10, v45, v10
	v_add_f32_e32 v16, 1.0, v16
	v_and_b32_e32 v7, 0xffff0000, v7
	v_and_b32_e32 v11, 0xffff0000, v11
	v_mul_f32_e32 v11, v44, v11
	v_rcp_f32_e32 v17, v16
	s_nop 0
	v_mul_f32_e32 v15, v15, v17
	v_mul_f32_e32 v10, v15, v10
	v_mul_f32_e32 v15, 0xbfb8aa3b, v7
	v_exp_f32_e32 v15, v15
	v_med3_f32 v10, v10, s9, v214
	v_add_f32_e32 v15, 1.0, v15
	s_nop 0
	v_rcp_f32_e32 v16, v15
	s_nop 0
	v_mul_f32_e32 v7, v7, v16
	v_mul_f32_e32 v7, v7, v11
	v_med3_f32 v11, v14, s9, v214
	v_med3_f32 v14, v6, s9, v214
	v_mov_b32_e32 v6, v125
	v_cvt_pk_fp8_f32 v6, v11, v14
	v_med3_f32 v7, v7, s9, v214
	v_cvt_pk_fp8_f32 v6, v10, v7 op_sel:[0,0,1]
	v_lshlrev_b32_e32 v10, 16, v8
	v_mul_f32_e32 v11, 0xbfb8aa3b, v10
	v_exp_f32_e32 v11, v11
	v_and_b32_e32 v8, 0xffff0000, v8
	v_lshlrev_b32_e32 v7, 16, v12
	v_mul_f32_e32 v7, v43, v7
	v_add_f32_e32 v11, 1.0, v11
	s_nop 0
	v_rcp_f32_e32 v14, v11
	s_nop 0
	v_mul_f32_e32 v10, v10, v14
	v_mul_f32_e32 v11, 0xbfb8aa3b, v8
	v_exp_f32_e32 v11, v11
	v_mul_f32_e32 v7, v10, v7
	v_and_b32_e32 v10, 0xffff0000, v12
	v_mul_f32_e32 v10, v42, v10
	v_add_f32_e32 v11, 1.0, v11
	s_nop 0
	v_rcp_f32_e32 v12, v11
	s_nop 0
	v_mul_f32_e32 v8, v8, v12
	v_lshlrev_b32_e32 v11, 16, v9
	v_mul_f32_e32 v12, 0xbfb8aa3b, v11
	v_exp_f32_e32 v12, v12
	v_and_b32_e32 v9, 0xffff0000, v9
	v_mul_f32_e32 v8, v8, v10
	v_lshlrev_b32_e32 v10, 16, v13
	v_add_f32_e32 v12, 1.0, v12
	v_mul_f32_e32 v10, v41, v10
	v_med3_f32 v8, v8, s9, v214
	v_rcp_f32_e32 v14, v12
	s_nop 0
	v_mul_f32_e32 v11, v11, v14
	v_mul_f32_e32 v12, 0xbfb8aa3b, v9
	v_exp_f32_e32 v12, v12
	v_mul_f32_e32 v10, v11, v10
	v_and_b32_e32 v11, 0xffff0000, v13
	v_mul_f32_e32 v11, v40, v11
	v_add_f32_e32 v12, 1.0, v12
	v_med3_f32 v10, v10, s9, v214
	v_rcp_f32_e32 v13, v12
	s_nop 0
	v_mul_f32_e32 v9, v9, v13
	v_mul_f32_e32 v9, v9, v11
	v_med3_f32 v11, v7, s9, v214
	v_mov_b32_e32 v7, v125
	v_cvt_pk_fp8_f32 v7, v11, v8
	s_waitcnt vmcnt(6)
	v_lshlrev_b32_e32 v11, 16, v2
	v_mul_f32_e32 v12, 0xbfb8aa3b, v11
	v_exp_f32_e32 v12, v12
	v_med3_f32 v9, v9, s9, v214
	v_cvt_pk_fp8_f32 v7, v10, v9 op_sel:[0,0,1]
	v_lshlrev_b64 v[8:9], 11, v[124:125]
	v_add_f32_e32 v12, 1.0, v12
	v_lshl_add_u64 v[8:9], s[86:87], 0, v[8:9]
	v_lshl_add_u64 v[8:9], v[8:9], 0, s[84:85]
	v_lshl_add_u64 v[8:9], v[8:9], 0, v[136:137]
	global_store_dwordx2 v[8:9], v[6:7], off
	ds_read_b128 v[6:9], v209 offset:60160
	s_waitcnt lgkmcnt(0)
	v_lshlrev_b32_e32 v10, 16, v6
	v_mul_f32_e32 v10, v47, v10
	v_rcp_f32_e32 v13, v12
	s_nop 0
	v_mul_f32_e32 v11, v11, v13
	v_and_b32_e32 v2, 0xffff0000, v2
	v_mul_f32_e32 v10, v11, v10
	v_mul_f32_e32 v11, 0xbfb8aa3b, v2
	v_exp_f32_e32 v11, v11
	v_and_b32_e32 v6, 0xffff0000, v6
	v_mul_f32_e32 v6, v46, v6
	v_add_u32_e32 v124, s11, v197
	v_add_f32_e32 v11, 1.0, v11
	s_nop 0
	v_rcp_f32_e32 v12, v11
	s_nop 0
	v_mul_f32_e32 v2, v2, v12
	v_lshlrev_b32_e32 v11, 16, v3
	v_mul_f32_e32 v12, 0xbfb8aa3b, v11
	v_exp_f32_e32 v12, v12
	v_mul_f32_e32 v2, v2, v6
	v_lshlrev_b32_e32 v6, 16, v7
	v_mul_f32_e32 v6, v45, v6
	v_add_f32_e32 v12, 1.0, v12
	v_and_b32_e32 v3, 0xffff0000, v3
	v_and_b32_e32 v7, 0xffff0000, v7
	v_mul_f32_e32 v7, v44, v7
	v_rcp_f32_e32 v13, v12
	s_nop 0
	v_mul_f32_e32 v11, v11, v13
	v_mul_f32_e32 v6, v11, v6
	v_mul_f32_e32 v11, 0xbfb8aa3b, v3
	v_exp_f32_e32 v11, v11
	v_med3_f32 v6, v6, s9, v214
	v_add_f32_e32 v11, 1.0, v11
	s_nop 0
	v_rcp_f32_e32 v12, v11
	s_nop 0
	v_mul_f32_e32 v3, v3, v12
	v_mul_f32_e32 v3, v3, v7
	v_med3_f32 v7, v10, s9, v214
	v_med3_f32 v10, v2, s9, v214
	v_mov_b32_e32 v2, v125
	v_cvt_pk_fp8_f32 v2, v7, v10
	v_med3_f32 v3, v3, s9, v214
	v_cvt_pk_fp8_f32 v2, v6, v3 op_sel:[0,0,1]
	v_lshlrev_b32_e32 v6, 16, v4
	v_mul_f32_e32 v7, 0xbfb8aa3b, v6
	v_exp_f32_e32 v7, v7
	v_and_b32_e32 v4, 0xffff0000, v4
	v_lshlrev_b32_e32 v3, 16, v8
	v_mul_f32_e32 v3, v43, v3
	v_add_f32_e32 v7, 1.0, v7
	s_nop 0
	v_rcp_f32_e32 v10, v7
	s_nop 0
	v_mul_f32_e32 v6, v6, v10
	v_mul_f32_e32 v7, 0xbfb8aa3b, v4
	v_exp_f32_e32 v7, v7
	v_mul_f32_e32 v3, v6, v3
	v_and_b32_e32 v6, 0xffff0000, v8
	v_mul_f32_e32 v6, v42, v6
	v_add_f32_e32 v7, 1.0, v7
	s_nop 0
	v_rcp_f32_e32 v8, v7
	s_nop 0
	v_mul_f32_e32 v4, v4, v8
	v_lshlrev_b32_e32 v7, 16, v5
	v_mul_f32_e32 v8, 0xbfb8aa3b, v7
	v_exp_f32_e32 v8, v8
	v_and_b32_e32 v5, 0xffff0000, v5
	v_mul_f32_e32 v4, v4, v6
	v_lshlrev_b32_e32 v6, 16, v9
	v_add_f32_e32 v8, 1.0, v8
	v_mul_f32_e32 v6, v41, v6
	v_med3_f32 v4, v4, s9, v214
	v_rcp_f32_e32 v10, v8
	s_nop 0
	v_mul_f32_e32 v7, v7, v10
	v_mul_f32_e32 v8, 0xbfb8aa3b, v5
	v_exp_f32_e32 v8, v8
	v_mul_f32_e32 v6, v7, v6
	v_and_b32_e32 v7, 0xffff0000, v9
	v_mul_f32_e32 v7, v40, v7
	v_add_f32_e32 v8, 1.0, v8
	v_med3_f32 v6, v6, s9, v214
	v_rcp_f32_e32 v9, v8
	s_nop 0
	v_mul_f32_e32 v5, v5, v9
	v_mul_f32_e32 v5, v5, v7
	v_med3_f32 v7, v3, s9, v214
	v_mov_b32_e32 v3, v125
	v_cvt_pk_fp8_f32 v3, v7, v4
	v_med3_f32 v5, v5, s9, v214
	v_cvt_pk_fp8_f32 v3, v6, v5 op_sel:[0,0,1]
	v_lshlrev_b64 v[4:5], 11, v[124:125]
	v_lshl_add_u64 v[4:5], s[86:87], 0, v[4:5]
	v_lshl_add_u64 v[4:5], v[4:5], 0, s[84:85]
	v_lshl_add_u64 v[4:5], v[4:5], 0, v[136:137]
	global_store_dwordx2 v[4:5], v[2:3], off
	s_barrier
	s_cbranch_scc0 .LBB0_956

.LBB0_954:
	s_or_b64 exec, exec, s[0:1]
	s_waitcnt lgkmcnt(0)
	s_barrier
	s_and_saveexec_b64 s[94:95], s[76:77]
	s_cbranch_execz .LBB0_937
	v_add_u32_e32 v82, 0, v131
	v_add_u32_e32 v78, 0x21800, v82
	ds_read2st64_b64 v[66:69], v78 offset1:2
	ds_read2st64_b64 v[70:73], v78 offset0:4 offset1:6
	ds_read2st64_b64 v[74:77], v78 offset0:8 offset1:10
	ds_read2st64_b64 v[78:81], v78 offset0:12 offset1:14
	s_mov_b32 s0, 0x3b800000
	s_waitcnt lgkmcnt(3)
	v_pk_add_f32 v[66:67], v[66:67], 0 op_sel_hi:[1,0]
	s_nop 0
	v_pk_add_f32 v[66:67], v[66:67], v[68:69]
	s_waitcnt lgkmcnt(2)
	v_pk_add_f32 v[66:67], v[66:67], v[70:71]
	s_nop 0
	v_pk_add_f32 v[66:67], v[66:67], v[72:73]
	s_waitcnt lgkmcnt(1)
	v_pk_add_f32 v[66:67], v[66:67], v[74:75]
	s_nop 0
	v_pk_add_f32 v[66:67], v[66:67], v[76:77]
	s_waitcnt lgkmcnt(0)
	v_pk_add_f32 v[66:67], v[66:67], v[78:79]
	s_nop 0
	v_pk_add_f32 v[66:67], v[66:67], v[80:81]
	s_nop 0
	v_pk_mul_f32 v[66:67], v[66:67], s[0:1] op_sel_hi:[1,0]
	s_mov_b32 s0, 0xf800000
	v_fma_f32 v67, -v66, v66, v67
	v_max_f32_e32 v67, 0, v67
	v_add_f32_e32 v67, 0x3727c5ac, v67
	v_mul_f32_e32 v68, 0x4f800000, v67
	v_cmp_gt_f32_e32 vcc, s0, v67
	s_nop 1
	v_cndmask_b32_e32 v67, v67, v68, vcc
	v_sqrt_f32_e32 v68, v67
	s_nop 0
	v_add_u32_e32 v69, -1, v68
	v_add_u32_e32 v70, 1, v68
	v_fma_f32 v71, -v69, v68, v67
	v_fma_f32 v72, -v70, v68, v67
	v_cmp_ge_f32_e64 s[0:1], 0, v71
	s_nop 1
	v_cndmask_b32_e64 v68, v68, v69, s[0:1]
	v_cmp_lt_f32_e64 s[0:1], 0, v72
	s_nop 1
	v_cndmask_b32_e64 v68, v68, v70, s[0:1]
	v_mul_f32_e32 v69, 0x37800000, v68
	v_cndmask_b32_e32 v68, v68, v69, vcc
	v_cmp_class_f32_e32 vcc, v67, v205
	s_nop 1
	v_cndmask_b32_e32 v67, v68, v67, vcc
	v_div_scale_f32 v68, s[0:1], v67, v67, 1.0
	v_rcp_f32_e32 v69, v68
	s_nop 0
	v_fma_f32 v70, -v68, v69, 1.0
	v_fmac_f32_e32 v69, v70, v69
	v_div_scale_f32 v70, vcc, 1.0, v67, 1.0
	v_mul_f32_e32 v71, v70, v69
	v_fma_f32 v72, -v68, v71, v70
	v_fmac_f32_e32 v71, v72, v69
	v_fma_f32 v68, -v68, v71, v70
	v_div_fmas_f32 v68, v68, v69, v71
	v_rcp_f32_e32 v67, v67
	v_add_u32_e32 v68, 0x23800, v82
	ds_write_b64 v68, v[66:67]
	s_branch .LBB0_937

.LBB0_982:
	v_lshl_or_b32 v2, s57, 8, v202
	v_add_u32_e32 v4, s56, v201
	v_ashrrev_i32_e32 v3, 31, v2
	v_mov_b64_e32 v[6:7], s[16:17]
	v_mad_i64_i32 v[10:11], s[2:3], v4, s47, v[6:7]
	v_lshlrev_b64 v[8:9], 1, v[2:3]
	v_mad_u32_u24 v213, v4, s47, v8
	global_load_dwordx4 v[214:217], v213, s[16:17]
	global_load_dwordx4 v[218:221], v213, s[16:17] offset:256
	v_add_u32_e32 v213, 16, v4
	v_mad_u32_u24 v213, v213, s47, v8
	global_load_dwordx4 v[222:225], v213, s[16:17]
	global_load_dwordx4 v[226:229], v213, s[16:17] offset:256
	v_add_u32_e32 v213, 32, v4
	v_mad_u32_u24 v213, v213, s47, v8
	global_load_dwordx4 v[230:233], v213, s[16:17]
	global_load_dwordx4 v[234:237], v213, s[16:17] offset:256
	v_add_u32_e32 v213, 48, v4
	v_mad_u32_u24 v213, v213, s47, v8
	global_load_dwordx4 v[238:241], v213, s[16:17]
	global_load_dwordx4 v[242:245], v213, s[16:17] offset:256
	v_add_u32_e32 v213, 128, v4
	v_mad_u32_u24 v213, v213, s47, v8
	global_load_dwordx4 v[246:249], v213, s[16:17]
	global_load_dwordx4 v[250:253], v213, s[16:17] offset:256
	s_nop 15
	s_nop 15
	s_nop 15
	v_lshl_add_u64 v[10:11], v[10:11], 0, v[8:9]
	v_pk_mul_f32 v[20:21], v[156:157], s[24:25] op_sel_hi:[1,0]
	v_pk_mul_f32 v[18:19], v[158:159], s[24:25] op_sel_hi:[1,0]
	v_pk_mul_f32 v[16:17], v[160:161], s[24:25] op_sel_hi:[1,0]
	v_pk_mul_f32 v[22:23], v[154:155], s[24:25] op_sel_hi:[1,0]
	v_ashrrev_i32_e32 v5, 31, v4
	s_waitcnt vmcnt(9)
	v_mov_b64_e32 v[12:13], v[214:215]
	v_mov_b64_e32 v[14:15], v[216:217]
	v_add_u32_e32 v213, 144, v4
	v_mad_u32_u24 v213, v213, s47, v8
	global_load_dwordx4 v[214:217], v213, s[16:17]
	v_lshlrev_b32_e32 v24, 16, v12
	v_and_b32_e32 v12, 0xffff0000, v12
	v_mul_f32_e32 v24, 0xbfb8aa3b, v24
	v_lshlrev_b32_e32 v25, 16, v13
	v_mul_f32_e32 v12, 0xbfb8aa3b, v12
	v_exp_f32_e32 v24, v24
	v_mul_f32_e32 v25, 0xbfb8aa3b, v25
	v_exp_f32_e32 v12, v12
	v_and_b32_e32 v13, 0xffff0000, v13
	v_exp_f32_e32 v25, v25
	v_mul_f32_e32 v13, 0xbfb8aa3b, v13
	v_exp_f32_e32 v13, v13
	v_add_f32_e32 v24, 1.0, v24
	v_lshlrev_b32_e32 v26, 16, v14
	v_add_f32_e32 v12, 1.0, v12
	v_mul_f32_e32 v26, 0xbfb8aa3b, v26
	v_add_f32_e32 v25, 1.0, v25
	v_exp_f32_e32 v26, v26
	v_add_f32_e32 v13, 1.0, v13
	v_add_f32_e32 v26, 1.0, v26
	v_and_b32_e32 v14, 0xffff0000, v14
	v_mul_f32_e32 v14, 0xbfb8aa3b, v14
	v_exp_f32_e32 v14, v14
	v_rcp_f32_e32 v24, v24
	s_nop 0
	v_mul_f32_e32 v18, v18, v24
	v_rcp_f32_e32 v12, v12
	s_nop 0
	v_mul_f32_e32 v12, v19, v12
	v_rcp_f32_e32 v19, v25
	v_add_f32_e32 v14, 1.0, v14
	v_mul_f32_e32 v16, v16, v19
	v_rcp_f32_e32 v13, v13
	s_nop 0
	v_mul_f32_e32 v13, v17, v13
	v_rcp_f32_e32 v17, v26
	v_lshlrev_b32_e32 v26, 16, v15
	v_mul_f32_e32 v17, v22, v17
	v_mul_f32_e32 v26, 0xbfb8aa3b, v26
	v_exp_f32_e32 v26, v26
	s_nop 0
	v_add_f32_e32 v22, 1.0, v26
	v_and_b32_e32 v15, 0xffff0000, v15
	v_mul_f32_e32 v15, 0xbfb8aa3b, v15
	v_rcp_f32_e32 v14, v14
	v_exp_f32_e32 v15, v15
	v_mul_f32_e32 v19, v23, v14
	v_add_f32_e32 v15, 1.0, v15
	v_rcp_f32_e32 v14, v22
	s_nop 0
	v_mul_f32_e32 v20, v20, v14
	v_rcp_f32_e32 v14, v15
	s_nop 0
	v_mul_f32_e32 v21, v21, v14
	v_mul_f32_e32 v14, 0x41800000, v18
	v_mul_f32_e32 v12, 0x41800000, v12
	v_mul_f32_e32 v15, 0x41800000, v16
	v_med3_f32 v16, v14, s53, v205
	v_med3_f32 v12, v12, s53, v205
	v_mov_b32_e32 v14, v167
	v_cvt_pk_fp8_f32 v14, v16, v12
	v_mul_f32_e32 v12, 0x41800000, v13
	v_med3_f32 v13, v15, s53, v205
	v_med3_f32 v12, v12, s53, v205
	v_cvt_pk_fp8_f32 v14, v13, v12 op_sel:[0,0,1]
	v_mul_f32_e32 v12, 0x41800000, v17
	v_mul_f32_e32 v13, 0x41800000, v19
	v_med3_f32 v12, v12, s53, v205
	v_med3_f32 v13, v13, s53, v205
	v_mov_b32_e32 v15, v167
	v_cvt_pk_fp8_f32 v15, v12, v13
	v_mul_f32_e32 v16, 0x41800000, v20
	v_mul_f32_e32 v12, 0x41800000, v21
	v_med3_f32 v13, v16, s53, v205
	v_med3_f32 v12, v12, s53, v205
	v_cvt_pk_fp8_f32 v15, v13, v12 op_sel:[0,0,1]
	v_lshlrev_b64 v[12:13], 11, v[4:5]
	v_lshl_add_u64 v[12:13], s[14:15], 0, v[12:13]
	v_lshl_add_u64 v[12:13], v[12:13], 0, v[2:3]
	global_store_dwordx2 v[12:13], v[14:15], off
	v_pk_mul_f32 v[18:19], v[150:151], s[24:25] op_sel_hi:[1,0]
	v_pk_mul_f32 v[10:11], v[152:153], s[24:25] op_sel_hi:[1,0]
	v_pk_mul_f32 v[22:23], v[146:147], s[24:25] op_sel_hi:[1,0]
	v_pk_mul_f32 v[20:21], v[148:149], s[24:25] op_sel_hi:[1,0]
	s_waitcnt vmcnt(9)
	v_mov_b64_e32 v[14:15], v[218:219]
	v_mov_b64_e32 v[16:17], v[220:221]
	v_add_u32_e32 v213, 144, v4
	v_mad_u32_u24 v213, v213, s47, v8
	global_load_dwordx4 v[218:221], v213, s[16:17] offset:256
	v_lshlrev_b32_e32 v5, 16, v14
	v_mul_f32_e32 v5, 0xbfb8aa3b, v5
	v_exp_f32_e32 v5, v5
	v_and_b32_e32 v14, 0xffff0000, v14
	v_mul_f32_e32 v14, 0xbfb8aa3b, v14
	v_exp_f32_e32 v14, v14
	v_add_f32_e32 v5, 1.0, v5
	v_add_f32_e32 v14, 1.0, v14
	v_lshlrev_b32_e32 v25, 16, v15
	v_rcp_f32_e32 v5, v5
	v_mul_f32_e32 v25, 0xbfb8aa3b, v25
	v_mul_f32_e32 v5, v18, v5
	v_exp_f32_e32 v25, v25
	s_nop 0
	v_add_f32_e32 v25, 1.0, v25
	v_and_b32_e32 v15, 0xffff0000, v15
	v_mul_f32_e32 v15, 0xbfb8aa3b, v15
	v_exp_f32_e32 v15, v15
	v_rcp_f32_e32 v14, v14
	s_nop 0
	v_mul_f32_e32 v14, v19, v14
	v_add_f32_e32 v15, 1.0, v15
	v_rcp_f32_e32 v18, v25
	v_lshlrev_b32_e32 v25, 16, v16
	v_mul_f32_e32 v10, v10, v18
	v_mul_f32_e32 v25, 0xbfb8aa3b, v25
	v_exp_f32_e32 v25, v25
	s_nop 0
	v_add_f32_e32 v24, 1.0, v25
	v_and_b32_e32 v16, 0xffff0000, v16
	v_mul_f32_e32 v16, 0xbfb8aa3b, v16
	v_rcp_f32_e32 v15, v15
	v_exp_f32_e32 v16, v16
	v_mul_f32_e32 v11, v11, v15
	v_add_f32_e32 v16, 1.0, v16
	v_rcp_f32_e32 v15, v24
	v_lshlrev_b32_e32 v24, 16, v17
	v_mul_f32_e32 v24, 0xbfb8aa3b, v24
	v_exp_f32_e32 v24, v24
	v_mul_f32_e32 v15, v22, v15
	v_add_f32_e32 v19, 1.0, v24
	v_and_b32_e32 v17, 0xffff0000, v17
	v_mul_f32_e32 v17, 0xbfb8aa3b, v17
	v_exp_f32_e32 v17, v17
	v_rcp_f32_e32 v16, v16
	s_nop 0
	v_mul_f32_e32 v16, v23, v16
	v_add_f32_e32 v17, 1.0, v17
	v_rcp_f32_e32 v18, v19
	s_nop 0
	v_mul_f32_e32 v18, v20, v18
	v_mul_f32_e32 v5, 0x41800000, v5
	v_mul_f32_e32 v14, 0x41800000, v14
	v_rcp_f32_e32 v17, v17
	v_mul_f32_e32 v19, 0x41800000, v10
	v_med3_f32 v5, v5, s53, v205
	v_med3_f32 v14, v14, s53, v205
	v_mov_b32_e32 v10, v167
	v_cvt_pk_fp8_f32 v10, v5, v14
	v_mul_f32_e32 v5, 0x41800000, v11
	v_med3_f32 v11, v19, s53, v205
	v_med3_f32 v5, v5, s53, v205
	v_cvt_pk_fp8_f32 v10, v11, v5 op_sel:[0,0,1]
	v_mul_f32_e32 v5, 0x41800000, v15
	v_mul_f32_e32 v11, 0x41800000, v16
	v_med3_f32 v5, v5, s53, v205
	v_med3_f32 v15, v11, s53, v205
	v_mov_b32_e32 v11, v167
	v_cvt_pk_fp8_f32 v11, v5, v15
	v_mul_f32_e32 v17, v21, v17
	v_mul_f32_e32 v14, 0x41800000, v18
	v_mul_f32_e32 v5, 0x41800000, v17
	v_med3_f32 v14, v14, s53, v205
	v_med3_f32 v5, v5, s53, v205
	v_cvt_pk_fp8_f32 v11, v14, v5 op_sel:[0,0,1]
	v_add_u32_e32 v16, 16, v4
	v_pk_mul_f32 v[20:21], v[142:143], s[24:25] op_sel_hi:[1,0]
	v_pk_mul_f32 v[18:19], v[144:145], s[24:25] op_sel_hi:[1,0]
	global_store_dwordx2 v[12:13], v[10:11], off offset:128
	v_mad_i64_i32 v[10:11], s[2:3], v16, s47, v[6:7]
	v_lshl_add_u64 v[10:11], v[10:11], 0, v[8:9]
	v_pk_mul_f32 v[24:25], v[138:139], s[24:25] op_sel_hi:[1,0]
	v_pk_mul_f32 v[22:23], v[140:141], s[24:25] op_sel_hi:[1,0]
	v_ashrrev_i32_e32 v17, 31, v16
	s_waitcnt vmcnt(9)
	v_mov_b64_e32 v[12:13], v[222:223]
	v_mov_b64_e32 v[14:15], v[224:225]
	v_add_u32_e32 v213, 160, v4
	v_mad_u32_u24 v213, v213, s47, v8
	global_load_dwordx4 v[222:225], v213, s[16:17]
	v_lshlrev_b32_e32 v5, 16, v12
	v_mul_f32_e32 v5, 0xbfb8aa3b, v5
	v_exp_f32_e32 v5, v5
	v_and_b32_e32 v12, 0xffff0000, v12
	v_mul_f32_e32 v12, 0xbfb8aa3b, v12
	v_exp_f32_e32 v12, v12
	v_add_f32_e32 v5, 1.0, v5
	v_add_f32_e32 v12, 1.0, v12
	v_lshlrev_b32_e32 v27, 16, v13
	v_rcp_f32_e32 v5, v5
	v_mul_f32_e32 v27, 0xbfb8aa3b, v27
	v_mul_f32_e32 v5, v20, v5
	v_exp_f32_e32 v27, v27
	s_nop 0
	v_add_f32_e32 v27, 1.0, v27
	v_and_b32_e32 v13, 0xffff0000, v13
	v_mul_f32_e32 v13, 0xbfb8aa3b, v13
	v_exp_f32_e32 v13, v13
	v_rcp_f32_e32 v12, v12
	s_nop 0
	v_mul_f32_e32 v12, v21, v12
	v_add_f32_e32 v13, 1.0, v13
	v_rcp_f32_e32 v20, v27
	v_lshlrev_b32_e32 v27, 16, v14
	v_mul_f32_e32 v18, v18, v20
	v_mul_f32_e32 v27, 0xbfb8aa3b, v27
	v_exp_f32_e32 v27, v27
	s_nop 0
	v_add_f32_e32 v26, 1.0, v27
	v_and_b32_e32 v14, 0xffff0000, v14
	v_mul_f32_e32 v14, 0xbfb8aa3b, v14
	v_rcp_f32_e32 v13, v13
	v_exp_f32_e32 v14, v14
	v_mul_f32_e32 v13, v19, v13
	v_add_f32_e32 v14, 1.0, v14
	v_rcp_f32_e32 v19, v26
	v_lshlrev_b32_e32 v26, 16, v15
	v_mul_f32_e32 v26, 0xbfb8aa3b, v26
	v_exp_f32_e32 v26, v26
	v_mul_f32_e32 v19, v24, v19
	v_add_f32_e32 v21, 1.0, v26
	v_and_b32_e32 v15, 0xffff0000, v15
	v_mul_f32_e32 v15, 0xbfb8aa3b, v15
	v_exp_f32_e32 v15, v15
	v_rcp_f32_e32 v14, v14
	s_nop 0
	v_mul_f32_e32 v14, v25, v14
	v_add_f32_e32 v15, 1.0, v15
	v_rcp_f32_e32 v20, v21
	s_nop 0
	v_mul_f32_e32 v20, v22, v20
	v_mul_f32_e32 v5, 0x41800000, v5
	v_mul_f32_e32 v12, 0x41800000, v12
	v_rcp_f32_e32 v15, v15
	v_med3_f32 v5, v5, s53, v205
	v_med3_f32 v21, v12, s53, v205
	v_mov_b32_e32 v12, v167
	v_cvt_pk_fp8_f32 v12, v5, v21
	v_mul_f32_e32 v18, 0x41800000, v18
	v_mul_f32_e32 v5, 0x41800000, v13
	v_med3_f32 v13, v18, s53, v205
	v_med3_f32 v5, v5, s53, v205
	v_cvt_pk_fp8_f32 v12, v13, v5 op_sel:[0,0,1]
	v_mul_f32_e32 v5, 0x41800000, v19
	v_mul_f32_e32 v13, 0x41800000, v14
	v_med3_f32 v5, v5, s53, v205
	v_med3_f32 v18, v13, s53, v205
	v_mov_b32_e32 v13, v167
	v_cvt_pk_fp8_f32 v13, v5, v18
	v_mul_f32_e32 v15, v23, v15
	v_mul_f32_e32 v14, 0x41800000, v20
	v_mul_f32_e32 v5, 0x41800000, v15
	v_med3_f32 v14, v14, s53, v205
	v_med3_f32 v5, v5, s53, v205
	v_cvt_pk_fp8_f32 v13, v14, v5 op_sel:[0,0,1]
	v_lshlrev_b64 v[14:15], 11, v[16:17]
	v_lshl_add_u64 v[14:15], s[14:15], 0, v[14:15]
	v_lshl_add_u64 v[14:15], v[14:15], 0, v[2:3]
	global_store_dwordx2 v[14:15], v[12:13], off
	v_pk_mul_f32 v[18:19], v[134:135], s[24:25] op_sel_hi:[1,0]
	v_pk_mul_f32 v[16:17], v[136:137], s[24:25] op_sel_hi:[1,0]
	v_pk_mul_f32 v[22:23], v[130:131], s[24:25] op_sel_hi:[1,0]
	v_pk_mul_f32 v[20:21], v[132:133], s[24:25] op_sel_hi:[1,0]
	s_waitcnt vmcnt(9)
	v_mov_b64_e32 v[10:11], v[226:227]
	v_mov_b64_e32 v[12:13], v[228:229]
	v_add_u32_e32 v213, 160, v4
	v_mad_u32_u24 v213, v213, s47, v8
	global_load_dwordx4 v[226:229], v213, s[16:17] offset:256
	v_lshlrev_b32_e32 v5, 16, v10
	v_mul_f32_e32 v5, 0xbfb8aa3b, v5
	v_exp_f32_e32 v5, v5
	v_and_b32_e32 v10, 0xffff0000, v10
	v_mul_f32_e32 v10, 0xbfb8aa3b, v10
	v_exp_f32_e32 v10, v10
	v_add_f32_e32 v5, 1.0, v5
	v_add_f32_e32 v10, 1.0, v10
	v_lshlrev_b32_e32 v25, 16, v11
	v_rcp_f32_e32 v5, v5
	v_mul_f32_e32 v25, 0xbfb8aa3b, v25
	v_mul_f32_e32 v5, v18, v5
	v_exp_f32_e32 v25, v25
	s_nop 0
	v_add_f32_e32 v25, 1.0, v25
	v_and_b32_e32 v11, 0xffff0000, v11
	v_mul_f32_e32 v11, 0xbfb8aa3b, v11
	v_exp_f32_e32 v11, v11
	v_rcp_f32_e32 v10, v10
	s_nop 0
	v_mul_f32_e32 v10, v19, v10
	v_add_f32_e32 v11, 1.0, v11
	v_rcp_f32_e32 v18, v25
	v_lshlrev_b32_e32 v25, 16, v12
	v_mul_f32_e32 v16, v16, v18
	v_mul_f32_e32 v25, 0xbfb8aa3b, v25
	v_exp_f32_e32 v25, v25
	s_nop 0
	v_add_f32_e32 v24, 1.0, v25
	v_and_b32_e32 v12, 0xffff0000, v12
	v_mul_f32_e32 v12, 0xbfb8aa3b, v12
	v_rcp_f32_e32 v11, v11
	v_exp_f32_e32 v12, v12
	v_mul_f32_e32 v11, v17, v11
	v_add_f32_e32 v12, 1.0, v12
	v_rcp_f32_e32 v17, v24
	v_lshlrev_b32_e32 v24, 16, v13
	v_mul_f32_e32 v24, 0xbfb8aa3b, v24
	v_exp_f32_e32 v24, v24
	v_mul_f32_e32 v17, v22, v17
	v_add_f32_e32 v19, 1.0, v24
	v_and_b32_e32 v13, 0xffff0000, v13
	v_mul_f32_e32 v13, 0xbfb8aa3b, v13
	v_exp_f32_e32 v13, v13
	v_rcp_f32_e32 v12, v12
	s_nop 0
	v_mul_f32_e32 v12, v23, v12
	v_add_f32_e32 v13, 1.0, v13
	v_rcp_f32_e32 v18, v19
	s_nop 0
	v_mul_f32_e32 v18, v20, v18
	v_mul_f32_e32 v5, 0x41800000, v5
	v_mul_f32_e32 v10, 0x41800000, v10
	v_rcp_f32_e32 v13, v13
	v_med3_f32 v5, v5, s53, v205
	v_med3_f32 v19, v10, s53, v205
	v_mov_b32_e32 v10, v167
	v_cvt_pk_fp8_f32 v10, v5, v19
	v_mul_f32_e32 v16, 0x41800000, v16
	v_mul_f32_e32 v5, 0x41800000, v11
	v_med3_f32 v11, v16, s53, v205
	v_med3_f32 v5, v5, s53, v205
	v_cvt_pk_fp8_f32 v10, v11, v5 op_sel:[0,0,1]
	v_mul_f32_e32 v5, 0x41800000, v17
	v_mul_f32_e32 v11, 0x41800000, v12
	v_med3_f32 v5, v5, s53, v205
	v_med3_f32 v16, v11, s53, v205
	v_mov_b32_e32 v11, v167
	v_cvt_pk_fp8_f32 v11, v5, v16
	v_mul_f32_e32 v13, v21, v13
	v_mul_f32_e32 v12, 0x41800000, v18
	v_mul_f32_e32 v5, 0x41800000, v13
	v_med3_f32 v12, v12, s53, v205
	v_med3_f32 v5, v5, s53, v205
	v_cvt_pk_fp8_f32 v11, v12, v5 op_sel:[0,0,1]
	v_add_u32_e32 v16, 32, v4
	v_pk_mul_f32 v[20:21], v[126:127], s[24:25] op_sel_hi:[1,0]
	v_pk_mul_f32 v[18:19], v[128:129], s[24:25] op_sel_hi:[1,0]
	global_store_dwordx2 v[14:15], v[10:11], off offset:128
	v_mad_i64_i32 v[10:11], s[2:3], v16, s47, v[6:7]
	v_lshl_add_u64 v[10:11], v[10:11], 0, v[8:9]
	v_pk_mul_f32 v[24:25], v[122:123], s[24:25] op_sel_hi:[1,0]
	v_pk_mul_f32 v[22:23], v[124:125], s[24:25] op_sel_hi:[1,0]
	v_ashrrev_i32_e32 v17, 31, v16
	s_waitcnt vmcnt(9)
	v_mov_b64_e32 v[12:13], v[230:231]
	v_mov_b64_e32 v[14:15], v[232:233]
	v_add_u32_e32 v213, 176, v4
	v_mad_u32_u24 v213, v213, s47, v8
	global_load_dwordx4 v[230:233], v213, s[16:17]
	v_lshlrev_b32_e32 v5, 16, v12
	v_mul_f32_e32 v5, 0xbfb8aa3b, v5
	v_exp_f32_e32 v5, v5
	v_and_b32_e32 v12, 0xffff0000, v12
	v_mul_f32_e32 v12, 0xbfb8aa3b, v12
	v_exp_f32_e32 v12, v12
	v_add_f32_e32 v5, 1.0, v5
	v_add_f32_e32 v12, 1.0, v12
	v_lshlrev_b32_e32 v27, 16, v13
	v_rcp_f32_e32 v5, v5
	v_mul_f32_e32 v27, 0xbfb8aa3b, v27
	v_mul_f32_e32 v5, v20, v5
	v_exp_f32_e32 v27, v27
	s_nop 0
	v_add_f32_e32 v27, 1.0, v27
	v_and_b32_e32 v13, 0xffff0000, v13
	v_mul_f32_e32 v13, 0xbfb8aa3b, v13
	v_exp_f32_e32 v13, v13
	v_rcp_f32_e32 v12, v12
	s_nop 0
	v_mul_f32_e32 v12, v21, v12
	v_add_f32_e32 v13, 1.0, v13
	v_rcp_f32_e32 v20, v27
	v_lshlrev_b32_e32 v27, 16, v14
	v_mul_f32_e32 v18, v18, v20
	v_mul_f32_e32 v27, 0xbfb8aa3b, v27
	v_exp_f32_e32 v27, v27
	s_nop 0
	v_add_f32_e32 v26, 1.0, v27
	v_and_b32_e32 v14, 0xffff0000, v14
	v_mul_f32_e32 v14, 0xbfb8aa3b, v14
	v_rcp_f32_e32 v13, v13
	v_exp_f32_e32 v14, v14
	v_mul_f32_e32 v13, v19, v13
	v_add_f32_e32 v14, 1.0, v14
	v_rcp_f32_e32 v19, v26
	v_lshlrev_b32_e32 v26, 16, v15
	v_mul_f32_e32 v26, 0xbfb8aa3b, v26
	v_exp_f32_e32 v26, v26
	v_mul_f32_e32 v19, v24, v19
	v_add_f32_e32 v21, 1.0, v26
	v_and_b32_e32 v15, 0xffff0000, v15
	v_mul_f32_e32 v15, 0xbfb8aa3b, v15
	v_exp_f32_e32 v15, v15
	v_rcp_f32_e32 v14, v14
	s_nop 0
	v_mul_f32_e32 v14, v25, v14
	v_add_f32_e32 v15, 1.0, v15
	v_rcp_f32_e32 v20, v21
	s_nop 0
	v_mul_f32_e32 v20, v22, v20
	v_mul_f32_e32 v5, 0x41800000, v5
	v_mul_f32_e32 v12, 0x41800000, v12
	v_rcp_f32_e32 v15, v15
	v_med3_f32 v5, v5, s53, v205
	v_med3_f32 v21, v12, s53, v205
	v_mov_b32_e32 v12, v167
	v_cvt_pk_fp8_f32 v12, v5, v21
	v_mul_f32_e32 v18, 0x41800000, v18
	v_mul_f32_e32 v5, 0x41800000, v13
	v_med3_f32 v13, v18, s53, v205
	v_med3_f32 v5, v5, s53, v205
	v_cvt_pk_fp8_f32 v12, v13, v5 op_sel:[0,0,1]
	v_mul_f32_e32 v5, 0x41800000, v19
	v_mul_f32_e32 v13, 0x41800000, v14
	v_med3_f32 v5, v5, s53, v205
	v_med3_f32 v18, v13, s53, v205
	v_mov_b32_e32 v13, v167
	v_cvt_pk_fp8_f32 v13, v5, v18
	v_mul_f32_e32 v15, v23, v15
	v_mul_f32_e32 v14, 0x41800000, v20
	v_mul_f32_e32 v5, 0x41800000, v15
	v_med3_f32 v14, v14, s53, v205
	v_med3_f32 v5, v5, s53, v205
	v_cvt_pk_fp8_f32 v13, v14, v5 op_sel:[0,0,1]
	v_lshlrev_b64 v[14:15], 11, v[16:17]
	v_lshl_add_u64 v[14:15], s[14:15], 0, v[14:15]
	v_lshl_add_u64 v[14:15], v[14:15], 0, v[2:3]
	global_store_dwordx2 v[14:15], v[12:13], off
	v_pk_mul_f32 v[18:19], v[118:119], s[24:25] op_sel_hi:[1,0]
	v_pk_mul_f32 v[16:17], v[120:121], s[24:25] op_sel_hi:[1,0]
	v_pk_mul_f32 v[22:23], v[114:115], s[24:25] op_sel_hi:[1,0]
	v_pk_mul_f32 v[20:21], v[116:117], s[24:25] op_sel_hi:[1,0]
	s_waitcnt vmcnt(9)
	v_mov_b64_e32 v[10:11], v[234:235]
	v_mov_b64_e32 v[12:13], v[236:237]
	v_add_u32_e32 v213, 176, v4
	v_mad_u32_u24 v213, v213, s47, v8
	global_load_dwordx4 v[234:237], v213, s[16:17] offset:256
	v_lshlrev_b32_e32 v5, 16, v10
	v_mul_f32_e32 v5, 0xbfb8aa3b, v5
	v_exp_f32_e32 v5, v5
	v_and_b32_e32 v10, 0xffff0000, v10
	v_mul_f32_e32 v10, 0xbfb8aa3b, v10
	v_exp_f32_e32 v10, v10
	v_add_f32_e32 v5, 1.0, v5
	v_add_f32_e32 v10, 1.0, v10
	v_lshlrev_b32_e32 v25, 16, v11
	v_rcp_f32_e32 v5, v5
	v_mul_f32_e32 v25, 0xbfb8aa3b, v25
	v_mul_f32_e32 v5, v18, v5
	v_exp_f32_e32 v25, v25
	s_nop 0
	v_add_f32_e32 v25, 1.0, v25
	v_and_b32_e32 v11, 0xffff0000, v11
	v_mul_f32_e32 v11, 0xbfb8aa3b, v11
	v_exp_f32_e32 v11, v11
	v_rcp_f32_e32 v10, v10
	s_nop 0
	v_mul_f32_e32 v10, v19, v10
	v_add_f32_e32 v11, 1.0, v11
	v_rcp_f32_e32 v18, v25
	v_lshlrev_b32_e32 v25, 16, v12
	v_mul_f32_e32 v16, v16, v18
	v_mul_f32_e32 v25, 0xbfb8aa3b, v25
	v_exp_f32_e32 v25, v25
	s_nop 0
	v_add_f32_e32 v24, 1.0, v25
	v_and_b32_e32 v12, 0xffff0000, v12
	v_mul_f32_e32 v12, 0xbfb8aa3b, v12
	v_rcp_f32_e32 v11, v11
	v_exp_f32_e32 v12, v12
	v_mul_f32_e32 v11, v17, v11
	v_add_f32_e32 v12, 1.0, v12
	v_rcp_f32_e32 v17, v24
	v_lshlrev_b32_e32 v24, 16, v13
	v_mul_f32_e32 v24, 0xbfb8aa3b, v24
	v_exp_f32_e32 v24, v24
	v_mul_f32_e32 v17, v22, v17
	v_add_f32_e32 v19, 1.0, v24
	v_and_b32_e32 v13, 0xffff0000, v13
	v_mul_f32_e32 v13, 0xbfb8aa3b, v13
	v_exp_f32_e32 v13, v13
	v_rcp_f32_e32 v12, v12
	s_nop 0
	v_mul_f32_e32 v12, v23, v12
	v_add_f32_e32 v13, 1.0, v13
	v_rcp_f32_e32 v18, v19
	s_nop 0
	v_mul_f32_e32 v18, v20, v18
	v_mul_f32_e32 v5, 0x41800000, v5
	v_mul_f32_e32 v10, 0x41800000, v10
	v_rcp_f32_e32 v13, v13
	v_med3_f32 v5, v5, s53, v205
	v_med3_f32 v19, v10, s53, v205
	v_mov_b32_e32 v10, v167
	v_cvt_pk_fp8_f32 v10, v5, v19
	v_mul_f32_e32 v16, 0x41800000, v16
	v_mul_f32_e32 v5, 0x41800000, v11
	v_med3_f32 v11, v16, s53, v205
	v_med3_f32 v5, v5, s53, v205
	v_cvt_pk_fp8_f32 v10, v11, v5 op_sel:[0,0,1]
	v_mul_f32_e32 v5, 0x41800000, v17
	v_mul_f32_e32 v11, 0x41800000, v12
	v_med3_f32 v5, v5, s53, v205
	v_med3_f32 v16, v11, s53, v205
	v_mov_b32_e32 v11, v167
	v_cvt_pk_fp8_f32 v11, v5, v16
	v_mul_f32_e32 v13, v21, v13
	v_mul_f32_e32 v12, 0x41800000, v18
	v_mul_f32_e32 v5, 0x41800000, v13
	v_med3_f32 v12, v12, s53, v205
	v_med3_f32 v5, v5, s53, v205
	v_cvt_pk_fp8_f32 v11, v12, v5 op_sel:[0,0,1]
	v_add_u32_e32 v16, 48, v4
	v_pk_mul_f32 v[20:21], v[110:111], s[24:25] op_sel_hi:[1,0]
	v_pk_mul_f32 v[18:19], v[112:113], s[24:25] op_sel_hi:[1,0]
	global_store_dwordx2 v[14:15], v[10:11], off offset:128
	v_mad_i64_i32 v[10:11], s[2:3], v16, s47, v[6:7]
	v_lshl_add_u64 v[10:11], v[10:11], 0, v[8:9]
	v_pk_mul_f32 v[24:25], v[106:107], s[24:25] op_sel_hi:[1,0]
	v_pk_mul_f32 v[22:23], v[108:109], s[24:25] op_sel_hi:[1,0]
	v_ashrrev_i32_e32 v17, 31, v16
	s_waitcnt vmcnt(9)
	v_mov_b64_e32 v[12:13], v[238:239]
	v_mov_b64_e32 v[14:15], v[240:241]
	v_lshlrev_b32_e32 v5, 16, v12
	v_mul_f32_e32 v5, 0xbfb8aa3b, v5
	v_exp_f32_e32 v5, v5
	v_and_b32_e32 v12, 0xffff0000, v12
	v_mul_f32_e32 v12, 0xbfb8aa3b, v12
	v_exp_f32_e32 v12, v12
	v_add_f32_e32 v5, 1.0, v5
	v_add_f32_e32 v12, 1.0, v12
	v_lshlrev_b32_e32 v27, 16, v13
	v_rcp_f32_e32 v5, v5
	v_mul_f32_e32 v27, 0xbfb8aa3b, v27
	v_mul_f32_e32 v5, v20, v5
	v_exp_f32_e32 v27, v27
	s_nop 0
	v_add_f32_e32 v27, 1.0, v27
	v_and_b32_e32 v13, 0xffff0000, v13
	v_mul_f32_e32 v13, 0xbfb8aa3b, v13
	v_exp_f32_e32 v13, v13
	v_rcp_f32_e32 v12, v12
	s_nop 0
	v_mul_f32_e32 v12, v21, v12
	v_add_f32_e32 v13, 1.0, v13
	v_rcp_f32_e32 v20, v27
	v_lshlrev_b32_e32 v27, 16, v14
	v_mul_f32_e32 v18, v18, v20
	v_mul_f32_e32 v27, 0xbfb8aa3b, v27
	v_exp_f32_e32 v27, v27
	s_nop 0
	v_add_f32_e32 v26, 1.0, v27
	v_and_b32_e32 v14, 0xffff0000, v14
	v_mul_f32_e32 v14, 0xbfb8aa3b, v14
	v_rcp_f32_e32 v13, v13
	v_exp_f32_e32 v14, v14
	v_mul_f32_e32 v13, v19, v13
	v_add_f32_e32 v14, 1.0, v14
	v_rcp_f32_e32 v19, v26
	v_lshlrev_b32_e32 v26, 16, v15
	v_mul_f32_e32 v26, 0xbfb8aa3b, v26
	v_exp_f32_e32 v26, v26
	v_mul_f32_e32 v19, v24, v19
	v_add_f32_e32 v21, 1.0, v26
	v_and_b32_e32 v15, 0xffff0000, v15
	v_mul_f32_e32 v15, 0xbfb8aa3b, v15
	v_exp_f32_e32 v15, v15
	v_rcp_f32_e32 v14, v14
	s_nop 0
	v_mul_f32_e32 v14, v25, v14
	v_add_f32_e32 v15, 1.0, v15
	v_rcp_f32_e32 v20, v21
	s_nop 0
	v_mul_f32_e32 v20, v22, v20
	v_mul_f32_e32 v5, 0x41800000, v5
	v_mul_f32_e32 v12, 0x41800000, v12
	v_rcp_f32_e32 v15, v15
	v_med3_f32 v5, v5, s53, v205
	v_med3_f32 v21, v12, s53, v205
	v_mov_b32_e32 v12, v167
	v_cvt_pk_fp8_f32 v12, v5, v21
	v_mul_f32_e32 v18, 0x41800000, v18
	v_mul_f32_e32 v5, 0x41800000, v13
	v_med3_f32 v13, v18, s53, v205
	v_med3_f32 v5, v5, s53, v205
	v_cvt_pk_fp8_f32 v12, v13, v5 op_sel:[0,0,1]
	v_mul_f32_e32 v5, 0x41800000, v19
	v_mul_f32_e32 v13, 0x41800000, v14
	v_med3_f32 v5, v5, s53, v205
	v_med3_f32 v18, v13, s53, v205
	v_mov_b32_e32 v13, v167
	v_cvt_pk_fp8_f32 v13, v5, v18
	v_mul_f32_e32 v15, v23, v15
	v_mul_f32_e32 v14, 0x41800000, v20
	v_mul_f32_e32 v5, 0x41800000, v15
	v_med3_f32 v14, v14, s53, v205
	v_med3_f32 v5, v5, s53, v205
	v_cvt_pk_fp8_f32 v13, v14, v5 op_sel:[0,0,1]
	v_lshlrev_b64 v[14:15], 11, v[16:17]
	v_lshl_add_u64 v[14:15], s[14:15], 0, v[14:15]
	v_lshl_add_u64 v[14:15], v[14:15], 0, v[2:3]
	global_store_dwordx2 v[14:15], v[12:13], off
	v_pk_mul_f32 v[18:19], v[102:103], s[24:25] op_sel_hi:[1,0]
	v_pk_mul_f32 v[16:17], v[104:105], s[24:25] op_sel_hi:[1,0]
	v_pk_mul_f32 v[22:23], v[98:99], s[24:25] op_sel_hi:[1,0]
	v_pk_mul_f32 v[20:21], v[100:101], s[24:25] op_sel_hi:[1,0]
	s_waitcnt vmcnt(8)
	v_mov_b64_e32 v[10:11], v[242:243]
	v_mov_b64_e32 v[12:13], v[244:245]
	v_lshlrev_b32_e32 v5, 16, v10
	v_mul_f32_e32 v5, 0xbfb8aa3b, v5
	v_exp_f32_e32 v5, v5
	v_and_b32_e32 v10, 0xffff0000, v10
	v_mul_f32_e32 v10, 0xbfb8aa3b, v10
	v_exp_f32_e32 v10, v10
	v_add_f32_e32 v5, 1.0, v5
	v_add_f32_e32 v10, 1.0, v10
	v_lshlrev_b32_e32 v25, 16, v11
	v_rcp_f32_e32 v5, v5
	v_mul_f32_e32 v25, 0xbfb8aa3b, v25
	v_mul_f32_e32 v5, v18, v5
	v_exp_f32_e32 v25, v25
	s_nop 0
	v_add_f32_e32 v25, 1.0, v25
	v_and_b32_e32 v11, 0xffff0000, v11
	v_mul_f32_e32 v11, 0xbfb8aa3b, v11
	v_exp_f32_e32 v11, v11
	v_rcp_f32_e32 v10, v10
	s_nop 0
	v_mul_f32_e32 v10, v19, v10
	v_add_f32_e32 v11, 1.0, v11
	v_rcp_f32_e32 v18, v25
	v_lshlrev_b32_e32 v25, 16, v12
	v_mul_f32_e32 v16, v16, v18
	v_mul_f32_e32 v25, 0xbfb8aa3b, v25
	v_exp_f32_e32 v25, v25
	s_nop 0
	v_add_f32_e32 v24, 1.0, v25
	v_and_b32_e32 v12, 0xffff0000, v12
	v_mul_f32_e32 v12, 0xbfb8aa3b, v12
	v_rcp_f32_e32 v11, v11
	v_exp_f32_e32 v12, v12
	v_mul_f32_e32 v11, v17, v11
	v_add_f32_e32 v12, 1.0, v12
	v_rcp_f32_e32 v17, v24
	v_lshlrev_b32_e32 v24, 16, v13
	v_mul_f32_e32 v24, 0xbfb8aa3b, v24
	v_exp_f32_e32 v24, v24
	v_mul_f32_e32 v17, v22, v17
	v_add_f32_e32 v19, 1.0, v24
	v_and_b32_e32 v13, 0xffff0000, v13
	v_mul_f32_e32 v13, 0xbfb8aa3b, v13
	v_exp_f32_e32 v13, v13
	v_rcp_f32_e32 v12, v12
	s_nop 0
	v_mul_f32_e32 v12, v23, v12
	v_add_f32_e32 v13, 1.0, v13
	v_rcp_f32_e32 v18, v19
	s_nop 0
	v_mul_f32_e32 v18, v20, v18
	v_mul_f32_e32 v5, 0x41800000, v5
	v_mul_f32_e32 v10, 0x41800000, v10
	v_rcp_f32_e32 v13, v13
	v_med3_f32 v5, v5, s53, v205
	v_med3_f32 v19, v10, s53, v205
	v_mov_b32_e32 v10, v167
	v_cvt_pk_fp8_f32 v10, v5, v19
	v_mul_f32_e32 v16, 0x41800000, v16
	v_mul_f32_e32 v5, 0x41800000, v11
	v_med3_f32 v11, v16, s53, v205
	v_med3_f32 v5, v5, s53, v205
	v_cvt_pk_fp8_f32 v10, v11, v5 op_sel:[0,0,1]
	v_mul_f32_e32 v5, 0x41800000, v17
	v_mul_f32_e32 v11, 0x41800000, v12
	v_med3_f32 v5, v5, s53, v205
	v_med3_f32 v16, v11, s53, v205
	v_mov_b32_e32 v11, v167
	v_cvt_pk_fp8_f32 v11, v5, v16
	v_mul_f32_e32 v13, v21, v13
	v_mul_f32_e32 v12, 0x41800000, v18
	v_mul_f32_e32 v5, 0x41800000, v13
	v_med3_f32 v12, v12, s53, v205
	v_med3_f32 v5, v5, s53, v205
	v_cvt_pk_fp8_f32 v11, v12, v5 op_sel:[0,0,1]
	v_add_u32_e32 v16, 0x80, v4
	v_pk_mul_f32 v[20:21], v[94:95], s[24:25] op_sel_hi:[1,0]
	v_pk_mul_f32 v[18:19], v[96:97], s[24:25] op_sel_hi:[1,0]
	global_store_dwordx2 v[14:15], v[10:11], off offset:128
	v_mad_i64_i32 v[10:11], s[2:3], v16, s47, v[6:7]
	v_lshl_add_u64 v[10:11], v[10:11], 0, v[8:9]
	v_pk_mul_f32 v[24:25], v[90:91], s[24:25] op_sel_hi:[1,0]
	v_pk_mul_f32 v[22:23], v[92:93], s[24:25] op_sel_hi:[1,0]
	v_ashrrev_i32_e32 v17, 31, v16
	s_waitcnt vmcnt(7)
	v_mov_b64_e32 v[12:13], v[246:247]
	v_mov_b64_e32 v[14:15], v[248:249]
	v_lshlrev_b32_e32 v5, 16, v12
	v_mul_f32_e32 v5, 0xbfb8aa3b, v5
	v_exp_f32_e32 v5, v5
	v_and_b32_e32 v12, 0xffff0000, v12
	v_mul_f32_e32 v12, 0xbfb8aa3b, v12
	v_exp_f32_e32 v12, v12
	v_add_f32_e32 v5, 1.0, v5
	v_add_f32_e32 v12, 1.0, v12
	v_lshlrev_b32_e32 v27, 16, v13
	v_rcp_f32_e32 v5, v5
	v_mul_f32_e32 v27, 0xbfb8aa3b, v27
	v_mul_f32_e32 v5, v20, v5
	v_exp_f32_e32 v27, v27
	s_nop 0
	v_add_f32_e32 v27, 1.0, v27
	v_and_b32_e32 v13, 0xffff0000, v13
	v_mul_f32_e32 v13, 0xbfb8aa3b, v13
	v_exp_f32_e32 v13, v13
	v_rcp_f32_e32 v12, v12
	s_nop 0
	v_mul_f32_e32 v12, v21, v12
	v_add_f32_e32 v13, 1.0, v13
	v_rcp_f32_e32 v20, v27
	v_lshlrev_b32_e32 v27, 16, v14
	v_mul_f32_e32 v18, v18, v20
	v_mul_f32_e32 v27, 0xbfb8aa3b, v27
	v_exp_f32_e32 v27, v27
	s_nop 0
	v_add_f32_e32 v26, 1.0, v27
	v_and_b32_e32 v14, 0xffff0000, v14
	v_mul_f32_e32 v14, 0xbfb8aa3b, v14
	v_rcp_f32_e32 v13, v13
	v_exp_f32_e32 v14, v14
	v_mul_f32_e32 v13, v19, v13
	v_add_f32_e32 v14, 1.0, v14
	v_rcp_f32_e32 v19, v26
	v_lshlrev_b32_e32 v26, 16, v15
	v_mul_f32_e32 v26, 0xbfb8aa3b, v26
	v_exp_f32_e32 v26, v26
	v_mul_f32_e32 v19, v24, v19
	v_add_f32_e32 v21, 1.0, v26
	v_and_b32_e32 v15, 0xffff0000, v15
	v_mul_f32_e32 v15, 0xbfb8aa3b, v15
	v_exp_f32_e32 v15, v15
	v_rcp_f32_e32 v14, v14
	s_nop 0
	v_mul_f32_e32 v14, v25, v14
	v_add_f32_e32 v15, 1.0, v15
	v_rcp_f32_e32 v20, v21
	s_nop 0
	v_mul_f32_e32 v20, v22, v20
	v_mul_f32_e32 v5, 0x41800000, v5
	v_mul_f32_e32 v12, 0x41800000, v12
	v_rcp_f32_e32 v15, v15
	v_med3_f32 v5, v5, s53, v205
	v_med3_f32 v21, v12, s53, v205
	v_mov_b32_e32 v12, v167
	v_cvt_pk_fp8_f32 v12, v5, v21
	v_mul_f32_e32 v18, 0x41800000, v18
	v_mul_f32_e32 v5, 0x41800000, v13
	v_med3_f32 v13, v18, s53, v205
	v_med3_f32 v5, v5, s53, v205
	v_cvt_pk_fp8_f32 v12, v13, v5 op_sel:[0,0,1]
	v_mul_f32_e32 v5, 0x41800000, v19
	v_mul_f32_e32 v13, 0x41800000, v14
	v_med3_f32 v5, v5, s53, v205
	v_med3_f32 v18, v13, s53, v205
	v_mov_b32_e32 v13, v167
	v_cvt_pk_fp8_f32 v13, v5, v18
	v_mul_f32_e32 v15, v23, v15
	v_mul_f32_e32 v14, 0x41800000, v20
	v_mul_f32_e32 v5, 0x41800000, v15
	v_med3_f32 v14, v14, s53, v205
	v_med3_f32 v5, v5, s53, v205
	v_cvt_pk_fp8_f32 v13, v14, v5 op_sel:[0,0,1]
	v_lshlrev_b64 v[14:15], 11, v[16:17]
	v_lshl_add_u64 v[14:15], s[14:15], 0, v[14:15]
	v_lshl_add_u64 v[14:15], v[14:15], 0, v[2:3]
	global_store_dwordx2 v[14:15], v[12:13], off
	v_pk_mul_f32 v[18:19], v[86:87], s[24:25] op_sel_hi:[1,0]
	v_pk_mul_f32 v[16:17], v[88:89], s[24:25] op_sel_hi:[1,0]
	v_pk_mul_f32 v[22:23], v[82:83], s[24:25] op_sel_hi:[1,0]
	v_pk_mul_f32 v[20:21], v[84:85], s[24:25] op_sel_hi:[1,0]
	s_waitcnt vmcnt(6)
	v_mov_b64_e32 v[10:11], v[250:251]
	v_mov_b64_e32 v[12:13], v[252:253]
	v_lshlrev_b32_e32 v5, 16, v10
	v_mul_f32_e32 v5, 0xbfb8aa3b, v5
	v_exp_f32_e32 v5, v5
	v_and_b32_e32 v10, 0xffff0000, v10
	v_mul_f32_e32 v10, 0xbfb8aa3b, v10
	v_exp_f32_e32 v10, v10
	v_add_f32_e32 v5, 1.0, v5
	v_add_f32_e32 v10, 1.0, v10
	v_lshlrev_b32_e32 v25, 16, v11
	v_rcp_f32_e32 v5, v5
	v_mul_f32_e32 v25, 0xbfb8aa3b, v25
	v_mul_f32_e32 v5, v18, v5
	v_exp_f32_e32 v25, v25
	s_nop 0
	v_add_f32_e32 v25, 1.0, v25
	v_and_b32_e32 v11, 0xffff0000, v11
	v_mul_f32_e32 v11, 0xbfb8aa3b, v11
	v_exp_f32_e32 v11, v11
	v_rcp_f32_e32 v10, v10
	s_nop 0
	v_mul_f32_e32 v10, v19, v10
	v_add_f32_e32 v11, 1.0, v11
	v_rcp_f32_e32 v18, v25
	v_lshlrev_b32_e32 v25, 16, v12
	v_mul_f32_e32 v16, v16, v18
	v_mul_f32_e32 v25, 0xbfb8aa3b, v25
	v_exp_f32_e32 v25, v25
	s_nop 0
	v_add_f32_e32 v24, 1.0, v25
	v_and_b32_e32 v12, 0xffff0000, v12
	v_mul_f32_e32 v12, 0xbfb8aa3b, v12
	v_rcp_f32_e32 v11, v11
	v_exp_f32_e32 v12, v12
	v_mul_f32_e32 v11, v17, v11
	v_add_f32_e32 v12, 1.0, v12
	v_rcp_f32_e32 v17, v24
	v_lshlrev_b32_e32 v24, 16, v13
	v_mul_f32_e32 v24, 0xbfb8aa3b, v24
	v_exp_f32_e32 v24, v24
	v_mul_f32_e32 v17, v22, v17
	v_add_f32_e32 v19, 1.0, v24
	v_and_b32_e32 v13, 0xffff0000, v13
	v_mul_f32_e32 v13, 0xbfb8aa3b, v13
	v_exp_f32_e32 v13, v13
	v_rcp_f32_e32 v12, v12
	s_nop 0
	v_mul_f32_e32 v12, v23, v12
	v_add_f32_e32 v13, 1.0, v13
	v_rcp_f32_e32 v18, v19
	s_nop 0
	v_mul_f32_e32 v18, v20, v18
	v_mul_f32_e32 v5, 0x41800000, v5
	v_mul_f32_e32 v10, 0x41800000, v10
	v_rcp_f32_e32 v13, v13
	v_med3_f32 v5, v5, s53, v205
	v_med3_f32 v19, v10, s53, v205
	v_mov_b32_e32 v10, v167
	v_cvt_pk_fp8_f32 v10, v5, v19
	v_mul_f32_e32 v16, 0x41800000, v16
	v_mul_f32_e32 v5, 0x41800000, v11
	v_med3_f32 v11, v16, s53, v205
	v_med3_f32 v5, v5, s53, v205
	v_cvt_pk_fp8_f32 v10, v11, v5 op_sel:[0,0,1]
	v_mul_f32_e32 v5, 0x41800000, v17
	v_mul_f32_e32 v11, 0x41800000, v12
	v_med3_f32 v5, v5, s53, v205
	v_med3_f32 v16, v11, s53, v205
	v_mov_b32_e32 v11, v167
	v_cvt_pk_fp8_f32 v11, v5, v16
	v_mul_f32_e32 v13, v21, v13
	v_mul_f32_e32 v12, 0x41800000, v18
	v_mul_f32_e32 v5, 0x41800000, v13
	v_med3_f32 v12, v12, s53, v205
	v_med3_f32 v5, v5, s53, v205
	v_cvt_pk_fp8_f32 v11, v12, v5 op_sel:[0,0,1]
	v_add_u32_e32 v16, 0x90, v4
	v_pk_mul_f32 v[20:21], v[78:79], s[24:25] op_sel_hi:[1,0]
	v_pk_mul_f32 v[18:19], v[80:81], s[24:25] op_sel_hi:[1,0]
	global_store_dwordx2 v[14:15], v[10:11], off offset:128
	v_mad_i64_i32 v[10:11], s[2:3], v16, s47, v[6:7]
	v_lshl_add_u64 v[10:11], v[10:11], 0, v[8:9]
	v_pk_mul_f32 v[24:25], v[74:75], s[24:25] op_sel_hi:[1,0]
	v_pk_mul_f32 v[22:23], v[76:77], s[24:25] op_sel_hi:[1,0]
	v_ashrrev_i32_e32 v17, 31, v16
	s_waitcnt vmcnt(5)
	v_mov_b64_e32 v[12:13], v[214:215]
	v_mov_b64_e32 v[14:15], v[216:217]
	v_lshlrev_b32_e32 v5, 16, v12
	v_mul_f32_e32 v5, 0xbfb8aa3b, v5
	v_exp_f32_e32 v5, v5
	v_and_b32_e32 v12, 0xffff0000, v12
	v_mul_f32_e32 v12, 0xbfb8aa3b, v12
	v_exp_f32_e32 v12, v12
	v_add_f32_e32 v5, 1.0, v5
	v_add_f32_e32 v12, 1.0, v12
	v_lshlrev_b32_e32 v27, 16, v13
	v_rcp_f32_e32 v5, v5
	v_mul_f32_e32 v27, 0xbfb8aa3b, v27
	v_mul_f32_e32 v5, v20, v5
	v_exp_f32_e32 v27, v27
	s_nop 0
	v_add_f32_e32 v27, 1.0, v27
	v_and_b32_e32 v13, 0xffff0000, v13
	v_mul_f32_e32 v13, 0xbfb8aa3b, v13
	v_exp_f32_e32 v13, v13
	v_rcp_f32_e32 v12, v12
	s_nop 0
	v_mul_f32_e32 v12, v21, v12
	v_add_f32_e32 v13, 1.0, v13
	v_rcp_f32_e32 v20, v27
	v_lshlrev_b32_e32 v27, 16, v14
	v_mul_f32_e32 v18, v18, v20
	v_mul_f32_e32 v27, 0xbfb8aa3b, v27
	v_exp_f32_e32 v27, v27
	s_nop 0
	v_add_f32_e32 v26, 1.0, v27
	v_and_b32_e32 v14, 0xffff0000, v14
	v_mul_f32_e32 v14, 0xbfb8aa3b, v14
	v_rcp_f32_e32 v13, v13
	v_exp_f32_e32 v14, v14
	v_mul_f32_e32 v13, v19, v13
	v_add_f32_e32 v14, 1.0, v14
	v_rcp_f32_e32 v19, v26
	v_lshlrev_b32_e32 v26, 16, v15
	v_mul_f32_e32 v26, 0xbfb8aa3b, v26
	v_exp_f32_e32 v26, v26
	v_mul_f32_e32 v19, v24, v19
	v_add_f32_e32 v21, 1.0, v26
	v_and_b32_e32 v15, 0xffff0000, v15
	v_mul_f32_e32 v15, 0xbfb8aa3b, v15
	v_exp_f32_e32 v15, v15
	v_rcp_f32_e32 v14, v14
	s_nop 0
	v_mul_f32_e32 v14, v25, v14
	v_add_f32_e32 v15, 1.0, v15
	v_rcp_f32_e32 v20, v21
	s_nop 0
	v_mul_f32_e32 v20, v22, v20
	v_mul_f32_e32 v5, 0x41800000, v5
	v_mul_f32_e32 v12, 0x41800000, v12
	v_rcp_f32_e32 v15, v15
	v_med3_f32 v5, v5, s53, v205
	v_med3_f32 v21, v12, s53, v205
	v_mov_b32_e32 v12, v167
	v_cvt_pk_fp8_f32 v12, v5, v21
	v_mul_f32_e32 v18, 0x41800000, v18
	v_mul_f32_e32 v5, 0x41800000, v13
	v_med3_f32 v13, v18, s53, v205
	v_med3_f32 v5, v5, s53, v205
	v_cvt_pk_fp8_f32 v12, v13, v5 op_sel:[0,0,1]
	v_mul_f32_e32 v5, 0x41800000, v19
	v_mul_f32_e32 v13, 0x41800000, v14
	v_med3_f32 v5, v5, s53, v205
	v_med3_f32 v18, v13, s53, v205
	v_mov_b32_e32 v13, v167
	v_cvt_pk_fp8_f32 v13, v5, v18
	v_mul_f32_e32 v15, v23, v15
	v_mul_f32_e32 v14, 0x41800000, v20
	v_mul_f32_e32 v5, 0x41800000, v15
	v_med3_f32 v14, v14, s53, v205
	v_med3_f32 v5, v5, s53, v205
	v_cvt_pk_fp8_f32 v13, v14, v5 op_sel:[0,0,1]
	v_lshlrev_b64 v[14:15], 11, v[16:17]
	v_lshl_add_u64 v[14:15], s[14:15], 0, v[14:15]
	v_lshl_add_u64 v[14:15], v[14:15], 0, v[2:3]
	global_store_dwordx2 v[14:15], v[12:13], off
	v_pk_mul_f32 v[18:19], v[70:71], s[24:25] op_sel_hi:[1,0]
	v_pk_mul_f32 v[16:17], v[72:73], s[24:25] op_sel_hi:[1,0]
	v_pk_mul_f32 v[22:23], v[66:67], s[24:25] op_sel_hi:[1,0]
	v_pk_mul_f32 v[20:21], v[68:69], s[24:25] op_sel_hi:[1,0]
	s_waitcnt vmcnt(4)
	v_mov_b64_e32 v[10:11], v[218:219]
	v_mov_b64_e32 v[12:13], v[220:221]
	v_lshlrev_b32_e32 v5, 16, v10
	v_mul_f32_e32 v5, 0xbfb8aa3b, v5
	v_exp_f32_e32 v5, v5
	v_and_b32_e32 v10, 0xffff0000, v10
	v_mul_f32_e32 v10, 0xbfb8aa3b, v10
	v_exp_f32_e32 v10, v10
	v_add_f32_e32 v5, 1.0, v5
	v_add_f32_e32 v10, 1.0, v10
	v_lshlrev_b32_e32 v25, 16, v11
	v_rcp_f32_e32 v5, v5
	v_mul_f32_e32 v25, 0xbfb8aa3b, v25
	v_mul_f32_e32 v5, v18, v5
	v_exp_f32_e32 v25, v25
	s_nop 0
	v_add_f32_e32 v25, 1.0, v25
	v_and_b32_e32 v11, 0xffff0000, v11
	v_mul_f32_e32 v11, 0xbfb8aa3b, v11
	v_exp_f32_e32 v11, v11
	v_rcp_f32_e32 v10, v10
	s_nop 0
	v_mul_f32_e32 v10, v19, v10
	v_add_f32_e32 v11, 1.0, v11
	v_rcp_f32_e32 v18, v25
	v_lshlrev_b32_e32 v25, 16, v12
	v_mul_f32_e32 v16, v16, v18
	v_mul_f32_e32 v25, 0xbfb8aa3b, v25
	v_exp_f32_e32 v25, v25
	s_nop 0
	v_add_f32_e32 v24, 1.0, v25
	v_and_b32_e32 v12, 0xffff0000, v12
	v_mul_f32_e32 v12, 0xbfb8aa3b, v12
	v_rcp_f32_e32 v11, v11
	v_exp_f32_e32 v12, v12
	v_mul_f32_e32 v11, v17, v11
	v_add_f32_e32 v12, 1.0, v12
	v_rcp_f32_e32 v17, v24
	v_lshlrev_b32_e32 v24, 16, v13
	v_mul_f32_e32 v24, 0xbfb8aa3b, v24
	v_exp_f32_e32 v24, v24
	v_mul_f32_e32 v17, v22, v17
	v_add_f32_e32 v19, 1.0, v24
	v_and_b32_e32 v13, 0xffff0000, v13
	v_mul_f32_e32 v13, 0xbfb8aa3b, v13
	v_exp_f32_e32 v13, v13
	v_rcp_f32_e32 v12, v12
	s_nop 0
	v_mul_f32_e32 v12, v23, v12
	v_add_f32_e32 v13, 1.0, v13
	v_rcp_f32_e32 v18, v19
	s_nop 0
	v_mul_f32_e32 v18, v20, v18
	v_mul_f32_e32 v5, 0x41800000, v5
	v_mul_f32_e32 v10, 0x41800000, v10
	v_rcp_f32_e32 v13, v13
	v_med3_f32 v5, v5, s53, v205
	v_med3_f32 v19, v10, s53, v205
	v_mov_b32_e32 v10, v167
	v_cvt_pk_fp8_f32 v10, v5, v19
	v_mul_f32_e32 v16, 0x41800000, v16
	v_mul_f32_e32 v5, 0x41800000, v11
	v_med3_f32 v11, v16, s53, v205
	v_med3_f32 v5, v5, s53, v205
	v_cvt_pk_fp8_f32 v10, v11, v5 op_sel:[0,0,1]
	v_mul_f32_e32 v5, 0x41800000, v17
	v_mul_f32_e32 v11, 0x41800000, v12
	v_med3_f32 v5, v5, s53, v205
	v_med3_f32 v16, v11, s53, v205
	v_mov_b32_e32 v11, v167
	v_cvt_pk_fp8_f32 v11, v5, v16
	v_mul_f32_e32 v13, v21, v13
	v_mul_f32_e32 v12, 0x41800000, v18
	v_mul_f32_e32 v5, 0x41800000, v13
	v_med3_f32 v12, v12, s53, v205
	v_med3_f32 v5, v5, s53, v205
	v_cvt_pk_fp8_f32 v11, v12, v5 op_sel:[0,0,1]
	v_add_u32_e32 v16, 0xa0, v4
	v_pk_mul_f32 v[20:21], v[62:63], s[24:25] op_sel_hi:[1,0]
	v_pk_mul_f32 v[18:19], v[64:65], s[24:25] op_sel_hi:[1,0]
	global_store_dwordx2 v[14:15], v[10:11], off offset:128
	v_mad_i64_i32 v[10:11], s[2:3], v16, s47, v[6:7]
	v_lshl_add_u64 v[10:11], v[10:11], 0, v[8:9]
	v_pk_mul_f32 v[24:25], v[58:59], s[24:25] op_sel_hi:[1,0]
	v_pk_mul_f32 v[22:23], v[60:61], s[24:25] op_sel_hi:[1,0]
	v_ashrrev_i32_e32 v17, 31, v16
	s_waitcnt vmcnt(3)
	v_mov_b64_e32 v[12:13], v[222:223]
	v_mov_b64_e32 v[14:15], v[224:225]
	v_lshlrev_b32_e32 v5, 16, v12
	v_mul_f32_e32 v5, 0xbfb8aa3b, v5
	v_exp_f32_e32 v5, v5
	v_and_b32_e32 v12, 0xffff0000, v12
	v_mul_f32_e32 v12, 0xbfb8aa3b, v12
	v_exp_f32_e32 v12, v12
	v_add_f32_e32 v5, 1.0, v5
	v_add_f32_e32 v12, 1.0, v12
	v_lshlrev_b32_e32 v27, 16, v13
	v_rcp_f32_e32 v5, v5
	v_mul_f32_e32 v27, 0xbfb8aa3b, v27
	v_mul_f32_e32 v5, v20, v5
	v_exp_f32_e32 v27, v27
	s_nop 0
	v_add_f32_e32 v27, 1.0, v27
	v_and_b32_e32 v13, 0xffff0000, v13
	v_mul_f32_e32 v13, 0xbfb8aa3b, v13
	v_exp_f32_e32 v13, v13
	v_rcp_f32_e32 v12, v12
	s_nop 0
	v_mul_f32_e32 v12, v21, v12
	v_add_f32_e32 v13, 1.0, v13
	v_rcp_f32_e32 v20, v27
	v_lshlrev_b32_e32 v27, 16, v14
	v_mul_f32_e32 v18, v18, v20
	v_mul_f32_e32 v27, 0xbfb8aa3b, v27
	v_exp_f32_e32 v27, v27
	s_nop 0
	v_add_f32_e32 v26, 1.0, v27
	v_and_b32_e32 v14, 0xffff0000, v14
	v_mul_f32_e32 v14, 0xbfb8aa3b, v14
	v_rcp_f32_e32 v13, v13
	v_exp_f32_e32 v14, v14
	v_mul_f32_e32 v13, v19, v13
	v_add_f32_e32 v14, 1.0, v14
	v_rcp_f32_e32 v19, v26
	v_lshlrev_b32_e32 v26, 16, v15
	v_mul_f32_e32 v26, 0xbfb8aa3b, v26
	v_exp_f32_e32 v26, v26
	v_mul_f32_e32 v19, v24, v19
	v_add_f32_e32 v21, 1.0, v26
	v_and_b32_e32 v15, 0xffff0000, v15
	v_mul_f32_e32 v15, 0xbfb8aa3b, v15
	v_exp_f32_e32 v15, v15
	v_rcp_f32_e32 v14, v14
	s_nop 0
	v_mul_f32_e32 v14, v25, v14
	v_add_f32_e32 v15, 1.0, v15
	v_rcp_f32_e32 v20, v21
	s_nop 0
	v_mul_f32_e32 v20, v22, v20
	v_mul_f32_e32 v5, 0x41800000, v5
	v_mul_f32_e32 v12, 0x41800000, v12
	v_rcp_f32_e32 v15, v15
	v_med3_f32 v5, v5, s53, v205
	v_med3_f32 v21, v12, s53, v205
	v_mov_b32_e32 v12, v167
	v_cvt_pk_fp8_f32 v12, v5, v21
	v_mul_f32_e32 v18, 0x41800000, v18
	v_mul_f32_e32 v5, 0x41800000, v13
	v_med3_f32 v13, v18, s53, v205
	v_med3_f32 v5, v5, s53, v205
	v_cvt_pk_fp8_f32 v12, v13, v5 op_sel:[0,0,1]
	v_mul_f32_e32 v5, 0x41800000, v19
	v_mul_f32_e32 v13, 0x41800000, v14
	v_med3_f32 v5, v5, s53, v205
	v_med3_f32 v18, v13, s53, v205
	v_mov_b32_e32 v13, v167
	v_cvt_pk_fp8_f32 v13, v5, v18
	v_mul_f32_e32 v15, v23, v15
	v_mul_f32_e32 v14, 0x41800000, v20
	v_mul_f32_e32 v5, 0x41800000, v15
	v_med3_f32 v14, v14, s53, v205
	v_med3_f32 v5, v5, s53, v205
	v_cvt_pk_fp8_f32 v13, v14, v5 op_sel:[0,0,1]
	v_lshlrev_b64 v[14:15], 11, v[16:17]
	v_lshl_add_u64 v[14:15], s[14:15], 0, v[14:15]
	v_lshl_add_u64 v[14:15], v[14:15], 0, v[2:3]
	global_store_dwordx2 v[14:15], v[12:13], off
	v_pk_mul_f32 v[18:19], v[54:55], s[24:25] op_sel_hi:[1,0]
	v_pk_mul_f32 v[16:17], v[56:57], s[24:25] op_sel_hi:[1,0]
	v_pk_mul_f32 v[22:23], v[50:51], s[24:25] op_sel_hi:[1,0]
	v_pk_mul_f32 v[20:21], v[52:53], s[24:25] op_sel_hi:[1,0]
	s_waitcnt vmcnt(2)
	v_mov_b64_e32 v[10:11], v[226:227]
	v_mov_b64_e32 v[12:13], v[228:229]
	v_lshlrev_b32_e32 v5, 16, v10
	v_mul_f32_e32 v5, 0xbfb8aa3b, v5
	v_exp_f32_e32 v5, v5
	v_and_b32_e32 v10, 0xffff0000, v10
	v_mul_f32_e32 v10, 0xbfb8aa3b, v10
	v_exp_f32_e32 v10, v10
	v_add_f32_e32 v5, 1.0, v5
	v_add_f32_e32 v10, 1.0, v10
	v_lshlrev_b32_e32 v25, 16, v11
	v_rcp_f32_e32 v5, v5
	v_mul_f32_e32 v25, 0xbfb8aa3b, v25
	v_mul_f32_e32 v5, v18, v5
	v_exp_f32_e32 v25, v25
	s_nop 0
	v_add_f32_e32 v25, 1.0, v25
	v_and_b32_e32 v11, 0xffff0000, v11
	v_mul_f32_e32 v11, 0xbfb8aa3b, v11
	v_exp_f32_e32 v11, v11
	v_rcp_f32_e32 v10, v10
	s_nop 0
	v_mul_f32_e32 v10, v19, v10
	v_add_f32_e32 v11, 1.0, v11
	v_rcp_f32_e32 v18, v25
	v_lshlrev_b32_e32 v25, 16, v12
	v_mul_f32_e32 v16, v16, v18
	v_mul_f32_e32 v25, 0xbfb8aa3b, v25
	v_exp_f32_e32 v25, v25
	s_nop 0
	v_add_f32_e32 v24, 1.0, v25
	v_and_b32_e32 v12, 0xffff0000, v12
	v_mul_f32_e32 v12, 0xbfb8aa3b, v12
	v_rcp_f32_e32 v11, v11
	v_exp_f32_e32 v12, v12
	v_mul_f32_e32 v11, v17, v11
	v_add_f32_e32 v12, 1.0, v12
	v_rcp_f32_e32 v17, v24
	v_lshlrev_b32_e32 v24, 16, v13
	v_mul_f32_e32 v24, 0xbfb8aa3b, v24
	v_exp_f32_e32 v24, v24
	v_mul_f32_e32 v17, v22, v17
	v_add_f32_e32 v19, 1.0, v24
	v_and_b32_e32 v13, 0xffff0000, v13
	v_mul_f32_e32 v13, 0xbfb8aa3b, v13
	v_exp_f32_e32 v13, v13
	v_rcp_f32_e32 v12, v12
	s_nop 0
	v_mul_f32_e32 v12, v23, v12
	v_add_f32_e32 v13, 1.0, v13
	v_rcp_f32_e32 v18, v19
	s_nop 0
	v_mul_f32_e32 v18, v20, v18
	v_mul_f32_e32 v5, 0x41800000, v5
	v_mul_f32_e32 v10, 0x41800000, v10
	v_rcp_f32_e32 v13, v13
	v_med3_f32 v5, v5, s53, v205
	v_med3_f32 v19, v10, s53, v205
	v_mov_b32_e32 v10, v167
	v_cvt_pk_fp8_f32 v10, v5, v19
	v_mul_f32_e32 v16, 0x41800000, v16
	v_mul_f32_e32 v5, 0x41800000, v11
	v_med3_f32 v11, v16, s53, v205
	v_med3_f32 v5, v5, s53, v205
	v_cvt_pk_fp8_f32 v10, v11, v5 op_sel:[0,0,1]
	v_mul_f32_e32 v5, 0x41800000, v17
	v_mul_f32_e32 v11, 0x41800000, v12
	v_med3_f32 v5, v5, s53, v205
	v_med3_f32 v16, v11, s53, v205
	v_mov_b32_e32 v11, v167
	v_cvt_pk_fp8_f32 v11, v5, v16
	v_mul_f32_e32 v13, v21, v13
	v_mul_f32_e32 v12, 0x41800000, v18
	v_mul_f32_e32 v5, 0x41800000, v13
	v_med3_f32 v12, v12, s53, v205
	v_med3_f32 v5, v5, s53, v205
	v_cvt_pk_fp8_f32 v11, v12, v5 op_sel:[0,0,1]
	v_pk_mul_f32 v[12:13], v[48:49], s[24:25] op_sel_hi:[1,0]
	v_pk_mul_f32 v[18:19], v[42:43], s[24:25] op_sel_hi:[1,0]
	v_pk_mul_f32 v[16:17], v[44:45], s[24:25] op_sel_hi:[1,0]
	global_store_dwordx2 v[14:15], v[10:11], off offset:128
	v_add_u32_e32 v10, 0xb0, v4
	v_mad_i64_i32 v[4:5], s[2:3], v10, s47, v[6:7]
	v_lshl_add_u64 v[4:5], v[4:5], 0, v[8:9]
	s_waitcnt vmcnt(1)
	v_mov_b64_e32 v[6:7], v[230:231]
	v_mov_b64_e32 v[8:9], v[232:233]
	v_lshlrev_b32_e32 v11, 16, v6
	v_mul_f32_e32 v11, 0xbfb8aa3b, v11
	v_exp_f32_e32 v14, v11
	v_and_b32_e32 v6, 0xffff0000, v6
	v_mul_f32_e32 v6, 0xbfb8aa3b, v6
	v_exp_f32_e32 v6, v6
	v_add_f32_e32 v20, 1.0, v14
	v_add_f32_e32 v6, 1.0, v6
	v_pk_mul_f32 v[14:15], v[46:47], s[24:25] op_sel_hi:[1,0]
	v_ashrrev_i32_e32 v11, 31, v10
	v_lshlrev_b32_e32 v22, 16, v7
	v_rcp_f32_e32 v20, v20
	v_mul_f32_e32 v22, 0xbfb8aa3b, v22
	v_mul_f32_e32 v14, v14, v20
	v_exp_f32_e32 v22, v22
	s_nop 0
	v_add_f32_e32 v22, 1.0, v22
	v_and_b32_e32 v7, 0xffff0000, v7
	v_mul_f32_e32 v7, 0xbfb8aa3b, v7
	v_rcp_f32_e32 v6, v6
	v_exp_f32_e32 v7, v7
	v_mul_f32_e32 v6, v15, v6
	v_add_f32_e32 v7, 1.0, v7
	v_rcp_f32_e32 v15, v22
	v_lshlrev_b32_e32 v22, 16, v8
	v_mul_f32_e32 v12, v12, v15
	v_mul_f32_e32 v22, 0xbfb8aa3b, v22
	v_exp_f32_e32 v22, v22
	s_nop 0
	v_add_f32_e32 v21, 1.0, v22
	v_and_b32_e32 v8, 0xffff0000, v8
	v_mul_f32_e32 v8, 0xbfb8aa3b, v8
	v_rcp_f32_e32 v7, v7
	v_exp_f32_e32 v8, v8
	v_mul_f32_e32 v7, v13, v7
	v_add_f32_e32 v8, 1.0, v8
	v_rcp_f32_e32 v13, v21
	v_lshlrev_b32_e32 v21, 16, v9
	v_mul_f32_e32 v21, 0xbfb8aa3b, v21
	v_exp_f32_e32 v21, v21
	v_mul_f32_e32 v13, v18, v13
	v_add_f32_e32 v20, 1.0, v21
	v_and_b32_e32 v9, 0xffff0000, v9
	v_mul_f32_e32 v9, 0xbfb8aa3b, v9
	v_exp_f32_e32 v9, v9
	v_rcp_f32_e32 v8, v8
	s_nop 0
	v_mul_f32_e32 v8, v19, v8
	v_add_f32_e32 v9, 1.0, v9
	v_rcp_f32_e32 v15, v20
	s_nop 0
	v_mul_f32_e32 v15, v16, v15
	v_mul_f32_e32 v14, 0x41800000, v14
	v_mul_f32_e32 v6, 0x41800000, v6
	v_rcp_f32_e32 v9, v9
	v_med3_f32 v14, v14, s53, v205
	v_med3_f32 v16, v6, s53, v205
	v_mov_b32_e32 v6, v167
	v_cvt_pk_fp8_f32 v6, v14, v16
	v_mul_f32_e32 v12, 0x41800000, v12
	v_mul_f32_e32 v7, 0x41800000, v7
	v_med3_f32 v12, v12, s53, v205
	v_med3_f32 v7, v7, s53, v205
	v_cvt_pk_fp8_f32 v6, v12, v7 op_sel:[0,0,1]
	v_mul_f32_e32 v7, 0x41800000, v13
	v_mul_f32_e32 v8, 0x41800000, v8
	v_med3_f32 v13, v7, s53, v205
	v_med3_f32 v8, v8, s53, v205
	v_mov_b32_e32 v7, v167
	v_cvt_pk_fp8_f32 v7, v13, v8
	v_mul_f32_e32 v9, v17, v9
	v_mul_f32_e32 v12, 0x41800000, v15
	v_mul_f32_e32 v8, 0x41800000, v9
	v_med3_f32 v9, v12, s53, v205
	v_med3_f32 v8, v8, s53, v205
	v_cvt_pk_fp8_f32 v7, v9, v8 op_sel:[0,0,1]
	v_lshlrev_b64 v[8:9], 11, v[10:11]
	v_lshl_add_u64 v[8:9], s[14:15], 0, v[8:9]
	v_lshl_add_u64 v[8:9], v[8:9], 0, v[2:3]
	global_store_dwordx2 v[8:9], v[6:7], off
	v_pk_mul_f32 v[14:15], v[34:35], s[24:25] op_sel_hi:[1,0]
	v_pk_mul_f32 v[12:13], v[36:37], s[24:25] op_sel_hi:[1,0]
	s_waitcnt vmcnt(0)
	v_mov_b64_e32 v[2:3], v[234:235]
	v_mov_b64_e32 v[4:5], v[236:237]
	v_lshlrev_b32_e32 v6, 16, v2
	v_mul_f32_e32 v6, 0xbfb8aa3b, v6
	v_exp_f32_e32 v10, v6
	v_and_b32_e32 v2, 0xffff0000, v2
	v_mul_f32_e32 v2, 0xbfb8aa3b, v2
	v_exp_f32_e32 v2, v2
	v_add_f32_e32 v16, 1.0, v10
	v_add_f32_e32 v2, 1.0, v2
	v_pk_mul_f32 v[10:11], v[38:39], s[24:25] op_sel_hi:[1,0]
	v_pk_mul_f32 v[6:7], v[40:41], s[24:25] op_sel_hi:[1,0]
	v_lshlrev_b32_e32 v18, 16, v3
	v_rcp_f32_e32 v16, v16
	v_mul_f32_e32 v18, 0xbfb8aa3b, v18
	v_mul_f32_e32 v10, v10, v16
	v_exp_f32_e32 v18, v18
	s_nop 0
	v_add_f32_e32 v18, 1.0, v18
	v_and_b32_e32 v3, 0xffff0000, v3
	v_mul_f32_e32 v3, 0xbfb8aa3b, v3
	v_rcp_f32_e32 v2, v2
	v_exp_f32_e32 v3, v3
	v_mul_f32_e32 v2, v11, v2
	v_add_f32_e32 v3, 1.0, v3
	v_rcp_f32_e32 v11, v18
	v_lshlrev_b32_e32 v18, 16, v4
	v_mul_f32_e32 v6, v6, v11
	v_mul_f32_e32 v18, 0xbfb8aa3b, v18
	v_exp_f32_e32 v18, v18
	s_nop 0
	v_add_f32_e32 v17, 1.0, v18
	v_and_b32_e32 v4, 0xffff0000, v4
	v_mul_f32_e32 v4, 0xbfb8aa3b, v4
	v_rcp_f32_e32 v3, v3
	v_exp_f32_e32 v4, v4
	v_mul_f32_e32 v3, v7, v3
	v_add_f32_e32 v4, 1.0, v4
	v_rcp_f32_e32 v7, v17
	v_lshlrev_b32_e32 v17, 16, v5
	v_mul_f32_e32 v17, 0xbfb8aa3b, v17
	v_exp_f32_e32 v17, v17
	v_mul_f32_e32 v7, v14, v7
	v_add_f32_e32 v16, 1.0, v17
	v_and_b32_e32 v5, 0xffff0000, v5
	v_mul_f32_e32 v5, 0xbfb8aa3b, v5
	v_exp_f32_e32 v5, v5
	v_rcp_f32_e32 v4, v4
	s_nop 0
	v_mul_f32_e32 v4, v15, v4
	v_add_f32_e32 v5, 1.0, v5
	v_rcp_f32_e32 v11, v16
	s_nop 0
	v_mul_f32_e32 v11, v12, v11
	v_mul_f32_e32 v10, 0x41800000, v10
	v_mul_f32_e32 v2, 0x41800000, v2
	v_rcp_f32_e32 v5, v5
	v_med3_f32 v10, v10, s53, v205
	v_med3_f32 v12, v2, s53, v205
	v_mov_b32_e32 v2, v167
	v_cvt_pk_fp8_f32 v2, v10, v12
	v_mul_f32_e32 v6, 0x41800000, v6
	v_mul_f32_e32 v3, 0x41800000, v3
	v_med3_f32 v6, v6, s53, v205
	v_med3_f32 v3, v3, s53, v205
	v_cvt_pk_fp8_f32 v2, v6, v3 op_sel:[0,0,1]
	v_mul_f32_e32 v3, 0x41800000, v7
	v_mul_f32_e32 v4, 0x41800000, v4
	v_med3_f32 v7, v3, s53, v205
	v_med3_f32 v4, v4, s53, v205
	v_mov_b32_e32 v3, v167
	v_cvt_pk_fp8_f32 v3, v7, v4
	v_mul_f32_e32 v5, v13, v5
	v_mul_f32_e32 v6, 0x41800000, v11
	v_mul_f32_e32 v4, 0x41800000, v5
	v_med3_f32 v5, v6, s53, v205
	v_med3_f32 v4, v4, s53, v205
	v_cvt_pk_fp8_f32 v3, v5, v4 op_sel:[0,0,1]
	s_andn2_b64 vcc, exec, s[0:1]
	s_mov_b64 s[0:1], -1
	global_store_dwordx2 v[8:9], v[2:3], off offset:128
	s_cbranch_vccnz .LBB0_966
	s_andn2_b64 vcc, exec, s[12:13]
	s_cbranch_vccnz .LBB0_965
	s_barrier
	s_branch .LBB0_965

.LBB0_1066:
	v_lshl_or_b32 v6, s61, 8, v204
	v_add_u32_e32 v8, s60, v202
	v_ashrrev_i32_e32 v7, 31, v6
	v_mov_b64_e32 v[10:11], s[18:19]
	v_mad_i64_i32 v[2:3], s[0:1], v8, s56, v[10:11]
	v_lshlrev_b64 v[12:13], 1, v[6:7]
	v_lshl_add_u32 v251, v8, 11, v6
	v_mad_u32_u24 v250, v8, s56, v12
	global_load_dwordx4 v[214:217], v250, s[18:19]
	global_load_dwordx2 v[238:239], v251, s[16:17]
	v_lshl_add_u32 v251, v8, 11, v6
	v_mad_u32_u24 v250, v8, s56, v12
	global_load_dwordx4 v[218:221], v250, s[18:19] offset:256
	global_load_dwordx2 v[240:241], v251, s[16:17] offset:128
	v_add_u32_e32 v250, 16, v8
	v_lshl_add_u32 v251, v250, 11, v6
	v_mad_u32_u24 v250, v250, s56, v12
	global_load_dwordx4 v[222:225], v250, s[18:19]
	global_load_dwordx2 v[242:243], v251, s[16:17]
	v_add_u32_e32 v250, 16, v8
	v_lshl_add_u32 v251, v250, 11, v6
	v_mad_u32_u24 v250, v250, s56, v12
	global_load_dwordx4 v[226:229], v250, s[18:19] offset:256
	global_load_dwordx2 v[244:245], v251, s[16:17] offset:128
	v_add_u32_e32 v250, 32, v8
	v_lshl_add_u32 v251, v250, 11, v6
	v_mad_u32_u24 v250, v250, s56, v12
	global_load_dwordx4 v[230:233], v250, s[18:19]
	global_load_dwordx2 v[246:247], v251, s[16:17]
	v_add_u32_e32 v250, 32, v8
	v_lshl_add_u32 v251, v250, 11, v6
	v_mad_u32_u24 v250, v250, s56, v12
	global_load_dwordx4 v[234:237], v250, s[18:19] offset:256
	global_load_dwordx2 v[248:249], v251, s[16:17] offset:128
	s_nop 15
	s_nop 15
	s_nop 15
	v_lshl_add_u64 v[14:15], v[2:3], 0, v[12:13]
	v_ashrrev_i32_e32 v9, 31, v8
	v_lshlrev_b64 v[16:17], 11, v[8:9]
	v_lshl_add_u64 v[18:19], s[16:17], 0, v[16:17]
	v_lshl_add_u64 v[18:19], v[18:19], 0, v[6:7]
	v_pk_mul_f32 v[22:23], v[154:155], s[28:29] op_sel_hi:[1,0]
	v_pk_mul_f32 v[20:21], v[156:157], s[28:29] op_sel_hi:[1,0]
	v_pk_mul_f32 v[26:27], v[158:159], s[28:29] op_sel_hi:[1,0]
	v_pk_mul_f32 v[24:25], v[160:161], s[28:29] op_sel_hi:[1,0]
	s_waitcnt vmcnt(11)
	v_mov_b64_e32 v[2:3], v[214:215]
	v_mov_b64_e32 v[4:5], v[216:217]
	s_waitcnt vmcnt(10)
	v_mov_b64_e32 v[28:29], v[238:239]
	v_add_u32_e32 v250, 48, v8
	v_lshl_add_u32 v251, v250, 11, v6
	v_mad_u32_u24 v250, v250, s56, v12
	global_load_dwordx4 v[214:217], v250, s[18:19]
	global_load_dwordx2 v[238:239], v251, s[16:17]
	v_lshlrev_b32_e32 v9, 16, v2
	v_and_b32_e32 v2, 0xffff0000, v2
	v_mul_f32_e32 v9, 0xbfb8aa3b, v9
	v_lshlrev_b32_e32 v30, 16, v3
	v_mul_f32_e32 v2, 0xbfb8aa3b, v2
	v_exp_f32_e32 v9, v9
	v_and_b32_e32 v3, 0xffff0000, v3
	v_mul_f32_e32 v30, 0xbfb8aa3b, v30
	v_exp_f32_e32 v2, v2
	v_mul_f32_e32 v3, 0xbfb8aa3b, v3
	v_exp_f32_e32 v30, v30
	v_exp_f32_e32 v3, v3
	v_add_f32_e32 v9, 1.0, v9
	v_add_f32_e32 v2, 1.0, v2
	v_add_f32_e32 v30, 1.0, v30
	v_lshlrev_b32_e32 v31, 16, v4
	v_add_f32_e32 v3, 1.0, v3
	v_mul_f32_e32 v31, 0xbfb8aa3b, v31
	v_exp_f32_e32 v31, v31
	s_nop 0
	v_add_f32_e32 v31, 1.0, v31
	v_and_b32_e32 v4, 0xffff0000, v4
	v_mul_f32_e32 v4, 0xbfb8aa3b, v4
	v_exp_f32_e32 v4, v4
	v_rcp_f32_e32 v179, v9
	v_rcp_f32_e32 v9, v2
	v_rcp_f32_e32 v154, v30
	v_rcp_f32_e32 v155, v3
	v_add_f32_e32 v3, 1.0, v4
	v_lshlrev_b32_e32 v32, 16, v5
	v_rcp_f32_e32 v156, v31
	v_mul_f32_e32 v32, 0xbfb8aa3b, v32
	v_exp_f32_e32 v32, v32
	s_nop 0
	v_add_f32_e32 v4, 1.0, v32
	v_and_b32_e32 v5, 0xffff0000, v5
	v_mul_f32_e32 v5, 0xbfb8aa3b, v5
	v_exp_f32_e32 v5, v5
	v_rcp_f32_e32 v157, v3
	v_add_f32_e32 v5, 1.0, v5
	v_rcp_f32_e32 v158, v4
	v_rcp_f32_e32 v159, v5
	v_cvt_pk_f32_fp8_e32 v[2:3], v28
	v_cvt_pk_f32_fp8_sdwa v[4:5], v28 src0_sel:WORD_1
	v_mov_b32_e32 v33, v26
	v_cvt_pk_f32_fp8_e32 v[30:31], v29
	v_mov_b32_e32 v32, v2
	v_pk_mul_f32 v[32:33], v[32:33], v[178:179]
	v_mov_b32_e32 v26, v3
	v_mov_b32_e32 v179, v9
	v_pk_mul_f32 v[2:3], v[26:27], v[178:179]
	v_mov_b32_e32 v179, v154
	v_add_f32_e32 v9, v2, v3
	v_mov_b32_e32 v2, v4
	v_mov_b32_e32 v3, v24
	v_pk_mul_f32 v[2:3], v[2:3], v[178:179]
	v_mov_b32_e32 v24, v5
	v_mov_b32_e32 v179, v155
	v_cvt_pk_f32_fp8_sdwa v[28:29], v29 src0_sel:WORD_1
	v_add_f32_e32 v4, v2, v3
	v_pk_mul_f32 v[2:3], v[24:25], v[178:179]
	v_mov_b32_e32 v179, v156
	v_add_f32_e32 v5, v2, v3
	v_mov_b32_e32 v2, v30
	v_mov_b32_e32 v3, v22
	v_pk_mul_f32 v[2:3], v[2:3], v[178:179]
	v_mov_b32_e32 v22, v31
	v_mov_b32_e32 v179, v157
	v_add_f32_e32 v24, v2, v3
	v_pk_mul_f32 v[2:3], v[22:23], v[178:179]
	v_mov_b32_e32 v179, v158
	v_add_f32_e32 v22, v2, v3
	v_mov_b32_e32 v2, v28
	v_mov_b32_e32 v3, v20
	v_pk_mul_f32 v[2:3], v[2:3], v[178:179]
	v_mov_b32_e32 v20, v29
	v_mov_b32_e32 v179, v159
	v_add_f32_e32 v32, v32, v33
	v_add_f32_e32 v23, v2, v3
	v_pk_mul_f32 v[2:3], v[20:21], v[178:179]
	v_mul_f32_e32 v4, 0x41800000, v4
	v_add_f32_e32 v20, v2, v3
	v_mul_f32_e32 v2, 0x41800000, v32
	v_mul_f32_e32 v3, 0x41800000, v9
	v_med3_f32 v9, v2, s57, v207
	v_med3_f32 v3, v3, s57, v207
	v_mov_b32_e32 v2, v167
	v_cvt_pk_fp8_f32 v2, v9, v3
	v_mul_f32_e32 v3, 0x41800000, v5
	v_med3_f32 v4, v4, s57, v207
	v_med3_f32 v3, v3, s57, v207
	v_cvt_pk_fp8_f32 v2, v4, v3 op_sel:[0,0,1]
	v_mul_f32_e32 v3, 0x41800000, v24
	v_mul_f32_e32 v4, 0x41800000, v22
	v_med3_f32 v9, v3, s57, v207
	v_med3_f32 v4, v4, s57, v207
	v_mov_b32_e32 v3, v167
	v_cvt_pk_fp8_f32 v3, v9, v4
	v_mul_f32_e32 v5, 0x41800000, v23
	v_mul_f32_e32 v4, 0x41800000, v20
	v_med3_f32 v5, v5, s57, v207
	v_med3_f32 v4, v4, s57, v207
	v_cvt_pk_fp8_f32 v3, v5, v4 op_sel:[0,0,1]
	v_lshl_add_u64 v[4:5], s[20:21], 0, v[16:17]
	v_lshl_add_u64 v[16:17], v[4:5], 0, v[6:7]
	v_pk_mul_f32 v[24:25], v[146:147], s[28:29] op_sel_hi:[1,0]
	global_store_dwordx2 v[16:17], v[2:3], off
	s_nop 0
	v_pk_mul_f32 v[20:21], v[150:151], s[28:29] op_sel_hi:[1,0]
	v_pk_mul_f32 v[18:19], v[152:153], s[28:29] op_sel_hi:[1,0]
	v_pk_mul_f32 v[22:23], v[148:149], s[28:29] op_sel_hi:[1,0]
	s_waitcnt vmcnt(11)
	v_mov_b64_e32 v[2:3], v[218:219]
	v_mov_b64_e32 v[4:5], v[220:221]
	v_lshlrev_b32_e32 v9, 16, v2
	v_mul_f32_e32 v9, 0xbfb8aa3b, v9
	v_exp_f32_e32 v9, v9
	v_and_b32_e32 v2, 0xffff0000, v2
	v_mul_f32_e32 v2, 0xbfb8aa3b, v2
	v_exp_f32_e32 v2, v2
	v_add_f32_e32 v9, 1.0, v9
	v_add_f32_e32 v2, 1.0, v2
	v_lshlrev_b32_e32 v27, 16, v3
	v_mul_f32_e32 v27, 0xbfb8aa3b, v27
	v_rcp_f32_e32 v179, v9
	v_exp_f32_e32 v27, v27
	s_nop 0
	v_add_f32_e32 v27, 1.0, v27
	v_and_b32_e32 v3, 0xffff0000, v3
	v_mul_f32_e32 v3, 0xbfb8aa3b, v3
	v_rcp_f32_e32 v9, v2
	v_exp_f32_e32 v3, v3
	s_nop 0
	v_add_f32_e32 v3, 1.0, v3
	v_rcp_f32_e32 v31, v27
	v_lshlrev_b32_e32 v27, 16, v4
	v_mul_f32_e32 v27, 0xbfb8aa3b, v27
	v_exp_f32_e32 v27, v27
	s_nop 0
	v_add_f32_e32 v27, 1.0, v27
	v_and_b32_e32 v4, 0xffff0000, v4
	v_mul_f32_e32 v4, 0xbfb8aa3b, v4
	v_exp_f32_e32 v4, v4
	v_rcp_f32_e32 v30, v3
	v_add_f32_e32 v4, 1.0, v4
	v_rcp_f32_e32 v32, v27
	v_lshlrev_b32_e32 v27, 16, v5
	v_mul_f32_e32 v27, 0xbfb8aa3b, v27
	v_exp_f32_e32 v27, v27
	s_nop 0
	v_add_f32_e32 v26, 1.0, v27
	v_rcp_f32_e32 v33, v4
	v_and_b32_e32 v4, 0xffff0000, v5
	v_mul_f32_e32 v4, 0xbfb8aa3b, v4
	v_exp_f32_e32 v4, v4
	s_nop 0
	v_add_f32_e32 v4, 1.0, v4
	v_rcp_f32_e32 v146, v26
	v_mov_b32_e32 v29, v20
	v_rcp_f32_e32 v147, v4
	s_waitcnt vmcnt(10)
	v_mov_b64_e32 v[14:15], v[240:241]
	v_add_u32_e32 v250, 48, v8
	v_lshl_add_u32 v251, v250, 11, v6
	v_mad_u32_u24 v250, v250, s56, v12
	global_load_dwordx4 v[218:221], v250, s[18:19] offset:256
	global_load_dwordx2 v[240:241], v251, s[16:17] offset:128
	v_cvt_pk_f32_fp8_e32 v[2:3], v14
	v_cvt_pk_f32_fp8_sdwa v[4:5], v14 src0_sel:WORD_1
	v_cvt_pk_f32_fp8_e32 v[26:27], v15
	v_cvt_pk_f32_fp8_sdwa v[14:15], v15 src0_sel:WORD_1
	v_mov_b32_e32 v28, v2
	v_pk_mul_f32 v[28:29], v[28:29], v[178:179]
	v_mov_b32_e32 v20, v3
	v_mov_b32_e32 v179, v9
	v_pk_mul_f32 v[2:3], v[20:21], v[178:179]
	v_mov_b32_e32 v179, v31
	v_add_f32_e32 v9, v2, v3
	v_mov_b32_e32 v2, v4
	v_mov_b32_e32 v3, v18
	v_pk_mul_f32 v[2:3], v[2:3], v[178:179]
	v_mov_b32_e32 v18, v5
	v_mov_b32_e32 v179, v30
	v_add_f32_e32 v4, v2, v3
	v_pk_mul_f32 v[2:3], v[18:19], v[178:179]
	v_mov_b32_e32 v179, v32
	v_add_f32_e32 v5, v2, v3
	v_mov_b32_e32 v2, v26
	v_mov_b32_e32 v3, v24
	v_pk_mul_f32 v[2:3], v[2:3], v[178:179]
	v_mov_b32_e32 v24, v27
	v_mov_b32_e32 v179, v33
	v_add_f32_e32 v18, v2, v3
	v_pk_mul_f32 v[2:3], v[24:25], v[178:179]
	v_mov_b32_e32 v179, v146
	v_add_f32_e32 v19, v2, v3
	v_mov_b32_e32 v2, v14
	v_mov_b32_e32 v3, v22
	v_pk_mul_f32 v[2:3], v[2:3], v[178:179]
	v_mov_b32_e32 v22, v15
	v_mov_b32_e32 v179, v147
	v_add_f32_e32 v28, v28, v29
	v_add_f32_e32 v14, v2, v3
	v_pk_mul_f32 v[2:3], v[22:23], v[178:179]
	v_mul_f32_e32 v4, 0x41800000, v4
	v_add_f32_e32 v15, v2, v3
	v_mul_f32_e32 v2, 0x41800000, v28
	v_mul_f32_e32 v3, 0x41800000, v9
	v_med3_f32 v9, v2, s57, v207
	v_med3_f32 v3, v3, s57, v207
	v_mov_b32_e32 v2, v167
	v_cvt_pk_fp8_f32 v2, v9, v3
	v_mul_f32_e32 v3, 0x41800000, v5
	v_med3_f32 v4, v4, s57, v207
	v_med3_f32 v3, v3, s57, v207
	v_cvt_pk_fp8_f32 v2, v4, v3 op_sel:[0,0,1]
	v_mul_f32_e32 v3, 0x41800000, v18
	v_mul_f32_e32 v4, 0x41800000, v19
	v_med3_f32 v9, v3, s57, v207
	v_med3_f32 v4, v4, s57, v207
	v_mov_b32_e32 v3, v167
	v_cvt_pk_fp8_f32 v3, v9, v4
	v_mul_f32_e32 v5, 0x41800000, v14
	v_mul_f32_e32 v4, 0x41800000, v15
	v_med3_f32 v5, v5, s57, v207
	v_med3_f32 v4, v4, s57, v207
	v_cvt_pk_fp8_f32 v3, v5, v4 op_sel:[0,0,1]
	v_pk_mul_f32 v[28:29], v[138:139], s[28:29] op_sel_hi:[1,0]
	v_pk_mul_f32 v[26:27], v[140:141], s[28:29] op_sel_hi:[1,0]
	v_pk_mul_f32 v[24:25], v[142:143], s[28:29] op_sel_hi:[1,0]
	global_store_dwordx2 v[16:17], v[2:3], off offset:128
	v_add_u32_e32 v16, 16, v8
	v_mad_i64_i32 v[2:3], s[0:1], v16, s56, v[10:11]
	v_lshl_add_u64 v[14:15], v[2:3], 0, v[12:13]
	v_ashrrev_i32_e32 v17, 31, v16
	v_lshlrev_b64 v[18:19], 11, v[16:17]
	v_lshl_add_u64 v[16:17], s[16:17], 0, v[18:19]
	v_lshl_add_u64 v[16:17], v[16:17], 0, v[6:7]
	v_pk_mul_f32 v[22:23], v[144:145], s[28:29] op_sel_hi:[1,0]
	s_waitcnt vmcnt(11)
	v_mov_b64_e32 v[2:3], v[222:223]
	v_mov_b64_e32 v[4:5], v[224:225]
	v_lshlrev_b32_e32 v9, 16, v2
	v_mul_f32_e32 v9, 0xbfb8aa3b, v9
	v_exp_f32_e32 v9, v9
	v_and_b32_e32 v2, 0xffff0000, v2
	v_mul_f32_e32 v2, 0xbfb8aa3b, v2
	v_exp_f32_e32 v2, v2
	v_add_f32_e32 v9, 1.0, v9
	v_add_f32_e32 v2, 1.0, v2
	v_lshlrev_b32_e32 v31, 16, v3
	v_mul_f32_e32 v31, 0xbfb8aa3b, v31
	v_rcp_f32_e32 v179, v9
	v_exp_f32_e32 v31, v31
	s_nop 0
	v_add_f32_e32 v31, 1.0, v31
	v_and_b32_e32 v3, 0xffff0000, v3
	v_mul_f32_e32 v3, 0xbfb8aa3b, v3
	v_rcp_f32_e32 v9, v2
	v_exp_f32_e32 v3, v3
	s_nop 0
	v_add_f32_e32 v3, 1.0, v3
	v_rcp_f32_e32 v139, v31
	v_lshlrev_b32_e32 v31, 16, v4
	v_mul_f32_e32 v31, 0xbfb8aa3b, v31
	v_exp_f32_e32 v31, v31
	s_nop 0
	v_add_f32_e32 v31, 1.0, v31
	v_and_b32_e32 v4, 0xffff0000, v4
	v_mul_f32_e32 v4, 0xbfb8aa3b, v4
	v_exp_f32_e32 v4, v4
	v_rcp_f32_e32 v138, v3
	v_add_f32_e32 v4, 1.0, v4
	v_rcp_f32_e32 v140, v31
	v_lshlrev_b32_e32 v31, 16, v5
	v_mul_f32_e32 v31, 0xbfb8aa3b, v31
	v_exp_f32_e32 v31, v31
	s_nop 0
	v_add_f32_e32 v30, 1.0, v31
	v_rcp_f32_e32 v141, v4
	v_and_b32_e32 v4, 0xffff0000, v5
	v_mul_f32_e32 v4, 0xbfb8aa3b, v4
	v_exp_f32_e32 v4, v4
	s_nop 0
	v_add_f32_e32 v4, 1.0, v4
	v_rcp_f32_e32 v142, v30
	v_mov_b32_e32 v33, v24
	v_rcp_f32_e32 v143, v4
	s_waitcnt vmcnt(10)
	v_mov_b64_e32 v[20:21], v[242:243]
	v_add_u32_e32 v250, 128, v8
	v_lshl_add_u32 v251, v250, 11, v6
	v_mad_u32_u24 v250, v250, s56, v12
	global_load_dwordx4 v[222:225], v250, s[18:19]
	global_load_dwordx2 v[242:243], v251, s[16:17]
	v_cvt_pk_f32_fp8_e32 v[2:3], v20
	v_cvt_pk_f32_fp8_sdwa v[4:5], v20 src0_sel:WORD_1
	v_cvt_pk_f32_fp8_e32 v[30:31], v21
	v_cvt_pk_f32_fp8_sdwa v[20:21], v21 src0_sel:WORD_1
	v_mov_b32_e32 v32, v2
	v_pk_mul_f32 v[32:33], v[32:33], v[178:179]
	v_mov_b32_e32 v24, v3
	v_mov_b32_e32 v179, v9
	v_pk_mul_f32 v[2:3], v[24:25], v[178:179]
	v_mov_b32_e32 v179, v139
	v_add_f32_e32 v9, v2, v3
	v_mov_b32_e32 v2, v4
	v_mov_b32_e32 v3, v22
	v_pk_mul_f32 v[2:3], v[2:3], v[178:179]
	v_mov_b32_e32 v22, v5
	v_mov_b32_e32 v179, v138
	v_add_f32_e32 v4, v2, v3
	v_pk_mul_f32 v[2:3], v[22:23], v[178:179]
	v_mov_b32_e32 v179, v140
	v_add_f32_e32 v5, v2, v3
	v_mov_b32_e32 v2, v30
	v_mov_b32_e32 v3, v28
	v_pk_mul_f32 v[2:3], v[2:3], v[178:179]
	v_mov_b32_e32 v28, v31
	v_mov_b32_e32 v179, v141
	v_add_f32_e32 v22, v2, v3
	v_pk_mul_f32 v[2:3], v[28:29], v[178:179]
	v_mov_b32_e32 v179, v142
	v_add_f32_e32 v23, v2, v3
	v_mov_b32_e32 v2, v20
	v_mov_b32_e32 v3, v26
	v_pk_mul_f32 v[2:3], v[2:3], v[178:179]
	v_mov_b32_e32 v26, v21
	v_mov_b32_e32 v179, v143
	v_add_f32_e32 v32, v32, v33
	v_add_f32_e32 v20, v2, v3
	v_pk_mul_f32 v[2:3], v[26:27], v[178:179]
	v_mul_f32_e32 v4, 0x41800000, v4
	v_add_f32_e32 v21, v2, v3
	v_mul_f32_e32 v2, 0x41800000, v32
	v_mul_f32_e32 v3, 0x41800000, v9
	v_med3_f32 v9, v2, s57, v207
	v_med3_f32 v3, v3, s57, v207
	v_mov_b32_e32 v2, v167
	v_cvt_pk_fp8_f32 v2, v9, v3
	v_mul_f32_e32 v3, 0x41800000, v5
	v_med3_f32 v4, v4, s57, v207
	v_med3_f32 v3, v3, s57, v207
	v_cvt_pk_fp8_f32 v2, v4, v3 op_sel:[0,0,1]
	v_mul_f32_e32 v3, 0x41800000, v22
	v_mul_f32_e32 v4, 0x41800000, v23
	v_med3_f32 v9, v3, s57, v207
	v_med3_f32 v4, v4, s57, v207
	v_mov_b32_e32 v3, v167
	v_cvt_pk_fp8_f32 v3, v9, v4
	v_mul_f32_e32 v5, 0x41800000, v20
	v_mul_f32_e32 v4, 0x41800000, v21
	v_med3_f32 v5, v5, s57, v207
	v_med3_f32 v4, v4, s57, v207
	v_cvt_pk_fp8_f32 v3, v5, v4 op_sel:[0,0,1]
	v_lshl_add_u64 v[4:5], s[20:21], 0, v[18:19]
	v_lshl_add_u64 v[18:19], v[4:5], 0, v[6:7]
	v_pk_mul_f32 v[24:25], v[130:131], s[28:29] op_sel_hi:[1,0]
	global_store_dwordx2 v[18:19], v[2:3], off
	s_nop 0
	v_pk_mul_f32 v[20:21], v[134:135], s[28:29] op_sel_hi:[1,0]
	v_pk_mul_f32 v[16:17], v[136:137], s[28:29] op_sel_hi:[1,0]
	v_pk_mul_f32 v[22:23], v[132:133], s[28:29] op_sel_hi:[1,0]
	s_waitcnt vmcnt(11)
	v_mov_b64_e32 v[2:3], v[226:227]
	v_mov_b64_e32 v[4:5], v[228:229]
	v_lshlrev_b32_e32 v9, 16, v2
	v_mul_f32_e32 v9, 0xbfb8aa3b, v9
	v_exp_f32_e32 v9, v9
	v_and_b32_e32 v2, 0xffff0000, v2
	v_mul_f32_e32 v2, 0xbfb8aa3b, v2
	v_exp_f32_e32 v2, v2
	v_add_f32_e32 v9, 1.0, v9
	v_add_f32_e32 v2, 1.0, v2
	v_lshlrev_b32_e32 v27, 16, v3
	v_mul_f32_e32 v27, 0xbfb8aa3b, v27
	v_rcp_f32_e32 v179, v9
	v_exp_f32_e32 v27, v27
	s_nop 0
	v_add_f32_e32 v27, 1.0, v27
	v_and_b32_e32 v3, 0xffff0000, v3
	v_mul_f32_e32 v3, 0xbfb8aa3b, v3
	v_rcp_f32_e32 v9, v2
	v_exp_f32_e32 v3, v3
	s_nop 0
	v_add_f32_e32 v3, 1.0, v3
	v_rcp_f32_e32 v31, v27
	v_lshlrev_b32_e32 v27, 16, v4
	v_mul_f32_e32 v27, 0xbfb8aa3b, v27
	v_exp_f32_e32 v27, v27
	s_nop 0
	v_add_f32_e32 v27, 1.0, v27
	v_and_b32_e32 v4, 0xffff0000, v4
	v_mul_f32_e32 v4, 0xbfb8aa3b, v4
	v_exp_f32_e32 v4, v4
	v_rcp_f32_e32 v30, v3
	v_add_f32_e32 v4, 1.0, v4
	v_rcp_f32_e32 v32, v27
	v_lshlrev_b32_e32 v27, 16, v5
	v_mul_f32_e32 v27, 0xbfb8aa3b, v27
	v_exp_f32_e32 v27, v27
	s_nop 0
	v_add_f32_e32 v26, 1.0, v27
	v_rcp_f32_e32 v33, v4
	v_and_b32_e32 v4, 0xffff0000, v5
	v_mul_f32_e32 v4, 0xbfb8aa3b, v4
	v_exp_f32_e32 v4, v4
	s_nop 0
	v_add_f32_e32 v4, 1.0, v4
	v_rcp_f32_e32 v130, v26
	v_mov_b32_e32 v29, v20
	v_rcp_f32_e32 v131, v4
	s_waitcnt vmcnt(10)
	v_mov_b64_e32 v[14:15], v[244:245]
	v_add_u32_e32 v250, 128, v8
	v_lshl_add_u32 v251, v250, 11, v6
	v_mad_u32_u24 v250, v250, s56, v12
	global_load_dwordx4 v[226:229], v250, s[18:19] offset:256
	global_load_dwordx2 v[244:245], v251, s[16:17] offset:128
	v_cvt_pk_f32_fp8_e32 v[2:3], v14
	v_cvt_pk_f32_fp8_sdwa v[4:5], v14 src0_sel:WORD_1
	v_cvt_pk_f32_fp8_e32 v[26:27], v15
	v_cvt_pk_f32_fp8_sdwa v[14:15], v15 src0_sel:WORD_1
	v_mov_b32_e32 v28, v2
	v_pk_mul_f32 v[28:29], v[28:29], v[178:179]
	v_mov_b32_e32 v20, v3
	v_mov_b32_e32 v179, v9
	v_pk_mul_f32 v[2:3], v[20:21], v[178:179]
	v_mov_b32_e32 v179, v31
	v_add_f32_e32 v9, v2, v3
	v_mov_b32_e32 v2, v4
	v_mov_b32_e32 v3, v16
	v_pk_mul_f32 v[2:3], v[2:3], v[178:179]
	v_mov_b32_e32 v16, v5
	v_mov_b32_e32 v179, v30
	v_add_f32_e32 v4, v2, v3
	v_pk_mul_f32 v[2:3], v[16:17], v[178:179]
	v_mov_b32_e32 v179, v32
	v_add_f32_e32 v5, v2, v3
	v_mov_b32_e32 v2, v26
	v_mov_b32_e32 v3, v24
	v_pk_mul_f32 v[2:3], v[2:3], v[178:179]
	v_mov_b32_e32 v24, v27
	v_mov_b32_e32 v179, v33
	v_add_f32_e32 v16, v2, v3
	v_pk_mul_f32 v[2:3], v[24:25], v[178:179]
	v_mov_b32_e32 v179, v130
	v_add_f32_e32 v17, v2, v3
	v_mov_b32_e32 v2, v14
	v_mov_b32_e32 v3, v22
	v_pk_mul_f32 v[2:3], v[2:3], v[178:179]
	v_mov_b32_e32 v22, v15
	v_mov_b32_e32 v179, v131
	v_add_f32_e32 v28, v28, v29
	v_add_f32_e32 v14, v2, v3
	v_pk_mul_f32 v[2:3], v[22:23], v[178:179]
	v_mul_f32_e32 v4, 0x41800000, v4
	v_add_f32_e32 v15, v2, v3
	v_mul_f32_e32 v2, 0x41800000, v28
	v_mul_f32_e32 v3, 0x41800000, v9
	v_med3_f32 v9, v2, s57, v207
	v_med3_f32 v3, v3, s57, v207
	v_mov_b32_e32 v2, v167
	v_cvt_pk_fp8_f32 v2, v9, v3
	v_mul_f32_e32 v3, 0x41800000, v5
	v_med3_f32 v4, v4, s57, v207
	v_med3_f32 v3, v3, s57, v207
	v_cvt_pk_fp8_f32 v2, v4, v3 op_sel:[0,0,1]
	v_mul_f32_e32 v3, 0x41800000, v16
	v_mul_f32_e32 v4, 0x41800000, v17
	v_med3_f32 v9, v3, s57, v207
	v_med3_f32 v4, v4, s57, v207
	v_mov_b32_e32 v3, v167
	v_cvt_pk_fp8_f32 v3, v9, v4
	v_mul_f32_e32 v5, 0x41800000, v14
	v_mul_f32_e32 v4, 0x41800000, v15
	v_med3_f32 v5, v5, s57, v207
	v_med3_f32 v4, v4, s57, v207
	v_cvt_pk_fp8_f32 v3, v5, v4 op_sel:[0,0,1]
	v_add_u32_e32 v16, 32, v8
	v_ashrrev_i32_e32 v17, 31, v16
	v_pk_mul_f32 v[28:29], v[122:123], s[28:29] op_sel_hi:[1,0]
	global_store_dwordx2 v[18:19], v[2:3], off offset:128
	v_mad_i64_i32 v[2:3], s[0:1], v16, s56, v[10:11]
	v_lshl_add_u64 v[14:15], v[2:3], 0, v[12:13]
	v_lshlrev_b64 v[18:19], 11, v[16:17]
	v_lshl_add_u64 v[16:17], s[16:17], 0, v[18:19]
	v_lshl_add_u64 v[16:17], v[16:17], 0, v[6:7]
	v_pk_mul_f32 v[26:27], v[124:125], s[28:29] op_sel_hi:[1,0]
	v_pk_mul_f32 v[24:25], v[126:127], s[28:29] op_sel_hi:[1,0]
	v_pk_mul_f32 v[22:23], v[128:129], s[28:29] op_sel_hi:[1,0]
	s_waitcnt vmcnt(11)
	v_mov_b64_e32 v[2:3], v[230:231]
	v_mov_b64_e32 v[4:5], v[232:233]
	v_lshlrev_b32_e32 v9, 16, v2
	v_mul_f32_e32 v9, 0xbfb8aa3b, v9
	v_exp_f32_e32 v9, v9
	v_and_b32_e32 v2, 0xffff0000, v2
	v_mul_f32_e32 v2, 0xbfb8aa3b, v2
	v_exp_f32_e32 v2, v2
	v_add_f32_e32 v9, 1.0, v9
	v_add_f32_e32 v2, 1.0, v2
	v_lshlrev_b32_e32 v31, 16, v3
	v_mul_f32_e32 v31, 0xbfb8aa3b, v31
	v_rcp_f32_e32 v179, v9
	v_exp_f32_e32 v31, v31
	s_nop 0
	v_add_f32_e32 v31, 1.0, v31
	v_and_b32_e32 v3, 0xffff0000, v3
	v_mul_f32_e32 v3, 0xbfb8aa3b, v3
	v_rcp_f32_e32 v9, v2
	v_exp_f32_e32 v3, v3
	s_nop 0
	v_add_f32_e32 v3, 1.0, v3
	v_rcp_f32_e32 v123, v31
	v_lshlrev_b32_e32 v31, 16, v4
	v_mul_f32_e32 v31, 0xbfb8aa3b, v31
	v_exp_f32_e32 v31, v31
	s_nop 0
	v_add_f32_e32 v31, 1.0, v31
	v_and_b32_e32 v4, 0xffff0000, v4
	v_mul_f32_e32 v4, 0xbfb8aa3b, v4
	v_exp_f32_e32 v4, v4
	v_rcp_f32_e32 v122, v3
	v_add_f32_e32 v4, 1.0, v4
	v_rcp_f32_e32 v124, v31
	v_lshlrev_b32_e32 v31, 16, v5
	v_mul_f32_e32 v31, 0xbfb8aa3b, v31
	v_exp_f32_e32 v31, v31
	s_nop 0
	v_add_f32_e32 v30, 1.0, v31
	v_rcp_f32_e32 v125, v4
	v_and_b32_e32 v4, 0xffff0000, v5
	v_mul_f32_e32 v4, 0xbfb8aa3b, v4
	v_exp_f32_e32 v4, v4
	s_nop 0
	v_add_f32_e32 v4, 1.0, v4
	v_rcp_f32_e32 v126, v30
	v_mov_b32_e32 v33, v24
	v_rcp_f32_e32 v127, v4
	s_waitcnt vmcnt(10)
	v_mov_b64_e32 v[20:21], v[246:247]
	v_add_u32_e32 v250, 144, v8
	v_lshl_add_u32 v251, v250, 11, v6
	v_mad_u32_u24 v250, v250, s56, v12
	global_load_dwordx4 v[230:233], v250, s[18:19]
	global_load_dwordx2 v[246:247], v251, s[16:17]
	v_cvt_pk_f32_fp8_e32 v[2:3], v20
	v_cvt_pk_f32_fp8_sdwa v[4:5], v20 src0_sel:WORD_1
	v_cvt_pk_f32_fp8_e32 v[30:31], v21
	v_cvt_pk_f32_fp8_sdwa v[20:21], v21 src0_sel:WORD_1
	v_mov_b32_e32 v32, v2
	v_pk_mul_f32 v[32:33], v[32:33], v[178:179]
	v_mov_b32_e32 v24, v3
	v_mov_b32_e32 v179, v9
	v_pk_mul_f32 v[2:3], v[24:25], v[178:179]
	v_mov_b32_e32 v179, v123
	v_add_f32_e32 v9, v2, v3
	v_mov_b32_e32 v2, v4
	v_mov_b32_e32 v3, v22
	v_pk_mul_f32 v[2:3], v[2:3], v[178:179]
	v_mov_b32_e32 v22, v5
	v_mov_b32_e32 v179, v122
	v_add_f32_e32 v4, v2, v3
	v_pk_mul_f32 v[2:3], v[22:23], v[178:179]
	v_mov_b32_e32 v179, v124
	v_add_f32_e32 v5, v2, v3
	v_mov_b32_e32 v2, v30
	v_mov_b32_e32 v3, v28
	v_pk_mul_f32 v[2:3], v[2:3], v[178:179]
	v_mov_b32_e32 v28, v31
	v_mov_b32_e32 v179, v125
	v_add_f32_e32 v22, v2, v3
	v_pk_mul_f32 v[2:3], v[28:29], v[178:179]
	v_mov_b32_e32 v179, v126
	v_add_f32_e32 v23, v2, v3
	v_mov_b32_e32 v2, v20
	v_mov_b32_e32 v3, v26
	v_pk_mul_f32 v[2:3], v[2:3], v[178:179]
	v_mov_b32_e32 v26, v21
	v_mov_b32_e32 v179, v127
	v_add_f32_e32 v32, v32, v33
	v_add_f32_e32 v20, v2, v3
	v_pk_mul_f32 v[2:3], v[26:27], v[178:179]
	v_mul_f32_e32 v4, 0x41800000, v4
	v_add_f32_e32 v21, v2, v3
	v_mul_f32_e32 v2, 0x41800000, v32
	v_mul_f32_e32 v3, 0x41800000, v9
	v_med3_f32 v9, v2, s57, v207
	v_med3_f32 v3, v3, s57, v207
	v_mov_b32_e32 v2, v167
	v_cvt_pk_fp8_f32 v2, v9, v3
	v_mul_f32_e32 v3, 0x41800000, v5
	v_med3_f32 v4, v4, s57, v207
	v_med3_f32 v3, v3, s57, v207
	v_cvt_pk_fp8_f32 v2, v4, v3 op_sel:[0,0,1]
	v_mul_f32_e32 v3, 0x41800000, v22
	v_mul_f32_e32 v4, 0x41800000, v23
	v_med3_f32 v9, v3, s57, v207
	v_med3_f32 v4, v4, s57, v207
	v_mov_b32_e32 v3, v167
	v_cvt_pk_fp8_f32 v3, v9, v4
	v_mul_f32_e32 v5, 0x41800000, v20
	v_mul_f32_e32 v4, 0x41800000, v21
	v_med3_f32 v5, v5, s57, v207
	v_med3_f32 v4, v4, s57, v207
	v_cvt_pk_fp8_f32 v3, v5, v4 op_sel:[0,0,1]
	v_lshl_add_u64 v[4:5], s[20:21], 0, v[18:19]
	v_lshl_add_u64 v[18:19], v[4:5], 0, v[6:7]
	v_pk_mul_f32 v[24:25], v[114:115], s[28:29] op_sel_hi:[1,0]
	global_store_dwordx2 v[18:19], v[2:3], off
	s_nop 0
	v_pk_mul_f32 v[20:21], v[118:119], s[28:29] op_sel_hi:[1,0]
	v_pk_mul_f32 v[16:17], v[120:121], s[28:29] op_sel_hi:[1,0]
	v_pk_mul_f32 v[22:23], v[116:117], s[28:29] op_sel_hi:[1,0]
	s_waitcnt vmcnt(11)
	v_mov_b64_e32 v[2:3], v[234:235]
	v_mov_b64_e32 v[4:5], v[236:237]
	v_lshlrev_b32_e32 v9, 16, v2
	v_mul_f32_e32 v9, 0xbfb8aa3b, v9
	v_exp_f32_e32 v9, v9
	v_and_b32_e32 v2, 0xffff0000, v2
	v_mul_f32_e32 v2, 0xbfb8aa3b, v2
	v_exp_f32_e32 v2, v2
	v_add_f32_e32 v9, 1.0, v9
	v_add_f32_e32 v2, 1.0, v2
	v_lshlrev_b32_e32 v27, 16, v3
	v_mul_f32_e32 v27, 0xbfb8aa3b, v27
	v_rcp_f32_e32 v179, v9
	v_exp_f32_e32 v27, v27
	s_nop 0
	v_add_f32_e32 v27, 1.0, v27
	v_and_b32_e32 v3, 0xffff0000, v3
	v_mul_f32_e32 v3, 0xbfb8aa3b, v3
	v_rcp_f32_e32 v9, v2
	v_exp_f32_e32 v3, v3
	s_nop 0
	v_add_f32_e32 v3, 1.0, v3
	v_rcp_f32_e32 v31, v27
	v_lshlrev_b32_e32 v27, 16, v4
	v_mul_f32_e32 v27, 0xbfb8aa3b, v27
	v_exp_f32_e32 v27, v27
	s_nop 0
	v_add_f32_e32 v27, 1.0, v27
	v_and_b32_e32 v4, 0xffff0000, v4
	v_mul_f32_e32 v4, 0xbfb8aa3b, v4
	v_exp_f32_e32 v4, v4
	v_rcp_f32_e32 v30, v3
	v_add_f32_e32 v4, 1.0, v4
	v_rcp_f32_e32 v32, v27
	v_lshlrev_b32_e32 v27, 16, v5
	v_mul_f32_e32 v27, 0xbfb8aa3b, v27
	v_exp_f32_e32 v27, v27
	s_nop 0
	v_add_f32_e32 v26, 1.0, v27
	v_rcp_f32_e32 v33, v4
	v_and_b32_e32 v4, 0xffff0000, v5
	v_mul_f32_e32 v4, 0xbfb8aa3b, v4
	v_exp_f32_e32 v4, v4
	s_nop 0
	v_add_f32_e32 v4, 1.0, v4
	v_rcp_f32_e32 v114, v26
	v_mov_b32_e32 v29, v20
	v_rcp_f32_e32 v115, v4
	s_waitcnt vmcnt(10)
	v_mov_b64_e32 v[14:15], v[248:249]
	v_add_u32_e32 v250, 144, v8
	v_lshl_add_u32 v251, v250, 11, v6
	v_mad_u32_u24 v250, v250, s56, v12
	global_load_dwordx4 v[234:237], v250, s[18:19] offset:256
	global_load_dwordx2 v[248:249], v251, s[16:17] offset:128
	v_cvt_pk_f32_fp8_e32 v[2:3], v14
	v_cvt_pk_f32_fp8_sdwa v[4:5], v14 src0_sel:WORD_1
	v_cvt_pk_f32_fp8_e32 v[26:27], v15
	v_cvt_pk_f32_fp8_sdwa v[14:15], v15 src0_sel:WORD_1
	v_mov_b32_e32 v28, v2
	v_pk_mul_f32 v[28:29], v[28:29], v[178:179]
	v_mov_b32_e32 v20, v3
	v_mov_b32_e32 v179, v9
	v_pk_mul_f32 v[2:3], v[20:21], v[178:179]
	v_mov_b32_e32 v179, v31
	v_add_f32_e32 v9, v2, v3
	v_mov_b32_e32 v2, v4
	v_mov_b32_e32 v3, v16
	v_pk_mul_f32 v[2:3], v[2:3], v[178:179]
	v_mov_b32_e32 v16, v5
	v_mov_b32_e32 v179, v30
	v_add_f32_e32 v4, v2, v3
	v_pk_mul_f32 v[2:3], v[16:17], v[178:179]
	v_mov_b32_e32 v179, v32
	v_add_f32_e32 v5, v2, v3
	v_mov_b32_e32 v2, v26
	v_mov_b32_e32 v3, v24
	v_pk_mul_f32 v[2:3], v[2:3], v[178:179]
	v_mov_b32_e32 v24, v27
	v_mov_b32_e32 v179, v33
	v_add_f32_e32 v16, v2, v3
	v_pk_mul_f32 v[2:3], v[24:25], v[178:179]
	v_mov_b32_e32 v179, v114
	v_add_f32_e32 v17, v2, v3
	v_mov_b32_e32 v2, v14
	v_mov_b32_e32 v3, v22
	v_pk_mul_f32 v[2:3], v[2:3], v[178:179]
	v_mov_b32_e32 v22, v15
	v_mov_b32_e32 v179, v115
	v_add_f32_e32 v28, v28, v29
	v_add_f32_e32 v14, v2, v3
	v_pk_mul_f32 v[2:3], v[22:23], v[178:179]
	v_mul_f32_e32 v4, 0x41800000, v4
	v_add_f32_e32 v15, v2, v3
	v_mul_f32_e32 v2, 0x41800000, v28
	v_mul_f32_e32 v3, 0x41800000, v9
	v_med3_f32 v9, v2, s57, v207
	v_med3_f32 v3, v3, s57, v207
	v_mov_b32_e32 v2, v167
	v_cvt_pk_fp8_f32 v2, v9, v3
	v_mul_f32_e32 v3, 0x41800000, v5
	v_med3_f32 v4, v4, s57, v207
	v_med3_f32 v3, v3, s57, v207
	v_cvt_pk_fp8_f32 v2, v4, v3 op_sel:[0,0,1]
	v_mul_f32_e32 v3, 0x41800000, v16
	v_mul_f32_e32 v4, 0x41800000, v17
	v_med3_f32 v9, v3, s57, v207
	v_med3_f32 v4, v4, s57, v207
	v_mov_b32_e32 v3, v167
	v_cvt_pk_fp8_f32 v3, v9, v4
	v_mul_f32_e32 v5, 0x41800000, v14
	v_mul_f32_e32 v4, 0x41800000, v15
	v_med3_f32 v5, v5, s57, v207
	v_med3_f32 v4, v4, s57, v207
	v_cvt_pk_fp8_f32 v3, v5, v4 op_sel:[0,0,1]
	v_add_u32_e32 v16, 48, v8
	v_ashrrev_i32_e32 v17, 31, v16
	v_pk_mul_f32 v[28:29], v[106:107], s[28:29] op_sel_hi:[1,0]
	global_store_dwordx2 v[18:19], v[2:3], off offset:128
	v_mad_i64_i32 v[2:3], s[0:1], v16, s56, v[10:11]
	v_lshl_add_u64 v[14:15], v[2:3], 0, v[12:13]
	v_lshlrev_b64 v[18:19], 11, v[16:17]
	v_lshl_add_u64 v[16:17], s[16:17], 0, v[18:19]
	v_lshl_add_u64 v[16:17], v[16:17], 0, v[6:7]
	v_pk_mul_f32 v[26:27], v[108:109], s[28:29] op_sel_hi:[1,0]
	v_pk_mul_f32 v[24:25], v[110:111], s[28:29] op_sel_hi:[1,0]
	v_pk_mul_f32 v[22:23], v[112:113], s[28:29] op_sel_hi:[1,0]
	s_waitcnt vmcnt(11)
	v_mov_b64_e32 v[2:3], v[214:215]
	v_mov_b64_e32 v[4:5], v[216:217]
	v_lshlrev_b32_e32 v9, 16, v2
	v_mul_f32_e32 v9, 0xbfb8aa3b, v9
	v_exp_f32_e32 v9, v9
	v_and_b32_e32 v2, 0xffff0000, v2
	v_mul_f32_e32 v2, 0xbfb8aa3b, v2
	v_exp_f32_e32 v2, v2
	v_add_f32_e32 v9, 1.0, v9
	v_add_f32_e32 v2, 1.0, v2
	v_lshlrev_b32_e32 v31, 16, v3
	v_mul_f32_e32 v31, 0xbfb8aa3b, v31
	v_rcp_f32_e32 v179, v9
	v_exp_f32_e32 v31, v31
	s_nop 0
	v_add_f32_e32 v31, 1.0, v31
	v_and_b32_e32 v3, 0xffff0000, v3
	v_mul_f32_e32 v3, 0xbfb8aa3b, v3
	v_rcp_f32_e32 v9, v2
	v_exp_f32_e32 v3, v3
	s_nop 0
	v_add_f32_e32 v3, 1.0, v3
	v_rcp_f32_e32 v107, v31
	v_lshlrev_b32_e32 v31, 16, v4
	v_mul_f32_e32 v31, 0xbfb8aa3b, v31
	v_exp_f32_e32 v31, v31
	s_nop 0
	v_add_f32_e32 v31, 1.0, v31
	v_and_b32_e32 v4, 0xffff0000, v4
	v_mul_f32_e32 v4, 0xbfb8aa3b, v4
	v_exp_f32_e32 v4, v4
	v_rcp_f32_e32 v106, v3
	v_add_f32_e32 v4, 1.0, v4
	v_rcp_f32_e32 v108, v31
	v_lshlrev_b32_e32 v31, 16, v5
	v_mul_f32_e32 v31, 0xbfb8aa3b, v31
	v_exp_f32_e32 v31, v31
	s_nop 0
	v_add_f32_e32 v30, 1.0, v31
	v_rcp_f32_e32 v109, v4
	v_and_b32_e32 v4, 0xffff0000, v5
	v_mul_f32_e32 v4, 0xbfb8aa3b, v4
	v_exp_f32_e32 v4, v4
	s_nop 0
	v_add_f32_e32 v4, 1.0, v4
	v_rcp_f32_e32 v110, v30
	v_mov_b32_e32 v33, v24
	v_rcp_f32_e32 v111, v4
	s_waitcnt vmcnt(10)
	v_mov_b64_e32 v[20:21], v[238:239]
	v_add_u32_e32 v250, 160, v8
	v_lshl_add_u32 v251, v250, 11, v6
	v_mad_u32_u24 v250, v250, s56, v12
	global_load_dwordx4 v[214:217], v250, s[18:19]
	global_load_dwordx2 v[238:239], v251, s[16:17]
	v_cvt_pk_f32_fp8_e32 v[2:3], v20
	v_cvt_pk_f32_fp8_sdwa v[4:5], v20 src0_sel:WORD_1
	v_cvt_pk_f32_fp8_e32 v[30:31], v21
	v_cvt_pk_f32_fp8_sdwa v[20:21], v21 src0_sel:WORD_1
	v_mov_b32_e32 v32, v2
	v_pk_mul_f32 v[32:33], v[32:33], v[178:179]
	v_mov_b32_e32 v24, v3
	v_mov_b32_e32 v179, v9
	v_pk_mul_f32 v[2:3], v[24:25], v[178:179]
	v_mov_b32_e32 v179, v107
	v_add_f32_e32 v9, v2, v3
	v_mov_b32_e32 v2, v4
	v_mov_b32_e32 v3, v22
	v_pk_mul_f32 v[2:3], v[2:3], v[178:179]
	v_mov_b32_e32 v22, v5
	v_mov_b32_e32 v179, v106
	v_add_f32_e32 v4, v2, v3
	v_pk_mul_f32 v[2:3], v[22:23], v[178:179]
	v_mov_b32_e32 v179, v108
	v_add_f32_e32 v5, v2, v3
	v_mov_b32_e32 v2, v30
	v_mov_b32_e32 v3, v28
	v_pk_mul_f32 v[2:3], v[2:3], v[178:179]
	v_mov_b32_e32 v28, v31
	v_mov_b32_e32 v179, v109
	v_add_f32_e32 v22, v2, v3
	v_pk_mul_f32 v[2:3], v[28:29], v[178:179]
	v_mov_b32_e32 v179, v110
	v_add_f32_e32 v23, v2, v3
	v_mov_b32_e32 v2, v20
	v_mov_b32_e32 v3, v26
	v_pk_mul_f32 v[2:3], v[2:3], v[178:179]
	v_mov_b32_e32 v26, v21
	v_mov_b32_e32 v179, v111
	v_add_f32_e32 v32, v32, v33
	v_add_f32_e32 v20, v2, v3
	v_pk_mul_f32 v[2:3], v[26:27], v[178:179]
	v_mul_f32_e32 v4, 0x41800000, v4
	v_add_f32_e32 v21, v2, v3
	v_mul_f32_e32 v2, 0x41800000, v32
	v_mul_f32_e32 v3, 0x41800000, v9
	v_med3_f32 v9, v2, s57, v207
	v_med3_f32 v3, v3, s57, v207
	v_mov_b32_e32 v2, v167
	v_cvt_pk_fp8_f32 v2, v9, v3
	v_mul_f32_e32 v3, 0x41800000, v5
	v_med3_f32 v4, v4, s57, v207
	v_med3_f32 v3, v3, s57, v207
	v_cvt_pk_fp8_f32 v2, v4, v3 op_sel:[0,0,1]
	v_mul_f32_e32 v3, 0x41800000, v22
	v_mul_f32_e32 v4, 0x41800000, v23
	v_med3_f32 v9, v3, s57, v207
	v_med3_f32 v4, v4, s57, v207
	v_mov_b32_e32 v3, v167
	v_cvt_pk_fp8_f32 v3, v9, v4
	v_mul_f32_e32 v5, 0x41800000, v20
	v_mul_f32_e32 v4, 0x41800000, v21
	v_med3_f32 v5, v5, s57, v207
	v_med3_f32 v4, v4, s57, v207
	v_cvt_pk_fp8_f32 v3, v5, v4 op_sel:[0,0,1]
	v_lshl_add_u64 v[4:5], s[20:21], 0, v[18:19]
	v_lshl_add_u64 v[18:19], v[4:5], 0, v[6:7]
	v_pk_mul_f32 v[24:25], v[98:99], s[28:29] op_sel_hi:[1,0]
	global_store_dwordx2 v[18:19], v[2:3], off
	s_nop 0
	v_pk_mul_f32 v[20:21], v[102:103], s[28:29] op_sel_hi:[1,0]
	v_pk_mul_f32 v[16:17], v[104:105], s[28:29] op_sel_hi:[1,0]
	v_pk_mul_f32 v[22:23], v[100:101], s[28:29] op_sel_hi:[1,0]
	s_waitcnt vmcnt(11)
	v_mov_b64_e32 v[2:3], v[218:219]
	v_mov_b64_e32 v[4:5], v[220:221]
	v_lshlrev_b32_e32 v9, 16, v2
	v_mul_f32_e32 v9, 0xbfb8aa3b, v9
	v_exp_f32_e32 v9, v9
	v_and_b32_e32 v2, 0xffff0000, v2
	v_mul_f32_e32 v2, 0xbfb8aa3b, v2
	v_exp_f32_e32 v2, v2
	v_add_f32_e32 v9, 1.0, v9
	v_add_f32_e32 v2, 1.0, v2
	v_lshlrev_b32_e32 v27, 16, v3
	v_mul_f32_e32 v27, 0xbfb8aa3b, v27
	v_rcp_f32_e32 v179, v9
	v_exp_f32_e32 v27, v27
	s_nop 0
	v_add_f32_e32 v27, 1.0, v27
	v_and_b32_e32 v3, 0xffff0000, v3
	v_mul_f32_e32 v3, 0xbfb8aa3b, v3
	v_rcp_f32_e32 v9, v2
	v_exp_f32_e32 v3, v3
	s_nop 0
	v_add_f32_e32 v3, 1.0, v3
	v_rcp_f32_e32 v31, v27
	v_lshlrev_b32_e32 v27, 16, v4
	v_mul_f32_e32 v27, 0xbfb8aa3b, v27
	v_exp_f32_e32 v27, v27
	s_nop 0
	v_add_f32_e32 v27, 1.0, v27
	v_and_b32_e32 v4, 0xffff0000, v4
	v_mul_f32_e32 v4, 0xbfb8aa3b, v4
	v_exp_f32_e32 v4, v4
	v_rcp_f32_e32 v30, v3
	v_add_f32_e32 v4, 1.0, v4
	v_rcp_f32_e32 v32, v27
	v_lshlrev_b32_e32 v27, 16, v5
	v_mul_f32_e32 v27, 0xbfb8aa3b, v27
	v_exp_f32_e32 v27, v27
	s_nop 0
	v_add_f32_e32 v26, 1.0, v27
	v_rcp_f32_e32 v33, v4
	v_and_b32_e32 v4, 0xffff0000, v5
	v_mul_f32_e32 v4, 0xbfb8aa3b, v4
	v_exp_f32_e32 v4, v4
	s_nop 0
	v_add_f32_e32 v4, 1.0, v4
	v_rcp_f32_e32 v98, v26
	v_mov_b32_e32 v29, v20
	v_rcp_f32_e32 v99, v4
	s_waitcnt vmcnt(10)
	v_mov_b64_e32 v[14:15], v[240:241]
	v_add_u32_e32 v250, 160, v8
	v_lshl_add_u32 v251, v250, 11, v6
	v_mad_u32_u24 v250, v250, s56, v12
	global_load_dwordx4 v[218:221], v250, s[18:19] offset:256
	global_load_dwordx2 v[240:241], v251, s[16:17] offset:128
	v_cvt_pk_f32_fp8_e32 v[2:3], v14
	v_cvt_pk_f32_fp8_sdwa v[4:5], v14 src0_sel:WORD_1
	v_cvt_pk_f32_fp8_e32 v[26:27], v15
	v_cvt_pk_f32_fp8_sdwa v[14:15], v15 src0_sel:WORD_1
	v_mov_b32_e32 v28, v2
	v_pk_mul_f32 v[28:29], v[28:29], v[178:179]
	v_mov_b32_e32 v20, v3
	v_mov_b32_e32 v179, v9
	v_pk_mul_f32 v[2:3], v[20:21], v[178:179]
	v_mov_b32_e32 v179, v31
	v_add_f32_e32 v9, v2, v3
	v_mov_b32_e32 v2, v4
	v_mov_b32_e32 v3, v16
	v_pk_mul_f32 v[2:3], v[2:3], v[178:179]
	v_mov_b32_e32 v16, v5
	v_mov_b32_e32 v179, v30
	v_add_f32_e32 v4, v2, v3
	v_pk_mul_f32 v[2:3], v[16:17], v[178:179]
	v_mov_b32_e32 v179, v32
	v_add_f32_e32 v5, v2, v3
	v_mov_b32_e32 v2, v26
	v_mov_b32_e32 v3, v24
	v_pk_mul_f32 v[2:3], v[2:3], v[178:179]
	v_mov_b32_e32 v24, v27
	v_mov_b32_e32 v179, v33
	v_add_f32_e32 v16, v2, v3
	v_pk_mul_f32 v[2:3], v[24:25], v[178:179]
	v_mov_b32_e32 v179, v98
	v_add_f32_e32 v17, v2, v3
	v_mov_b32_e32 v2, v14
	v_mov_b32_e32 v3, v22
	v_pk_mul_f32 v[2:3], v[2:3], v[178:179]
	v_mov_b32_e32 v22, v15
	v_mov_b32_e32 v179, v99
	v_add_f32_e32 v28, v28, v29
	v_add_f32_e32 v14, v2, v3
	v_pk_mul_f32 v[2:3], v[22:23], v[178:179]
	v_mul_f32_e32 v4, 0x41800000, v4
	v_add_f32_e32 v15, v2, v3
	v_mul_f32_e32 v2, 0x41800000, v28
	v_mul_f32_e32 v3, 0x41800000, v9
	v_med3_f32 v9, v2, s57, v207
	v_med3_f32 v3, v3, s57, v207
	v_mov_b32_e32 v2, v167
	v_cvt_pk_fp8_f32 v2, v9, v3
	v_mul_f32_e32 v3, 0x41800000, v5
	v_med3_f32 v4, v4, s57, v207
	v_med3_f32 v3, v3, s57, v207
	v_cvt_pk_fp8_f32 v2, v4, v3 op_sel:[0,0,1]
	v_mul_f32_e32 v3, 0x41800000, v16
	v_mul_f32_e32 v4, 0x41800000, v17
	v_med3_f32 v9, v3, s57, v207
	v_med3_f32 v4, v4, s57, v207
	v_mov_b32_e32 v3, v167
	v_cvt_pk_fp8_f32 v3, v9, v4
	v_mul_f32_e32 v5, 0x41800000, v14
	v_mul_f32_e32 v4, 0x41800000, v15
	v_med3_f32 v5, v5, s57, v207
	v_med3_f32 v4, v4, s57, v207
	v_cvt_pk_fp8_f32 v3, v5, v4 op_sel:[0,0,1]
	v_add_u32_e32 v16, 0x80, v8
	v_ashrrev_i32_e32 v17, 31, v16
	v_pk_mul_f32 v[28:29], v[90:91], s[28:29] op_sel_hi:[1,0]
	global_store_dwordx2 v[18:19], v[2:3], off offset:128
	v_mad_i64_i32 v[2:3], s[0:1], v16, s56, v[10:11]
	v_lshl_add_u64 v[14:15], v[2:3], 0, v[12:13]
	v_lshlrev_b64 v[18:19], 11, v[16:17]
	v_lshl_add_u64 v[16:17], s[16:17], 0, v[18:19]
	v_lshl_add_u64 v[16:17], v[16:17], 0, v[6:7]
	v_pk_mul_f32 v[26:27], v[92:93], s[28:29] op_sel_hi:[1,0]
	v_pk_mul_f32 v[24:25], v[94:95], s[28:29] op_sel_hi:[1,0]
	v_pk_mul_f32 v[22:23], v[96:97], s[28:29] op_sel_hi:[1,0]
	s_waitcnt vmcnt(11)
	v_mov_b64_e32 v[2:3], v[222:223]
	v_mov_b64_e32 v[4:5], v[224:225]
	v_lshlrev_b32_e32 v9, 16, v2
	v_mul_f32_e32 v9, 0xbfb8aa3b, v9
	v_exp_f32_e32 v9, v9
	v_and_b32_e32 v2, 0xffff0000, v2
	v_mul_f32_e32 v2, 0xbfb8aa3b, v2
	v_exp_f32_e32 v2, v2
	v_add_f32_e32 v9, 1.0, v9
	v_add_f32_e32 v2, 1.0, v2
	v_lshlrev_b32_e32 v31, 16, v3
	v_mul_f32_e32 v31, 0xbfb8aa3b, v31
	v_rcp_f32_e32 v179, v9
	v_exp_f32_e32 v31, v31
	s_nop 0
	v_add_f32_e32 v31, 1.0, v31
	v_and_b32_e32 v3, 0xffff0000, v3
	v_mul_f32_e32 v3, 0xbfb8aa3b, v3
	v_rcp_f32_e32 v9, v2
	v_exp_f32_e32 v3, v3
	s_nop 0
	v_add_f32_e32 v3, 1.0, v3
	v_rcp_f32_e32 v91, v31
	v_lshlrev_b32_e32 v31, 16, v4
	v_mul_f32_e32 v31, 0xbfb8aa3b, v31
	v_exp_f32_e32 v31, v31
	s_nop 0
	v_add_f32_e32 v31, 1.0, v31
	v_and_b32_e32 v4, 0xffff0000, v4
	v_mul_f32_e32 v4, 0xbfb8aa3b, v4
	v_exp_f32_e32 v4, v4
	v_rcp_f32_e32 v90, v3
	v_add_f32_e32 v4, 1.0, v4
	v_rcp_f32_e32 v92, v31
	v_lshlrev_b32_e32 v31, 16, v5
	v_mul_f32_e32 v31, 0xbfb8aa3b, v31
	v_exp_f32_e32 v31, v31
	s_nop 0
	v_add_f32_e32 v30, 1.0, v31
	v_rcp_f32_e32 v93, v4
	v_and_b32_e32 v4, 0xffff0000, v5
	v_mul_f32_e32 v4, 0xbfb8aa3b, v4
	v_exp_f32_e32 v4, v4
	s_nop 0
	v_add_f32_e32 v4, 1.0, v4
	v_rcp_f32_e32 v94, v30
	v_mov_b32_e32 v33, v24
	v_rcp_f32_e32 v95, v4
	s_waitcnt vmcnt(10)
	v_mov_b64_e32 v[20:21], v[242:243]
	v_add_u32_e32 v250, 176, v8
	v_lshl_add_u32 v251, v250, 11, v6
	v_mad_u32_u24 v250, v250, s56, v12
	global_load_dwordx4 v[222:225], v250, s[18:19]
	global_load_dwordx2 v[242:243], v251, s[16:17]
	v_cvt_pk_f32_fp8_e32 v[2:3], v20
	v_cvt_pk_f32_fp8_sdwa v[4:5], v20 src0_sel:WORD_1
	v_cvt_pk_f32_fp8_e32 v[30:31], v21
	v_cvt_pk_f32_fp8_sdwa v[20:21], v21 src0_sel:WORD_1
	v_mov_b32_e32 v32, v2
	v_pk_mul_f32 v[32:33], v[32:33], v[178:179]
	v_mov_b32_e32 v24, v3
	v_mov_b32_e32 v179, v9
	v_pk_mul_f32 v[2:3], v[24:25], v[178:179]
	v_mov_b32_e32 v179, v91
	v_add_f32_e32 v9, v2, v3
	v_mov_b32_e32 v2, v4
	v_mov_b32_e32 v3, v22
	v_pk_mul_f32 v[2:3], v[2:3], v[178:179]
	v_mov_b32_e32 v22, v5
	v_mov_b32_e32 v179, v90
	v_add_f32_e32 v4, v2, v3
	v_pk_mul_f32 v[2:3], v[22:23], v[178:179]
	v_mov_b32_e32 v179, v92
	v_add_f32_e32 v5, v2, v3
	v_mov_b32_e32 v2, v30
	v_mov_b32_e32 v3, v28
	v_pk_mul_f32 v[2:3], v[2:3], v[178:179]
	v_mov_b32_e32 v28, v31
	v_mov_b32_e32 v179, v93
	v_add_f32_e32 v22, v2, v3
	v_pk_mul_f32 v[2:3], v[28:29], v[178:179]
	v_mov_b32_e32 v179, v94
	v_add_f32_e32 v23, v2, v3
	v_mov_b32_e32 v2, v20
	v_mov_b32_e32 v3, v26
	v_pk_mul_f32 v[2:3], v[2:3], v[178:179]
	v_mov_b32_e32 v26, v21
	v_mov_b32_e32 v179, v95
	v_add_f32_e32 v32, v32, v33
	v_add_f32_e32 v20, v2, v3
	v_pk_mul_f32 v[2:3], v[26:27], v[178:179]
	v_mul_f32_e32 v4, 0x41800000, v4
	v_add_f32_e32 v21, v2, v3
	v_mul_f32_e32 v2, 0x41800000, v32
	v_mul_f32_e32 v3, 0x41800000, v9
	v_med3_f32 v9, v2, s57, v207
	v_med3_f32 v3, v3, s57, v207
	v_mov_b32_e32 v2, v167
	v_cvt_pk_fp8_f32 v2, v9, v3
	v_mul_f32_e32 v3, 0x41800000, v5
	v_med3_f32 v4, v4, s57, v207
	v_med3_f32 v3, v3, s57, v207
	v_cvt_pk_fp8_f32 v2, v4, v3 op_sel:[0,0,1]
	v_mul_f32_e32 v3, 0x41800000, v22
	v_mul_f32_e32 v4, 0x41800000, v23
	v_med3_f32 v9, v3, s57, v207
	v_med3_f32 v4, v4, s57, v207
	v_mov_b32_e32 v3, v167
	v_cvt_pk_fp8_f32 v3, v9, v4
	v_mul_f32_e32 v5, 0x41800000, v20
	v_mul_f32_e32 v4, 0x41800000, v21
	v_med3_f32 v5, v5, s57, v207
	v_med3_f32 v4, v4, s57, v207
	v_cvt_pk_fp8_f32 v3, v5, v4 op_sel:[0,0,1]
	v_lshl_add_u64 v[4:5], s[20:21], 0, v[18:19]
	v_lshl_add_u64 v[18:19], v[4:5], 0, v[6:7]
	v_pk_mul_f32 v[24:25], v[82:83], s[28:29] op_sel_hi:[1,0]
	global_store_dwordx2 v[18:19], v[2:3], off
	s_nop 0
	v_pk_mul_f32 v[20:21], v[86:87], s[28:29] op_sel_hi:[1,0]
	v_pk_mul_f32 v[16:17], v[88:89], s[28:29] op_sel_hi:[1,0]
	v_pk_mul_f32 v[22:23], v[84:85], s[28:29] op_sel_hi:[1,0]
	s_waitcnt vmcnt(11)
	v_mov_b64_e32 v[2:3], v[226:227]
	v_mov_b64_e32 v[4:5], v[228:229]
	v_lshlrev_b32_e32 v9, 16, v2
	v_mul_f32_e32 v9, 0xbfb8aa3b, v9
	v_exp_f32_e32 v9, v9
	v_and_b32_e32 v2, 0xffff0000, v2
	v_mul_f32_e32 v2, 0xbfb8aa3b, v2
	v_exp_f32_e32 v2, v2
	v_add_f32_e32 v9, 1.0, v9
	v_add_f32_e32 v2, 1.0, v2
	v_lshlrev_b32_e32 v27, 16, v3
	v_mul_f32_e32 v27, 0xbfb8aa3b, v27
	v_rcp_f32_e32 v179, v9
	v_exp_f32_e32 v27, v27
	s_nop 0
	v_add_f32_e32 v27, 1.0, v27
	v_and_b32_e32 v3, 0xffff0000, v3
	v_mul_f32_e32 v3, 0xbfb8aa3b, v3
	v_rcp_f32_e32 v9, v2
	v_exp_f32_e32 v3, v3
	s_nop 0
	v_add_f32_e32 v3, 1.0, v3
	v_rcp_f32_e32 v31, v27
	v_lshlrev_b32_e32 v27, 16, v4
	v_mul_f32_e32 v27, 0xbfb8aa3b, v27
	v_exp_f32_e32 v27, v27
	s_nop 0
	v_add_f32_e32 v27, 1.0, v27
	v_and_b32_e32 v4, 0xffff0000, v4
	v_mul_f32_e32 v4, 0xbfb8aa3b, v4
	v_exp_f32_e32 v4, v4
	v_rcp_f32_e32 v30, v3
	v_add_f32_e32 v4, 1.0, v4
	v_rcp_f32_e32 v32, v27
	v_lshlrev_b32_e32 v27, 16, v5
	v_mul_f32_e32 v27, 0xbfb8aa3b, v27
	v_exp_f32_e32 v27, v27
	s_nop 0
	v_add_f32_e32 v26, 1.0, v27
	v_rcp_f32_e32 v33, v4
	v_and_b32_e32 v4, 0xffff0000, v5
	v_mul_f32_e32 v4, 0xbfb8aa3b, v4
	v_exp_f32_e32 v4, v4
	s_nop 0
	v_add_f32_e32 v4, 1.0, v4
	v_rcp_f32_e32 v82, v26
	v_mov_b32_e32 v29, v20
	v_rcp_f32_e32 v83, v4
	s_waitcnt vmcnt(10)
	v_mov_b64_e32 v[14:15], v[244:245]
	v_add_u32_e32 v250, 176, v8
	v_lshl_add_u32 v251, v250, 11, v6
	v_mad_u32_u24 v250, v250, s56, v12
	global_load_dwordx4 v[226:229], v250, s[18:19] offset:256
	global_load_dwordx2 v[244:245], v251, s[16:17] offset:128
	v_cvt_pk_f32_fp8_e32 v[2:3], v14
	v_cvt_pk_f32_fp8_sdwa v[4:5], v14 src0_sel:WORD_1
	v_cvt_pk_f32_fp8_e32 v[26:27], v15
	v_cvt_pk_f32_fp8_sdwa v[14:15], v15 src0_sel:WORD_1
	v_mov_b32_e32 v28, v2
	v_pk_mul_f32 v[28:29], v[28:29], v[178:179]
	v_mov_b32_e32 v20, v3
	v_mov_b32_e32 v179, v9
	v_pk_mul_f32 v[2:3], v[20:21], v[178:179]
	v_mov_b32_e32 v179, v31
	v_add_f32_e32 v9, v2, v3
	v_mov_b32_e32 v2, v4
	v_mov_b32_e32 v3, v16
	v_pk_mul_f32 v[2:3], v[2:3], v[178:179]
	v_mov_b32_e32 v16, v5
	v_mov_b32_e32 v179, v30
	v_add_f32_e32 v4, v2, v3
	v_pk_mul_f32 v[2:3], v[16:17], v[178:179]
	v_mov_b32_e32 v179, v32
	v_add_f32_e32 v5, v2, v3
	v_mov_b32_e32 v2, v26
	v_mov_b32_e32 v3, v24
	v_pk_mul_f32 v[2:3], v[2:3], v[178:179]
	v_mov_b32_e32 v24, v27
	v_mov_b32_e32 v179, v33
	v_add_f32_e32 v16, v2, v3
	v_pk_mul_f32 v[2:3], v[24:25], v[178:179]
	v_mov_b32_e32 v179, v82
	v_add_f32_e32 v17, v2, v3
	v_mov_b32_e32 v2, v14
	v_mov_b32_e32 v3, v22
	v_pk_mul_f32 v[2:3], v[2:3], v[178:179]
	v_mov_b32_e32 v22, v15
	v_mov_b32_e32 v179, v83
	v_add_f32_e32 v28, v28, v29
	v_add_f32_e32 v14, v2, v3
	v_pk_mul_f32 v[2:3], v[22:23], v[178:179]
	v_mul_f32_e32 v4, 0x41800000, v4
	v_add_f32_e32 v15, v2, v3
	v_mul_f32_e32 v2, 0x41800000, v28
	v_mul_f32_e32 v3, 0x41800000, v9
	v_med3_f32 v9, v2, s57, v207
	v_med3_f32 v3, v3, s57, v207
	v_mov_b32_e32 v2, v167
	v_cvt_pk_fp8_f32 v2, v9, v3
	v_mul_f32_e32 v3, 0x41800000, v5
	v_med3_f32 v4, v4, s57, v207
	v_med3_f32 v3, v3, s57, v207
	v_cvt_pk_fp8_f32 v2, v4, v3 op_sel:[0,0,1]
	v_mul_f32_e32 v3, 0x41800000, v16
	v_mul_f32_e32 v4, 0x41800000, v17
	v_med3_f32 v9, v3, s57, v207
	v_med3_f32 v4, v4, s57, v207
	v_mov_b32_e32 v3, v167
	v_cvt_pk_fp8_f32 v3, v9, v4
	v_mul_f32_e32 v5, 0x41800000, v14
	v_mul_f32_e32 v4, 0x41800000, v15
	v_med3_f32 v5, v5, s57, v207
	v_med3_f32 v4, v4, s57, v207
	v_cvt_pk_fp8_f32 v3, v5, v4 op_sel:[0,0,1]
	v_add_u32_e32 v16, 0x90, v8
	v_ashrrev_i32_e32 v17, 31, v16
	v_pk_mul_f32 v[28:29], v[74:75], s[28:29] op_sel_hi:[1,0]
	global_store_dwordx2 v[18:19], v[2:3], off offset:128
	v_mad_i64_i32 v[2:3], s[0:1], v16, s56, v[10:11]
	v_lshl_add_u64 v[14:15], v[2:3], 0, v[12:13]
	v_lshlrev_b64 v[18:19], 11, v[16:17]
	v_lshl_add_u64 v[16:17], s[16:17], 0, v[18:19]
	v_lshl_add_u64 v[16:17], v[16:17], 0, v[6:7]
	v_pk_mul_f32 v[26:27], v[76:77], s[28:29] op_sel_hi:[1,0]
	v_pk_mul_f32 v[24:25], v[78:79], s[28:29] op_sel_hi:[1,0]
	v_pk_mul_f32 v[22:23], v[80:81], s[28:29] op_sel_hi:[1,0]
	s_waitcnt vmcnt(11)
	v_mov_b64_e32 v[2:3], v[230:231]
	v_mov_b64_e32 v[4:5], v[232:233]
	v_lshlrev_b32_e32 v9, 16, v2
	v_mul_f32_e32 v9, 0xbfb8aa3b, v9
	v_exp_f32_e32 v9, v9
	v_and_b32_e32 v2, 0xffff0000, v2
	v_mul_f32_e32 v2, 0xbfb8aa3b, v2
	v_exp_f32_e32 v2, v2
	v_add_f32_e32 v9, 1.0, v9
	v_add_f32_e32 v2, 1.0, v2
	v_lshlrev_b32_e32 v31, 16, v3
	v_mul_f32_e32 v31, 0xbfb8aa3b, v31
	v_rcp_f32_e32 v179, v9
	v_exp_f32_e32 v31, v31
	s_nop 0
	v_add_f32_e32 v31, 1.0, v31
	v_and_b32_e32 v3, 0xffff0000, v3
	v_mul_f32_e32 v3, 0xbfb8aa3b, v3
	v_rcp_f32_e32 v9, v2
	v_exp_f32_e32 v3, v3
	s_nop 0
	v_add_f32_e32 v3, 1.0, v3
	v_rcp_f32_e32 v75, v31
	v_lshlrev_b32_e32 v31, 16, v4
	v_mul_f32_e32 v31, 0xbfb8aa3b, v31
	v_exp_f32_e32 v31, v31
	s_nop 0
	v_add_f32_e32 v31, 1.0, v31
	v_and_b32_e32 v4, 0xffff0000, v4
	v_mul_f32_e32 v4, 0xbfb8aa3b, v4
	v_exp_f32_e32 v4, v4
	v_rcp_f32_e32 v74, v3
	v_add_f32_e32 v4, 1.0, v4
	v_rcp_f32_e32 v76, v31
	v_lshlrev_b32_e32 v31, 16, v5
	v_mul_f32_e32 v31, 0xbfb8aa3b, v31
	v_exp_f32_e32 v31, v31
	s_nop 0
	v_add_f32_e32 v30, 1.0, v31
	v_rcp_f32_e32 v77, v4
	v_and_b32_e32 v4, 0xffff0000, v5
	v_mul_f32_e32 v4, 0xbfb8aa3b, v4
	v_exp_f32_e32 v4, v4
	s_nop 0
	v_add_f32_e32 v4, 1.0, v4
	v_rcp_f32_e32 v78, v30
	v_mov_b32_e32 v33, v24
	v_rcp_f32_e32 v79, v4
	s_waitcnt vmcnt(10)
	v_mov_b64_e32 v[20:21], v[246:247]
	v_cvt_pk_f32_fp8_e32 v[2:3], v20
	v_cvt_pk_f32_fp8_sdwa v[4:5], v20 src0_sel:WORD_1
	v_cvt_pk_f32_fp8_e32 v[30:31], v21
	v_cvt_pk_f32_fp8_sdwa v[20:21], v21 src0_sel:WORD_1
	v_mov_b32_e32 v32, v2
	v_pk_mul_f32 v[32:33], v[32:33], v[178:179]
	v_mov_b32_e32 v24, v3
	v_mov_b32_e32 v179, v9
	v_pk_mul_f32 v[2:3], v[24:25], v[178:179]
	v_mov_b32_e32 v179, v75
	v_add_f32_e32 v9, v2, v3
	v_mov_b32_e32 v2, v4
	v_mov_b32_e32 v3, v22
	v_pk_mul_f32 v[2:3], v[2:3], v[178:179]
	v_mov_b32_e32 v22, v5
	v_mov_b32_e32 v179, v74
	v_add_f32_e32 v4, v2, v3
	v_pk_mul_f32 v[2:3], v[22:23], v[178:179]
	v_mov_b32_e32 v179, v76
	v_add_f32_e32 v5, v2, v3
	v_mov_b32_e32 v2, v30
	v_mov_b32_e32 v3, v28
	v_pk_mul_f32 v[2:3], v[2:3], v[178:179]
	v_mov_b32_e32 v28, v31
	v_mov_b32_e32 v179, v77
	v_add_f32_e32 v22, v2, v3
	v_pk_mul_f32 v[2:3], v[28:29], v[178:179]
	v_mov_b32_e32 v179, v78
	v_add_f32_e32 v23, v2, v3
	v_mov_b32_e32 v2, v20
	v_mov_b32_e32 v3, v26
	v_pk_mul_f32 v[2:3], v[2:3], v[178:179]
	v_mov_b32_e32 v26, v21
	v_mov_b32_e32 v179, v79
	v_add_f32_e32 v32, v32, v33
	v_add_f32_e32 v20, v2, v3
	v_pk_mul_f32 v[2:3], v[26:27], v[178:179]
	v_mul_f32_e32 v4, 0x41800000, v4
	v_add_f32_e32 v21, v2, v3
	v_mul_f32_e32 v2, 0x41800000, v32
	v_mul_f32_e32 v3, 0x41800000, v9
	v_med3_f32 v9, v2, s57, v207
	v_med3_f32 v3, v3, s57, v207
	v_mov_b32_e32 v2, v167
	v_cvt_pk_fp8_f32 v2, v9, v3
	v_mul_f32_e32 v3, 0x41800000, v5
	v_med3_f32 v4, v4, s57, v207
	v_med3_f32 v3, v3, s57, v207
	v_cvt_pk_fp8_f32 v2, v4, v3 op_sel:[0,0,1]
	v_mul_f32_e32 v3, 0x41800000, v22
	v_mul_f32_e32 v4, 0x41800000, v23
	v_med3_f32 v9, v3, s57, v207
	v_med3_f32 v4, v4, s57, v207
	v_mov_b32_e32 v3, v167
	v_cvt_pk_fp8_f32 v3, v9, v4
	v_mul_f32_e32 v5, 0x41800000, v20
	v_mul_f32_e32 v4, 0x41800000, v21
	v_med3_f32 v5, v5, s57, v207
	v_med3_f32 v4, v4, s57, v207
	v_cvt_pk_fp8_f32 v3, v5, v4 op_sel:[0,0,1]
	v_lshl_add_u64 v[4:5], s[20:21], 0, v[18:19]
	v_lshl_add_u64 v[18:19], v[4:5], 0, v[6:7]
	v_pk_mul_f32 v[24:25], v[66:67], s[28:29] op_sel_hi:[1,0]
	global_store_dwordx2 v[18:19], v[2:3], off
	s_nop 0
	v_pk_mul_f32 v[20:21], v[70:71], s[28:29] op_sel_hi:[1,0]
	v_pk_mul_f32 v[16:17], v[72:73], s[28:29] op_sel_hi:[1,0]
	v_pk_mul_f32 v[22:23], v[68:69], s[28:29] op_sel_hi:[1,0]
	s_waitcnt vmcnt(9)
	v_mov_b64_e32 v[2:3], v[234:235]
	v_mov_b64_e32 v[4:5], v[236:237]
	v_lshlrev_b32_e32 v9, 16, v2
	v_mul_f32_e32 v9, 0xbfb8aa3b, v9
	v_exp_f32_e32 v9, v9
	v_and_b32_e32 v2, 0xffff0000, v2
	v_mul_f32_e32 v2, 0xbfb8aa3b, v2
	v_exp_f32_e32 v2, v2
	v_add_f32_e32 v9, 1.0, v9
	v_add_f32_e32 v2, 1.0, v2
	v_lshlrev_b32_e32 v27, 16, v3
	v_mul_f32_e32 v27, 0xbfb8aa3b, v27
	v_rcp_f32_e32 v179, v9
	v_exp_f32_e32 v27, v27
	s_nop 0
	v_add_f32_e32 v27, 1.0, v27
	v_and_b32_e32 v3, 0xffff0000, v3
	v_mul_f32_e32 v3, 0xbfb8aa3b, v3
	v_rcp_f32_e32 v9, v2
	v_exp_f32_e32 v3, v3
	s_nop 0
	v_add_f32_e32 v3, 1.0, v3
	v_rcp_f32_e32 v31, v27
	v_lshlrev_b32_e32 v27, 16, v4
	v_mul_f32_e32 v27, 0xbfb8aa3b, v27
	v_exp_f32_e32 v27, v27
	s_nop 0
	v_add_f32_e32 v27, 1.0, v27
	v_and_b32_e32 v4, 0xffff0000, v4
	v_mul_f32_e32 v4, 0xbfb8aa3b, v4
	v_exp_f32_e32 v4, v4
	v_rcp_f32_e32 v30, v3
	v_add_f32_e32 v4, 1.0, v4
	v_rcp_f32_e32 v32, v27
	v_lshlrev_b32_e32 v27, 16, v5
	v_mul_f32_e32 v27, 0xbfb8aa3b, v27
	v_exp_f32_e32 v27, v27
	s_nop 0
	v_add_f32_e32 v26, 1.0, v27
	v_rcp_f32_e32 v33, v4
	v_and_b32_e32 v4, 0xffff0000, v5
	v_mul_f32_e32 v4, 0xbfb8aa3b, v4
	v_exp_f32_e32 v4, v4
	s_nop 0
	v_add_f32_e32 v4, 1.0, v4
	v_rcp_f32_e32 v66, v26
	v_mov_b32_e32 v29, v20
	v_rcp_f32_e32 v67, v4
	s_waitcnt vmcnt(8)
	v_mov_b64_e32 v[14:15], v[248:249]
	v_cvt_pk_f32_fp8_e32 v[2:3], v14
	v_cvt_pk_f32_fp8_sdwa v[4:5], v14 src0_sel:WORD_1
	v_cvt_pk_f32_fp8_e32 v[26:27], v15
	v_cvt_pk_f32_fp8_sdwa v[14:15], v15 src0_sel:WORD_1
	v_mov_b32_e32 v28, v2
	v_pk_mul_f32 v[28:29], v[28:29], v[178:179]
	v_mov_b32_e32 v20, v3
	v_mov_b32_e32 v179, v9
	v_pk_mul_f32 v[2:3], v[20:21], v[178:179]
	v_mov_b32_e32 v179, v31
	v_add_f32_e32 v9, v2, v3
	v_mov_b32_e32 v2, v4
	v_mov_b32_e32 v3, v16
	v_pk_mul_f32 v[2:3], v[2:3], v[178:179]
	v_mov_b32_e32 v16, v5
	v_mov_b32_e32 v179, v30
	v_add_f32_e32 v4, v2, v3
	v_pk_mul_f32 v[2:3], v[16:17], v[178:179]
	v_mov_b32_e32 v179, v32
	v_add_f32_e32 v5, v2, v3
	v_mov_b32_e32 v2, v26
	v_mov_b32_e32 v3, v24
	v_pk_mul_f32 v[2:3], v[2:3], v[178:179]
	v_mov_b32_e32 v24, v27
	v_mov_b32_e32 v179, v33
	v_add_f32_e32 v16, v2, v3
	v_pk_mul_f32 v[2:3], v[24:25], v[178:179]
	v_mov_b32_e32 v179, v66
	v_add_f32_e32 v17, v2, v3
	v_mov_b32_e32 v2, v14
	v_mov_b32_e32 v3, v22
	v_pk_mul_f32 v[2:3], v[2:3], v[178:179]
	v_mov_b32_e32 v22, v15
	v_mov_b32_e32 v179, v67
	v_add_f32_e32 v28, v28, v29
	v_add_f32_e32 v14, v2, v3
	v_pk_mul_f32 v[2:3], v[22:23], v[178:179]
	v_mul_f32_e32 v4, 0x41800000, v4
	v_add_f32_e32 v15, v2, v3
	v_mul_f32_e32 v2, 0x41800000, v28
	v_mul_f32_e32 v3, 0x41800000, v9
	v_med3_f32 v9, v2, s57, v207
	v_med3_f32 v3, v3, s57, v207
	v_mov_b32_e32 v2, v167
	v_cvt_pk_fp8_f32 v2, v9, v3
	v_mul_f32_e32 v3, 0x41800000, v5
	v_med3_f32 v4, v4, s57, v207
	v_med3_f32 v3, v3, s57, v207
	v_cvt_pk_fp8_f32 v2, v4, v3 op_sel:[0,0,1]
	v_mul_f32_e32 v3, 0x41800000, v16
	v_mul_f32_e32 v4, 0x41800000, v17
	v_med3_f32 v9, v3, s57, v207
	v_med3_f32 v4, v4, s57, v207
	v_mov_b32_e32 v3, v167
	v_cvt_pk_fp8_f32 v3, v9, v4
	v_mul_f32_e32 v5, 0x41800000, v14
	v_mul_f32_e32 v4, 0x41800000, v15
	v_med3_f32 v5, v5, s57, v207
	v_med3_f32 v4, v4, s57, v207
	v_cvt_pk_fp8_f32 v3, v5, v4 op_sel:[0,0,1]
	v_add_u32_e32 v16, 0xa0, v8
	v_ashrrev_i32_e32 v17, 31, v16
	v_pk_mul_f32 v[28:29], v[58:59], s[28:29] op_sel_hi:[1,0]
	global_store_dwordx2 v[18:19], v[2:3], off offset:128
	v_mad_i64_i32 v[2:3], s[0:1], v16, s56, v[10:11]
	v_lshl_add_u64 v[14:15], v[2:3], 0, v[12:13]
	v_lshlrev_b64 v[18:19], 11, v[16:17]
	v_lshl_add_u64 v[16:17], s[16:17], 0, v[18:19]
	v_lshl_add_u64 v[16:17], v[16:17], 0, v[6:7]
	v_pk_mul_f32 v[26:27], v[60:61], s[28:29] op_sel_hi:[1,0]
	v_pk_mul_f32 v[24:25], v[62:63], s[28:29] op_sel_hi:[1,0]
	v_pk_mul_f32 v[22:23], v[64:65], s[28:29] op_sel_hi:[1,0]
	s_waitcnt vmcnt(7)
	v_mov_b64_e32 v[2:3], v[214:215]
	v_mov_b64_e32 v[4:5], v[216:217]
	v_lshlrev_b32_e32 v9, 16, v2
	v_mul_f32_e32 v9, 0xbfb8aa3b, v9
	v_exp_f32_e32 v9, v9
	v_and_b32_e32 v2, 0xffff0000, v2
	v_mul_f32_e32 v2, 0xbfb8aa3b, v2
	v_exp_f32_e32 v2, v2
	v_add_f32_e32 v9, 1.0, v9
	v_add_f32_e32 v2, 1.0, v2
	v_lshlrev_b32_e32 v31, 16, v3
	v_mul_f32_e32 v31, 0xbfb8aa3b, v31
	v_rcp_f32_e32 v179, v9
	v_exp_f32_e32 v31, v31
	s_nop 0
	v_add_f32_e32 v31, 1.0, v31
	v_and_b32_e32 v3, 0xffff0000, v3
	v_mul_f32_e32 v3, 0xbfb8aa3b, v3
	v_rcp_f32_e32 v9, v2
	v_exp_f32_e32 v3, v3
	s_nop 0
	v_add_f32_e32 v3, 1.0, v3
	v_rcp_f32_e32 v59, v31
	v_lshlrev_b32_e32 v31, 16, v4
	v_mul_f32_e32 v31, 0xbfb8aa3b, v31
	v_exp_f32_e32 v31, v31
	s_nop 0
	v_add_f32_e32 v31, 1.0, v31
	v_and_b32_e32 v4, 0xffff0000, v4
	v_mul_f32_e32 v4, 0xbfb8aa3b, v4
	v_exp_f32_e32 v4, v4
	v_rcp_f32_e32 v58, v3
	v_add_f32_e32 v4, 1.0, v4
	v_rcp_f32_e32 v60, v31
	v_lshlrev_b32_e32 v31, 16, v5
	v_mul_f32_e32 v31, 0xbfb8aa3b, v31
	v_exp_f32_e32 v31, v31
	s_nop 0
	v_add_f32_e32 v30, 1.0, v31
	v_rcp_f32_e32 v61, v4
	v_and_b32_e32 v4, 0xffff0000, v5
	v_mul_f32_e32 v4, 0xbfb8aa3b, v4
	v_exp_f32_e32 v4, v4
	s_nop 0
	v_add_f32_e32 v4, 1.0, v4
	v_rcp_f32_e32 v62, v30
	v_mov_b32_e32 v33, v24
	v_rcp_f32_e32 v63, v4
	s_waitcnt vmcnt(6)
	v_mov_b64_e32 v[20:21], v[238:239]
	v_cvt_pk_f32_fp8_e32 v[2:3], v20
	v_cvt_pk_f32_fp8_sdwa v[4:5], v20 src0_sel:WORD_1
	v_cvt_pk_f32_fp8_e32 v[30:31], v21
	v_cvt_pk_f32_fp8_sdwa v[20:21], v21 src0_sel:WORD_1
	v_mov_b32_e32 v32, v2
	v_pk_mul_f32 v[32:33], v[32:33], v[178:179]
	v_mov_b32_e32 v24, v3
	v_mov_b32_e32 v179, v9
	v_pk_mul_f32 v[2:3], v[24:25], v[178:179]
	v_mov_b32_e32 v179, v59
	v_add_f32_e32 v9, v2, v3
	v_mov_b32_e32 v2, v4
	v_mov_b32_e32 v3, v22
	v_pk_mul_f32 v[2:3], v[2:3], v[178:179]
	v_mov_b32_e32 v22, v5
	v_mov_b32_e32 v179, v58
	v_add_f32_e32 v4, v2, v3
	v_pk_mul_f32 v[2:3], v[22:23], v[178:179]
	v_mov_b32_e32 v179, v60
	v_add_f32_e32 v5, v2, v3
	v_mov_b32_e32 v2, v30
	v_mov_b32_e32 v3, v28
	v_pk_mul_f32 v[2:3], v[2:3], v[178:179]
	v_mov_b32_e32 v28, v31
	v_mov_b32_e32 v179, v61
	v_add_f32_e32 v22, v2, v3
	v_pk_mul_f32 v[2:3], v[28:29], v[178:179]
	v_mov_b32_e32 v179, v62
	v_add_f32_e32 v23, v2, v3
	v_mov_b32_e32 v2, v20
	v_mov_b32_e32 v3, v26
	v_pk_mul_f32 v[2:3], v[2:3], v[178:179]
	v_mov_b32_e32 v26, v21
	v_mov_b32_e32 v179, v63
	v_add_f32_e32 v32, v32, v33
	v_add_f32_e32 v20, v2, v3
	v_pk_mul_f32 v[2:3], v[26:27], v[178:179]
	v_mul_f32_e32 v4, 0x41800000, v4
	v_add_f32_e32 v21, v2, v3
	v_mul_f32_e32 v2, 0x41800000, v32
	v_mul_f32_e32 v3, 0x41800000, v9
	v_med3_f32 v9, v2, s57, v207
	v_med3_f32 v3, v3, s57, v207
	v_mov_b32_e32 v2, v167
	v_cvt_pk_fp8_f32 v2, v9, v3
	v_mul_f32_e32 v3, 0x41800000, v5
	v_med3_f32 v4, v4, s57, v207
	v_med3_f32 v3, v3, s57, v207
	v_cvt_pk_fp8_f32 v2, v4, v3 op_sel:[0,0,1]
	v_mul_f32_e32 v3, 0x41800000, v22
	v_mul_f32_e32 v4, 0x41800000, v23
	v_med3_f32 v9, v3, s57, v207
	v_med3_f32 v4, v4, s57, v207
	v_mov_b32_e32 v3, v167
	v_cvt_pk_fp8_f32 v3, v9, v4
	v_mul_f32_e32 v5, 0x41800000, v20
	v_mul_f32_e32 v4, 0x41800000, v21
	v_med3_f32 v5, v5, s57, v207
	v_med3_f32 v4, v4, s57, v207
	v_cvt_pk_fp8_f32 v3, v5, v4 op_sel:[0,0,1]
	v_lshl_add_u64 v[4:5], s[20:21], 0, v[18:19]
	v_lshl_add_u64 v[18:19], v[4:5], 0, v[6:7]
	v_pk_mul_f32 v[24:25], v[50:51], s[28:29] op_sel_hi:[1,0]
	global_store_dwordx2 v[18:19], v[2:3], off
	s_nop 0
	v_pk_mul_f32 v[20:21], v[54:55], s[28:29] op_sel_hi:[1,0]
	v_pk_mul_f32 v[16:17], v[56:57], s[28:29] op_sel_hi:[1,0]
	v_pk_mul_f32 v[22:23], v[52:53], s[28:29] op_sel_hi:[1,0]
	s_waitcnt vmcnt(5)
	v_mov_b64_e32 v[2:3], v[218:219]
	v_mov_b64_e32 v[4:5], v[220:221]
	v_lshlrev_b32_e32 v9, 16, v2
	v_mul_f32_e32 v9, 0xbfb8aa3b, v9
	v_exp_f32_e32 v9, v9
	v_and_b32_e32 v2, 0xffff0000, v2
	v_mul_f32_e32 v2, 0xbfb8aa3b, v2
	v_exp_f32_e32 v2, v2
	v_add_f32_e32 v9, 1.0, v9
	v_add_f32_e32 v2, 1.0, v2
	v_lshlrev_b32_e32 v27, 16, v3
	v_mul_f32_e32 v27, 0xbfb8aa3b, v27
	v_rcp_f32_e32 v179, v9
	v_exp_f32_e32 v27, v27
	s_nop 0
	v_add_f32_e32 v27, 1.0, v27
	v_and_b32_e32 v3, 0xffff0000, v3
	v_mul_f32_e32 v3, 0xbfb8aa3b, v3
	v_rcp_f32_e32 v9, v2
	v_exp_f32_e32 v3, v3
	s_nop 0
	v_add_f32_e32 v3, 1.0, v3
	v_rcp_f32_e32 v31, v27
	v_lshlrev_b32_e32 v27, 16, v4
	v_mul_f32_e32 v27, 0xbfb8aa3b, v27
	v_exp_f32_e32 v27, v27
	s_nop 0
	v_add_f32_e32 v27, 1.0, v27
	v_and_b32_e32 v4, 0xffff0000, v4
	v_mul_f32_e32 v4, 0xbfb8aa3b, v4
	v_exp_f32_e32 v4, v4
	v_rcp_f32_e32 v30, v3
	v_add_f32_e32 v4, 1.0, v4
	v_rcp_f32_e32 v32, v27
	v_lshlrev_b32_e32 v27, 16, v5
	v_mul_f32_e32 v27, 0xbfb8aa3b, v27
	v_exp_f32_e32 v27, v27
	s_nop 0
	v_add_f32_e32 v26, 1.0, v27
	v_rcp_f32_e32 v33, v4
	v_and_b32_e32 v4, 0xffff0000, v5
	v_mul_f32_e32 v4, 0xbfb8aa3b, v4
	v_exp_f32_e32 v4, v4
	s_nop 0
	v_add_f32_e32 v4, 1.0, v4
	v_rcp_f32_e32 v50, v26
	v_mov_b32_e32 v29, v20
	v_rcp_f32_e32 v51, v4
	s_waitcnt vmcnt(4)
	v_mov_b64_e32 v[14:15], v[240:241]
	v_cvt_pk_f32_fp8_e32 v[2:3], v14
	v_cvt_pk_f32_fp8_sdwa v[4:5], v14 src0_sel:WORD_1
	v_cvt_pk_f32_fp8_e32 v[26:27], v15
	v_cvt_pk_f32_fp8_sdwa v[14:15], v15 src0_sel:WORD_1
	v_mov_b32_e32 v28, v2
	v_pk_mul_f32 v[28:29], v[28:29], v[178:179]
	v_mov_b32_e32 v20, v3
	v_mov_b32_e32 v179, v9
	v_pk_mul_f32 v[2:3], v[20:21], v[178:179]
	v_mov_b32_e32 v179, v31
	v_add_f32_e32 v9, v2, v3
	v_mov_b32_e32 v2, v4
	v_mov_b32_e32 v3, v16
	v_pk_mul_f32 v[2:3], v[2:3], v[178:179]
	v_mov_b32_e32 v16, v5
	v_mov_b32_e32 v179, v30
	v_add_f32_e32 v4, v2, v3
	v_pk_mul_f32 v[2:3], v[16:17], v[178:179]
	v_mov_b32_e32 v179, v32
	v_add_f32_e32 v5, v2, v3
	v_mov_b32_e32 v2, v26
	v_mov_b32_e32 v3, v24
	v_pk_mul_f32 v[2:3], v[2:3], v[178:179]
	v_mov_b32_e32 v24, v27
	v_mov_b32_e32 v179, v33
	v_add_f32_e32 v16, v2, v3
	v_pk_mul_f32 v[2:3], v[24:25], v[178:179]
	v_mov_b32_e32 v179, v50
	v_add_f32_e32 v17, v2, v3
	v_mov_b32_e32 v2, v14
	v_mov_b32_e32 v3, v22
	v_pk_mul_f32 v[2:3], v[2:3], v[178:179]
	v_mov_b32_e32 v22, v15
	v_mov_b32_e32 v179, v51
	v_add_f32_e32 v28, v28, v29
	v_add_f32_e32 v14, v2, v3
	v_pk_mul_f32 v[2:3], v[22:23], v[178:179]
	v_mul_f32_e32 v4, 0x41800000, v4
	v_add_f32_e32 v15, v2, v3
	v_mul_f32_e32 v2, 0x41800000, v28
	v_mul_f32_e32 v3, 0x41800000, v9
	v_med3_f32 v9, v2, s57, v207
	v_med3_f32 v3, v3, s57, v207
	v_mov_b32_e32 v2, v167
	v_cvt_pk_fp8_f32 v2, v9, v3
	v_mul_f32_e32 v3, 0x41800000, v5
	v_med3_f32 v4, v4, s57, v207
	v_med3_f32 v3, v3, s57, v207
	v_cvt_pk_fp8_f32 v2, v4, v3 op_sel:[0,0,1]
	v_mul_f32_e32 v3, 0x41800000, v16
	v_mul_f32_e32 v4, 0x41800000, v17
	v_med3_f32 v9, v3, s57, v207
	v_med3_f32 v4, v4, s57, v207
	v_mov_b32_e32 v3, v167
	v_cvt_pk_fp8_f32 v3, v9, v4
	v_mul_f32_e32 v5, 0x41800000, v14
	v_mul_f32_e32 v4, 0x41800000, v15
	v_med3_f32 v5, v5, s57, v207
	v_med3_f32 v4, v4, s57, v207
	v_cvt_pk_fp8_f32 v3, v5, v4 op_sel:[0,0,1]
	v_add_u32_e32 v14, 0xb0, v8
	v_ashrrev_i32_e32 v15, 31, v14
	v_pk_mul_f32 v[22:23], v[42:43], s[28:29] op_sel_hi:[1,0]
	global_store_dwordx2 v[18:19], v[2:3], off offset:128
	v_mad_i64_i32 v[2:3], s[0:1], v14, s56, v[10:11]
	v_lshl_add_u64 v[8:9], v[2:3], 0, v[12:13]
	v_lshlrev_b64 v[12:13], 11, v[14:15]
	v_lshl_add_u64 v[10:11], s[16:17], 0, v[12:13]
	v_lshl_add_u64 v[10:11], v[10:11], 0, v[6:7]
	v_pk_mul_f32 v[20:21], v[44:45], s[28:29] op_sel_hi:[1,0]
	s_waitcnt vmcnt(3)
	v_mov_b64_e32 v[2:3], v[222:223]
	v_mov_b64_e32 v[4:5], v[224:225]
	v_lshlrev_b32_e32 v16, 16, v2
	v_mul_f32_e32 v16, 0xbfb8aa3b, v16
	v_exp_f32_e32 v18, v16
	v_and_b32_e32 v2, 0xffff0000, v2
	v_mul_f32_e32 v2, 0xbfb8aa3b, v2
	v_exp_f32_e32 v2, v2
	v_add_f32_e32 v24, 1.0, v18
	v_add_f32_e32 v2, 1.0, v2
	v_pk_mul_f32 v[18:19], v[46:47], s[28:29] op_sel_hi:[1,0]
	v_pk_mul_f32 v[16:17], v[48:49], s[28:29] op_sel_hi:[1,0]
	v_lshlrev_b32_e32 v26, 16, v3
	v_mul_f32_e32 v26, 0xbfb8aa3b, v26
	v_rcp_f32_e32 v179, v24
	v_exp_f32_e32 v26, v26
	s_nop 0
	v_add_f32_e32 v26, 1.0, v26
	v_and_b32_e32 v3, 0xffff0000, v3
	v_mul_f32_e32 v3, 0xbfb8aa3b, v3
	v_exp_f32_e32 v3, v3
	v_rcp_f32_e32 v29, v2
	v_add_f32_e32 v3, 1.0, v3
	v_rcp_f32_e32 v28, v26
	v_lshlrev_b32_e32 v26, 16, v4
	v_mul_f32_e32 v26, 0xbfb8aa3b, v26
	v_exp_f32_e32 v26, v26
	s_nop 0
	v_add_f32_e32 v25, 1.0, v26
	v_and_b32_e32 v4, 0xffff0000, v4
	v_mul_f32_e32 v4, 0xbfb8aa3b, v4
	v_exp_f32_e32 v4, v4
	v_rcp_f32_e32 v31, v3
	v_add_f32_e32 v4, 1.0, v4
	v_rcp_f32_e32 v30, v25
	v_lshlrev_b32_e32 v25, 16, v5
	v_mul_f32_e32 v25, 0xbfb8aa3b, v25
	v_exp_f32_e32 v25, v25
	s_nop 0
	v_add_f32_e32 v24, 1.0, v25
	v_rcp_f32_e32 v32, v4
	v_and_b32_e32 v4, 0xffff0000, v5
	v_mul_f32_e32 v4, 0xbfb8aa3b, v4
	v_exp_f32_e32 v4, v4
	s_nop 0
	v_add_f32_e32 v4, 1.0, v4
	v_rcp_f32_e32 v33, v24
	v_mov_b32_e32 v27, v18
	v_rcp_f32_e32 v42, v4
	s_waitcnt vmcnt(2)
	v_mov_b64_e32 v[14:15], v[242:243]
	v_cvt_pk_f32_fp8_e32 v[2:3], v14
	v_cvt_pk_f32_fp8_sdwa v[4:5], v14 src0_sel:WORD_1
	v_cvt_pk_f32_fp8_e32 v[24:25], v15
	v_cvt_pk_f32_fp8_sdwa v[14:15], v15 src0_sel:WORD_1
	v_mov_b32_e32 v26, v2
	v_pk_mul_f32 v[26:27], v[26:27], v[178:179]
	v_mov_b32_e32 v18, v3
	v_mov_b32_e32 v179, v29
	v_pk_mul_f32 v[2:3], v[18:19], v[178:179]
	v_mov_b32_e32 v179, v28
	v_add_f32_e32 v18, v2, v3
	v_mov_b32_e32 v2, v4
	v_mov_b32_e32 v3, v16
	v_pk_mul_f32 v[2:3], v[2:3], v[178:179]
	v_mov_b32_e32 v16, v5
	v_mov_b32_e32 v179, v31
	v_add_f32_e32 v4, v2, v3
	v_pk_mul_f32 v[2:3], v[16:17], v[178:179]
	v_mov_b32_e32 v179, v30
	v_add_f32_e32 v5, v2, v3
	v_mov_b32_e32 v2, v24
	v_mov_b32_e32 v3, v22
	v_pk_mul_f32 v[2:3], v[2:3], v[178:179]
	v_mov_b32_e32 v22, v25
	v_mov_b32_e32 v179, v32
	v_add_f32_e32 v16, v2, v3
	v_pk_mul_f32 v[2:3], v[22:23], v[178:179]
	v_mov_b32_e32 v179, v33
	v_add_f32_e32 v17, v2, v3
	v_mov_b32_e32 v2, v14
	v_mov_b32_e32 v3, v20
	v_pk_mul_f32 v[2:3], v[2:3], v[178:179]
	v_mov_b32_e32 v20, v15
	v_mov_b32_e32 v179, v42
	v_add_f32_e32 v26, v26, v27
	v_add_f32_e32 v14, v2, v3
	v_pk_mul_f32 v[2:3], v[20:21], v[178:179]
	v_mul_f32_e32 v4, 0x41800000, v4
	v_add_f32_e32 v15, v2, v3
	v_mul_f32_e32 v2, 0x41800000, v26
	v_mul_f32_e32 v3, 0x41800000, v18
	v_med3_f32 v18, v2, s57, v207
	v_med3_f32 v3, v3, s57, v207
	v_mov_b32_e32 v2, v167
	v_cvt_pk_fp8_f32 v2, v18, v3
	v_mul_f32_e32 v3, 0x41800000, v5
	v_med3_f32 v4, v4, s57, v207
	v_med3_f32 v3, v3, s57, v207
	v_cvt_pk_fp8_f32 v2, v4, v3 op_sel:[0,0,1]
	v_mul_f32_e32 v3, 0x41800000, v16
	v_mul_f32_e32 v4, 0x41800000, v17
	v_mul_f32_e32 v5, 0x41800000, v14
	v_med3_f32 v14, v3, s57, v207
	v_med3_f32 v4, v4, s57, v207
	v_mov_b32_e32 v3, v167
	v_cvt_pk_fp8_f32 v3, v14, v4
	v_mul_f32_e32 v4, 0x41800000, v15
	v_med3_f32 v5, v5, s57, v207
	v_med3_f32 v4, v4, s57, v207
	v_cvt_pk_fp8_f32 v3, v5, v4 op_sel:[0,0,1]
	v_lshl_add_u64 v[4:5], s[20:21], 0, v[12:13]
	v_lshl_add_u64 v[6:7], v[4:5], 0, v[6:7]
	v_pk_mul_f32 v[16:17], v[34:35], s[28:29] op_sel_hi:[1,0]
	global_store_dwordx2 v[6:7], v[2:3], off
	s_nop 0
	v_pk_mul_f32 v[14:15], v[36:37], s[28:29] op_sel_hi:[1,0]
	s_waitcnt vmcnt(1)
	v_mov_b64_e32 v[2:3], v[226:227]
	v_mov_b64_e32 v[4:5], v[228:229]
	v_lshlrev_b32_e32 v10, 16, v2
	v_mul_f32_e32 v10, 0xbfb8aa3b, v10
	v_exp_f32_e32 v12, v10
	v_and_b32_e32 v2, 0xffff0000, v2
	v_mul_f32_e32 v2, 0xbfb8aa3b, v2
	v_exp_f32_e32 v2, v2
	v_add_f32_e32 v18, 1.0, v12
	v_add_f32_e32 v2, 1.0, v2
	v_pk_mul_f32 v[12:13], v[38:39], s[28:29] op_sel_hi:[1,0]
	v_pk_mul_f32 v[10:11], v[40:41], s[28:29] op_sel_hi:[1,0]
	v_lshlrev_b32_e32 v20, 16, v3
	v_mul_f32_e32 v20, 0xbfb8aa3b, v20
	v_rcp_f32_e32 v179, v18
	v_exp_f32_e32 v20, v20
	s_nop 0
	v_add_f32_e32 v20, 1.0, v20
	v_and_b32_e32 v3, 0xffff0000, v3
	v_mul_f32_e32 v3, 0xbfb8aa3b, v3
	v_exp_f32_e32 v3, v3
	v_rcp_f32_e32 v23, v2
	v_add_f32_e32 v3, 1.0, v3
	v_rcp_f32_e32 v22, v20
	v_lshlrev_b32_e32 v20, 16, v4
	v_mul_f32_e32 v20, 0xbfb8aa3b, v20
	v_exp_f32_e32 v20, v20
	s_nop 0
	v_add_f32_e32 v19, 1.0, v20
	v_and_b32_e32 v4, 0xffff0000, v4
	v_mul_f32_e32 v4, 0xbfb8aa3b, v4
	v_exp_f32_e32 v4, v4
	v_rcp_f32_e32 v25, v3
	v_add_f32_e32 v4, 1.0, v4
	v_rcp_f32_e32 v24, v19
	v_lshlrev_b32_e32 v19, 16, v5
	v_mul_f32_e32 v19, 0xbfb8aa3b, v19
	v_exp_f32_e32 v19, v19
	s_nop 0
	v_add_f32_e32 v18, 1.0, v19
	v_rcp_f32_e32 v26, v4
	v_and_b32_e32 v4, 0xffff0000, v5
	v_mul_f32_e32 v4, 0xbfb8aa3b, v4
	v_exp_f32_e32 v4, v4
	s_nop 0
	v_add_f32_e32 v4, 1.0, v4
	v_rcp_f32_e32 v27, v18
	v_mov_b32_e32 v21, v12
	v_rcp_f32_e32 v28, v4
	s_waitcnt vmcnt(0)
	v_mov_b64_e32 v[8:9], v[244:245]
	v_cvt_pk_f32_fp8_e32 v[2:3], v8
	v_cvt_pk_f32_fp8_sdwa v[4:5], v8 src0_sel:WORD_1
	v_cvt_pk_f32_fp8_e32 v[18:19], v9
	v_cvt_pk_f32_fp8_sdwa v[8:9], v9 src0_sel:WORD_1
	v_mov_b32_e32 v20, v2
	v_pk_mul_f32 v[20:21], v[20:21], v[178:179]
	v_mov_b32_e32 v12, v3
	v_mov_b32_e32 v179, v23
	v_pk_mul_f32 v[2:3], v[12:13], v[178:179]
	v_mov_b32_e32 v179, v22
	v_add_f32_e32 v12, v2, v3
	v_mov_b32_e32 v2, v4
	v_mov_b32_e32 v3, v10
	v_pk_mul_f32 v[2:3], v[2:3], v[178:179]
	v_mov_b32_e32 v10, v5
	v_mov_b32_e32 v179, v25
	v_add_f32_e32 v4, v2, v3
	v_pk_mul_f32 v[2:3], v[10:11], v[178:179]
	v_mov_b32_e32 v179, v24
	v_add_f32_e32 v5, v2, v3
	v_mov_b32_e32 v2, v18
	v_mov_b32_e32 v3, v16
	v_pk_mul_f32 v[2:3], v[2:3], v[178:179]
	v_mov_b32_e32 v16, v19
	v_mov_b32_e32 v179, v26
	v_add_f32_e32 v10, v2, v3
	v_pk_mul_f32 v[2:3], v[16:17], v[178:179]
	v_mov_b32_e32 v179, v27
	v_add_f32_e32 v11, v2, v3
	v_mov_b32_e32 v2, v8
	v_mov_b32_e32 v3, v14
	v_pk_mul_f32 v[2:3], v[2:3], v[178:179]
	v_mov_b32_e32 v14, v9
	v_mov_b32_e32 v179, v28
	v_add_f32_e32 v20, v20, v21
	v_add_f32_e32 v8, v2, v3
	v_pk_mul_f32 v[2:3], v[14:15], v[178:179]
	v_mul_f32_e32 v4, 0x41800000, v4
	v_add_f32_e32 v9, v2, v3
	v_mul_f32_e32 v2, 0x41800000, v20
	v_mul_f32_e32 v3, 0x41800000, v12
	v_med3_f32 v12, v2, s57, v207
	v_med3_f32 v3, v3, s57, v207
	v_mov_b32_e32 v2, v167
	v_cvt_pk_fp8_f32 v2, v12, v3
	v_mul_f32_e32 v3, 0x41800000, v5
	v_med3_f32 v4, v4, s57, v207
	v_med3_f32 v3, v3, s57, v207
	v_cvt_pk_fp8_f32 v2, v4, v3 op_sel:[0,0,1]
	v_mul_f32_e32 v3, 0x41800000, v10
	v_mul_f32_e32 v4, 0x41800000, v11
	v_mul_f32_e32 v5, 0x41800000, v8
	v_med3_f32 v8, v3, s57, v207
	v_med3_f32 v4, v4, s57, v207
	v_mov_b32_e32 v3, v167
	v_cvt_pk_fp8_f32 v3, v8, v4
	v_mul_f32_e32 v4, 0x41800000, v9
	v_med3_f32 v5, v5, s57, v207
	v_med3_f32 v4, v4, s57, v207
	v_cvt_pk_fp8_f32 v3, v5, v4 op_sel:[0,0,1]
	s_andn2_b64 vcc, exec, s[6:7]
	s_mov_b64 s[0:1], -1
	global_store_dwordx2 v[6:7], v[2:3], off offset:128
	s_cbranch_vccnz .LBB0_1050
	s_andn2_b64 vcc, exec, s[14:15]
	s_cbranch_vccnz .LBB0_1049
	s_barrier
	s_branch .LBB0_1049

.LBB0_1150:
	v_lshl_or_b32 v6, s71, 8, v202
	v_ashrrev_i32_e32 v7, 31, v6
	v_add_u32_e32 v10, s70, v200
	v_lshl_add_u64 v[8:9], v[6:7], 2, s[14:15]
	v_ashrrev_i32_e32 v11, 31, v10
	global_load_dwordx4 v[16:19], v[8:9], off
	global_load_dwordx4 v[20:23], v[8:9], off offset:64
	global_load_dwordx4 v[24:27], v[8:9], off offset:512
	global_load_dwordx4 v[28:31], v[8:9], off offset:576
	v_lshlrev_b64 v[10:11], 11, v[10:11]
	v_lshl_add_u64 v[6:7], v[10:11], 0, v[6:7]
	v_lshlrev_b32_e32 v14, 2, v6
	global_load_dwordx4 v[212:215], v14, s[6:7]
	global_load_dwordx4 v[216:219], v14, s[6:7] offset:64
	global_load_dwordx4 v[220:223], v14, s[6:7] offset:512
	global_load_dwordx4 v[224:227], v14, s[6:7] offset:576
	v_add_u32_e32 v12, s24, v14
	global_load_dwordx4 v[228:231], v12, s[6:7]
	global_load_dwordx4 v[232:235], v12, s[6:7] offset:64
	global_load_dwordx4 v[236:239], v12, s[6:7] offset:512
	global_load_dwordx4 v[240:243], v12, s[6:7] offset:576
	v_add_u32_e32 v12, s10, v14
	global_load_dwordx4 v[244:247], v12, s[6:7]
	global_load_dwordx4 v[248:251], v12, s[6:7] offset:64
	global_load_dwordx4 v[2:5], v12, s[6:7] offset:512
	global_load_dwordx4 v[8:11], v12, s[6:7] offset:576
	s_andn2_b64 vcc, exec, s[0:1]
	s_mov_b64 s[0:1], -1
	s_nop 15
	s_waitcnt vmcnt(12)
	v_pk_mul_f32 v[16:17], v[16:17], s[22:23] op_sel_hi:[1,0]
	v_pk_mul_f32 v[18:19], v[18:19], s[22:23] op_sel_hi:[1,0]
	v_pk_mul_f32 v[20:21], v[20:21], s[22:23] op_sel_hi:[1,0]
	v_pk_mul_f32 v[22:23], v[22:23], s[22:23] op_sel_hi:[1,0]
	v_pk_mul_f32 v[24:25], v[24:25], s[22:23] op_sel_hi:[1,0]
	v_pk_mul_f32 v[26:27], v[26:27], s[22:23] op_sel_hi:[1,0]
	v_pk_mul_f32 v[28:29], v[28:29], s[22:23] op_sel_hi:[1,0]
	v_pk_mul_f32 v[30:31], v[30:31], s[22:23] op_sel_hi:[1,0]
	s_waitcnt vmcnt(8)
	v_pk_fma_f32 v[214:215], v[160:161], v[18:19], v[214:215]
	v_pk_fma_f32 v[212:213], v[158:159], v[16:17], v[212:213]
	v_pk_fma_f32 v[218:219], v[156:157], v[22:23], v[218:219]
	v_pk_fma_f32 v[216:217], v[154:155], v[20:21], v[216:217]
	v_pk_fma_f32 v[222:223], v[152:153], v[26:27], v[222:223]
	v_pk_fma_f32 v[220:221], v[150:151], v[24:25], v[220:221]
	v_pk_fma_f32 v[226:227], v[140:141], v[30:31], v[226:227]
	v_pk_fma_f32 v[224:225], v[138:139], v[28:29], v[224:225]
	global_store_dwordx4 v14, v[212:215], s[48:49]
	global_store_dwordx4 v14, v[216:219], s[48:49] offset:64
	global_store_dwordx4 v14, v[220:223], s[48:49] offset:512
	global_store_dwordx4 v14, v[224:227], s[48:49] offset:576
	v_add_u32_e32 v12, s26, v14
	global_load_dwordx4 v[212:215], v12, s[6:7]
	global_load_dwordx4 v[216:219], v12, s[6:7] offset:64
	global_load_dwordx4 v[220:223], v12, s[6:7] offset:512
	global_load_dwordx4 v[224:227], v12, s[6:7] offset:576
	s_waitcnt vmcnt(8)
	v_pk_fma_f32 v[230:231], v[148:149], v[18:19], v[230:231]
	v_pk_fma_f32 v[228:229], v[146:147], v[16:17], v[228:229]
	v_pk_fma_f32 v[234:235], v[144:145], v[22:23], v[234:235]
	v_pk_fma_f32 v[232:233], v[142:143], v[20:21], v[232:233]
	v_pk_fma_f32 v[238:239], v[136:137], v[26:27], v[238:239]
	v_pk_fma_f32 v[236:237], v[134:135], v[24:25], v[236:237]
	v_pk_fma_f32 v[242:243], v[124:125], v[30:31], v[242:243]
	v_pk_fma_f32 v[240:241], v[122:123], v[28:29], v[240:241]
	v_add_u32_e32 v13, s24, v14
	global_store_dwordx4 v13, v[228:231], s[48:49]
	global_store_dwordx4 v13, v[232:235], s[48:49] offset:64
	global_store_dwordx4 v13, v[236:239], s[48:49] offset:512
	global_store_dwordx4 v13, v[240:243], s[48:49] offset:576
	v_add_u32_e32 v12, s28, v14
	global_load_dwordx4 v[228:231], v12, s[6:7]
	global_load_dwordx4 v[232:235], v12, s[6:7] offset:64
	global_load_dwordx4 v[236:239], v12, s[6:7] offset:512
	global_load_dwordx4 v[240:243], v12, s[6:7] offset:576
	s_waitcnt vmcnt(8)
	v_pk_fma_f32 v[246:247], v[132:133], v[18:19], v[246:247]
	v_pk_fma_f32 v[244:245], v[130:131], v[16:17], v[244:245]
	v_pk_fma_f32 v[250:251], v[128:129], v[22:23], v[250:251]
	v_pk_fma_f32 v[248:249], v[126:127], v[20:21], v[248:249]
	v_pk_fma_f32 v[4:5], v[120:121], v[26:27], v[4:5]
	v_pk_fma_f32 v[2:3], v[118:119], v[24:25], v[2:3]
	v_pk_fma_f32 v[10:11], v[108:109], v[30:31], v[10:11]
	v_pk_fma_f32 v[8:9], v[106:107], v[28:29], v[8:9]
	v_add_u32_e32 v13, s10, v14
	global_store_dwordx4 v13, v[244:247], s[48:49]
	global_store_dwordx4 v13, v[248:251], s[48:49] offset:64
	global_store_dwordx4 v13, v[2:5], s[48:49] offset:512
	global_store_dwordx4 v13, v[8:11], s[48:49] offset:576
	v_add_u32_e32 v12, s30, v14
	global_load_dwordx4 v[244:247], v12, s[6:7]
	global_load_dwordx4 v[248:251], v12, s[6:7] offset:64
	global_load_dwordx4 v[2:5], v12, s[6:7] offset:512
	global_load_dwordx4 v[8:11], v12, s[6:7] offset:576
	s_waitcnt vmcnt(8)
	v_pk_fma_f32 v[214:215], v[116:117], v[18:19], v[214:215]
	v_pk_fma_f32 v[212:213], v[114:115], v[16:17], v[212:213]
	v_pk_fma_f32 v[218:219], v[112:113], v[22:23], v[218:219]
	v_pk_fma_f32 v[216:217], v[110:111], v[20:21], v[216:217]
	v_pk_fma_f32 v[222:223], v[104:105], v[26:27], v[222:223]
	v_pk_fma_f32 v[220:221], v[102:103], v[24:25], v[220:221]
	v_pk_fma_f32 v[226:227], v[100:101], v[30:31], v[226:227]
	v_pk_fma_f32 v[224:225], v[98:99], v[28:29], v[224:225]
	v_add_u32_e32 v13, s26, v14
	global_store_dwordx4 v13, v[212:215], s[48:49]
	global_store_dwordx4 v13, v[216:219], s[48:49] offset:64
	global_store_dwordx4 v13, v[220:223], s[48:49] offset:512
	global_store_dwordx4 v13, v[224:227], s[48:49] offset:576
	v_add_u32_e32 v12, s34, v14
	global_load_dwordx4 v[212:215], v12, s[6:7]
	global_load_dwordx4 v[216:219], v12, s[6:7] offset:64
	global_load_dwordx4 v[220:223], v12, s[6:7] offset:512
	global_load_dwordx4 v[224:227], v12, s[6:7] offset:576
	s_waitcnt vmcnt(8)
	v_pk_fma_f32 v[230:231], v[96:97], v[18:19], v[230:231]
	v_pk_fma_f32 v[228:229], v[94:95], v[16:17], v[228:229]
	v_pk_fma_f32 v[234:235], v[92:93], v[22:23], v[234:235]
	v_pk_fma_f32 v[232:233], v[90:91], v[20:21], v[232:233]
	v_pk_fma_f32 v[238:239], v[88:89], v[26:27], v[238:239]
	v_pk_fma_f32 v[236:237], v[86:87], v[24:25], v[236:237]
	v_pk_fma_f32 v[242:243], v[76:77], v[30:31], v[242:243]
	v_pk_fma_f32 v[240:241], v[74:75], v[28:29], v[240:241]
	v_add_u32_e32 v13, s28, v14
	global_store_dwordx4 v13, v[228:231], s[48:49]
	global_store_dwordx4 v13, v[232:235], s[48:49] offset:64
	global_store_dwordx4 v13, v[236:239], s[48:49] offset:512
	global_store_dwordx4 v13, v[240:243], s[48:49] offset:576
	v_add_u32_e32 v12, s36, v14
	global_load_dwordx4 v[228:231], v12, s[6:7]
	global_load_dwordx4 v[232:235], v12, s[6:7] offset:64
	global_load_dwordx4 v[236:239], v12, s[6:7] offset:512
	global_load_dwordx4 v[240:243], v12, s[6:7] offset:576
	s_waitcnt vmcnt(8)
	v_pk_fma_f32 v[246:247], v[84:85], v[18:19], v[246:247]
	v_pk_fma_f32 v[244:245], v[82:83], v[16:17], v[244:245]
	v_pk_fma_f32 v[250:251], v[80:81], v[22:23], v[250:251]
	v_pk_fma_f32 v[248:249], v[78:79], v[20:21], v[248:249]
	v_pk_fma_f32 v[4:5], v[72:73], v[26:27], v[4:5]
	v_pk_fma_f32 v[2:3], v[70:71], v[24:25], v[2:3]
	v_pk_fma_f32 v[10:11], v[60:61], v[30:31], v[10:11]
	v_pk_fma_f32 v[8:9], v[58:59], v[28:29], v[8:9]
	v_add_u32_e32 v13, s30, v14
	global_store_dwordx4 v13, v[244:247], s[48:49]
	global_store_dwordx4 v13, v[248:251], s[48:49] offset:64
	global_store_dwordx4 v13, v[2:5], s[48:49] offset:512
	global_store_dwordx4 v13, v[8:11], s[48:49] offset:576
	s_waitcnt vmcnt(4)
	v_pk_fma_f32 v[214:215], v[68:69], v[18:19], v[214:215]
	v_pk_fma_f32 v[212:213], v[66:67], v[16:17], v[212:213]
	v_pk_fma_f32 v[218:219], v[64:65], v[22:23], v[218:219]
	v_pk_fma_f32 v[216:217], v[62:63], v[20:21], v[216:217]
	v_pk_fma_f32 v[222:223], v[56:57], v[26:27], v[222:223]
	v_pk_fma_f32 v[220:221], v[54:55], v[24:25], v[220:221]
	v_pk_fma_f32 v[226:227], v[44:45], v[30:31], v[226:227]
	v_pk_fma_f32 v[224:225], v[42:43], v[28:29], v[224:225]
	v_add_u32_e32 v13, s34, v14
	global_store_dwordx4 v13, v[212:215], s[48:49]
	global_store_dwordx4 v13, v[216:219], s[48:49] offset:64
	global_store_dwordx4 v13, v[220:223], s[48:49] offset:512
	global_store_dwordx4 v13, v[224:227], s[48:49] offset:576
	s_waitcnt vmcnt(0)
	v_pk_fma_f32 v[230:231], v[52:53], v[18:19], v[230:231]
	v_pk_fma_f32 v[228:229], v[50:51], v[16:17], v[228:229]
	v_pk_fma_f32 v[234:235], v[48:49], v[22:23], v[234:235]
	v_pk_fma_f32 v[232:233], v[46:47], v[20:21], v[232:233]
	v_pk_fma_f32 v[238:239], v[40:41], v[26:27], v[238:239]
	v_pk_fma_f32 v[236:237], v[38:39], v[24:25], v[236:237]
	v_pk_fma_f32 v[242:243], v[36:37], v[30:31], v[242:243]
	v_pk_fma_f32 v[240:241], v[34:35], v[28:29], v[240:241]
	v_add_u32_e32 v13, s36, v14
	global_store_dwordx4 v13, v[228:231], s[48:49]
	global_store_dwordx4 v13, v[232:235], s[48:49] offset:64
	global_store_dwordx4 v13, v[236:239], s[48:49] offset:512
	global_store_dwordx4 v13, v[240:243], s[48:49] offset:576
	s_cbranch_vccnz .LBB0_1134
	s_andn2_b64 vcc, exec, s[12:13]
	s_cbranch_vccnz .LBB0_1133
	s_barrier
	s_branch .LBB0_1133

.LBB0_1677:
	v_mov_b32_e32 v2, v238
	s_add_u32 s0, s79, 0xffffff00
	s_nop 15
	s_nop 15
	s_nop 15
	s_addc_u32 s1, s80, -1
	v_lshlrev_b32_e32 v3, 5, v2
	v_ashrrev_i32_e32 v4, 1, v2
	v_and_b32_e32 v3, 0x1e0, v3
	v_and_b32_e32 v5, -8, v4
	s_add_i32 s2, s33, s69
	v_add3_u32 v8, s53, v3, v5
	v_add_u32_e32 v10, s2, v4
	v_pk_mul_f32 v[4:5], v[190:191], s[28:29] op_sel_hi:[1,0]
	v_lshlrev_b32_e32 v2, 4, v2
	v_mul_f32_e32 v6, 0xbfb8aa3b, v4
	v_exp_f32_e32 v16, v6
	v_mul_f32_e32 v27, 0xbfb8aa3b, v5
	v_exp_f32_e32 v27, v27
	v_add_u32_e32 v9, s53, v2
	v_add_f32_e32 v22, 1.0, v16
	v_and_b32_e32 v11, 16, v2
	v_pk_mul_f32 v[2:3], v[192:193], s[28:29] op_sel_hi:[1,0]
	v_pk_mul_f32 v[16:17], v[158:159], s[30:31] op_sel_hi:[1,0]
	v_add_f32_e32 v25, 1.0, v27
	v_rcp_f32_e32 v23, v22
	s_nop 0
	v_mul_f32_e32 v4, v4, v23
	v_mul_f32_e32 v23, 0xbfb8aa3b, v2
	v_exp_f32_e32 v23, v23
	v_mul_f32_e32 v4, v4, v16
	v_add_f32_e32 v23, 1.0, v23
	v_mul_f32_e32 v22, 0xbfb8aa3b, v3
	v_rcp_f32_e32 v16, v25
	s_nop 0
	v_mul_f32_e32 v5, v5, v16
	v_exp_f32_e32 v22, v22
	v_mul_f32_e32 v5, v5, v17
	v_add_f32_e32 v22, 1.0, v22
	v_pk_mul_f32 v[14:15], v[160:161], s[30:31] op_sel_hi:[1,0]
	v_rcp_f32_e32 v16, v23
	s_nop 0
	v_mul_f32_e32 v2, v2, v16
	v_mul_f32_e32 v14, v2, v14
	v_pk_mul_f32 v[12:13], v[186:187], s[28:29] op_sel_hi:[1,0]
	v_rcp_f32_e32 v2, v22
	s_nop 0
	v_mul_f32_e32 v2, v3, v2
	v_mul_f32_e32 v3, v2, v15
	v_mul_f32_e32 v2, 0xbfb8aa3b, v12
	v_exp_f32_e32 v15, v2
	v_med3_f32 v4, v4, s75, v239
	v_med3_f32 v5, v5, s75, v239
	v_mov_b32_e32 v2, v203
	v_cvt_pk_fp8_f32 v2, v4, v5
	v_add_f32_e32 v4, 1.0, v15
	v_med3_f32 v14, v14, s75, v239
	v_med3_f32 v3, v3, s75, v239
	v_cvt_pk_fp8_f32 v2, v14, v3 op_sel:[0,0,1]
	v_mul_f32_e32 v16, 0xbfb8aa3b, v13
	v_exp_f32_e32 v16, v16
	s_nop 0
	v_add_f32_e32 v5, 1.0, v16
	v_pk_mul_f32 v[6:7], v[188:189], s[28:29] op_sel_hi:[1,0]
	v_mul_f32_e32 v14, 0xbfb8aa3b, v6
	v_exp_f32_e32 v14, v14
	v_rcp_f32_e32 v3, v4
	s_nop 0
	v_mul_f32_e32 v3, v12, v3
	v_add_f32_e32 v14, 1.0, v14
	v_rcp_f32_e32 v4, v5
	s_nop 0
	v_mul_f32_e32 v4, v13, v4
	v_mul_f32_e32 v13, 0xbfb8aa3b, v7
	v_exp_f32_e32 v13, v13
	s_nop 0
	v_add_f32_e32 v13, 1.0, v13
	v_rcp_f32_e32 v5, v14
	s_nop 0
	v_mul_f32_e32 v5, v6, v5
	v_pk_mul_f32 v[20:21], v[154:155], s[30:31] op_sel_hi:[1,0]
	v_mul_f32_e32 v3, v3, v20
	v_mul_f32_e32 v4, v4, v21
	v_pk_mul_f32 v[18:19], v[156:157], s[30:31] op_sel_hi:[1,0]
	v_rcp_f32_e32 v6, v13
	s_nop 0
	v_mul_f32_e32 v6, v7, v6
	v_med3_f32 v7, v3, s75, v239
	v_med3_f32 v4, v4, s75, v239
	v_mov_b32_e32 v3, v203
	v_cvt_pk_fp8_f32 v3, v7, v4
	v_mul_f32_e32 v4, v6, v19
	v_pk_mul_f32 v[6:7], v[182:183], s[28:29] op_sel_hi:[1,0]
	v_mul_f32_e32 v5, v5, v18
	v_mul_f32_e32 v12, 0xbfb8aa3b, v6
	v_exp_f32_e32 v18, v12
	v_mul_f32_e32 v29, 0xbfb8aa3b, v7
	v_exp_f32_e32 v29, v29
	v_med3_f32 v5, v5, s75, v239
	v_add_f32_e32 v24, 1.0, v18
	v_med3_f32 v4, v4, s75, v239
	v_cvt_pk_fp8_f32 v3, v5, v4 op_sel:[0,0,1]
	v_pk_mul_f32 v[4:5], v[184:185], s[28:29] op_sel_hi:[1,0]
	v_add_f32_e32 v27, 1.0, v29
	v_rcp_f32_e32 v25, v24
	s_nop 0
	v_mul_f32_e32 v6, v6, v25
	v_mul_f32_e32 v25, 0xbfb8aa3b, v4
	v_pk_mul_f32 v[18:19], v[150:151], s[30:31] op_sel_hi:[1,0]
	v_exp_f32_e32 v25, v25
	v_mul_f32_e32 v6, v6, v18
	v_add_f32_e32 v25, 1.0, v25
	v_mul_f32_e32 v24, 0xbfb8aa3b, v5
	v_rcp_f32_e32 v18, v27
	s_nop 0
	v_mul_f32_e32 v7, v7, v18
	v_exp_f32_e32 v24, v24
	v_mul_f32_e32 v7, v7, v19
	v_add_f32_e32 v24, 1.0, v24
	v_pk_mul_f32 v[16:17], v[152:153], s[30:31] op_sel_hi:[1,0]
	v_rcp_f32_e32 v18, v25
	s_nop 0
	v_mul_f32_e32 v4, v4, v18
	v_mul_f32_e32 v16, v4, v16
	v_pk_mul_f32 v[14:15], v[178:179], s[28:29] op_sel_hi:[1,0]
	v_rcp_f32_e32 v4, v24
	s_nop 0
	v_mul_f32_e32 v4, v5, v4
	v_mul_f32_e32 v5, v4, v17
	v_mul_f32_e32 v4, 0xbfb8aa3b, v14
	v_exp_f32_e32 v17, v4
	v_med3_f32 v6, v6, s75, v239
	v_med3_f32 v7, v7, s75, v239
	v_mov_b32_e32 v4, v203
	v_cvt_pk_fp8_f32 v4, v6, v7
	v_add_f32_e32 v6, 1.0, v17
	v_med3_f32 v16, v16, s75, v239
	v_med3_f32 v5, v5, s75, v239
	v_cvt_pk_fp8_f32 v4, v16, v5 op_sel:[0,0,1]
	v_mul_f32_e32 v18, 0xbfb8aa3b, v15
	v_exp_f32_e32 v18, v18
	s_nop 0
	v_add_f32_e32 v7, 1.0, v18
	v_pk_mul_f32 v[12:13], v[180:181], s[28:29] op_sel_hi:[1,0]
	v_mul_f32_e32 v16, 0xbfb8aa3b, v12
	v_exp_f32_e32 v16, v16
	v_rcp_f32_e32 v5, v6
	s_nop 0
	v_mul_f32_e32 v5, v14, v5
	v_add_f32_e32 v16, 1.0, v16
	v_rcp_f32_e32 v6, v7
	s_nop 0
	v_mul_f32_e32 v6, v15, v6
	v_mul_f32_e32 v15, 0xbfb8aa3b, v13
	v_exp_f32_e32 v15, v15
	s_nop 0
	v_add_f32_e32 v15, 1.0, v15
	v_rcp_f32_e32 v7, v16
	s_nop 0
	v_mul_f32_e32 v7, v12, v7
	v_pk_mul_f32 v[22:23], v[146:147], s[30:31] op_sel_hi:[1,0]
	v_mul_f32_e32 v5, v5, v22
	v_mul_f32_e32 v6, v6, v23
	v_pk_mul_f32 v[20:21], v[148:149], s[30:31] op_sel_hi:[1,0]
	v_rcp_f32_e32 v12, v15
	s_nop 0
	v_mul_f32_e32 v12, v13, v12
	v_med3_f32 v13, v5, s75, v239
	v_med3_f32 v6, v6, s75, v239
	v_mov_b32_e32 v5, v203
	v_cvt_pk_fp8_f32 v5, v13, v6
	v_mul_f32_e32 v6, v12, v21
	v_pk_mul_f32 v[12:13], v[174:175], s[28:29] op_sel_hi:[1,0]
	v_mul_f32_e32 v7, v7, v20
	v_mul_f32_e32 v14, 0xbfb8aa3b, v12
	v_exp_f32_e32 v20, v14
	v_mul_f32_e32 v31, 0xbfb8aa3b, v13
	v_exp_f32_e32 v31, v31
	v_med3_f32 v7, v7, s75, v239
	v_add_f32_e32 v26, 1.0, v20
	v_med3_f32 v6, v6, s75, v239
	v_cvt_pk_fp8_f32 v5, v7, v6 op_sel:[0,0,1]
	v_lshl_or_b32 v6, s18, 7, v11
	v_add_f32_e32 v29, 1.0, v31
	v_or_b32_e32 v11, s70, v6
	v_pk_mul_f32 v[6:7], v[176:177], s[28:29] op_sel_hi:[1,0]
	v_rcp_f32_e32 v27, v26
	s_nop 0
	v_mul_f32_e32 v12, v12, v27
	v_mul_f32_e32 v27, 0xbfb8aa3b, v6
	v_pk_mul_f32 v[20:21], v[142:143], s[30:31] op_sel_hi:[1,0]
	v_exp_f32_e32 v27, v27
	v_mul_f32_e32 v12, v12, v20
	v_add_f32_e32 v27, 1.0, v27
	v_mul_f32_e32 v26, 0xbfb8aa3b, v7
	v_rcp_f32_e32 v20, v29
	s_nop 0
	v_mul_f32_e32 v13, v13, v20
	v_exp_f32_e32 v26, v26
	v_mul_f32_e32 v13, v13, v21
	v_add_f32_e32 v26, 1.0, v26
	v_pk_mul_f32 v[18:19], v[144:145], s[30:31] op_sel_hi:[1,0]
	v_rcp_f32_e32 v20, v27
	s_nop 0
	v_mul_f32_e32 v6, v6, v20
	v_mul_f32_e32 v18, v6, v18
	v_pk_mul_f32 v[16:17], v[170:171], s[28:29] op_sel_hi:[1,0]
	v_rcp_f32_e32 v6, v26
	s_nop 0
	v_mul_f32_e32 v6, v7, v6
	v_mul_f32_e32 v7, v6, v19
	v_mul_f32_e32 v6, 0xbfb8aa3b, v16
	v_exp_f32_e32 v19, v6
	v_med3_f32 v12, v12, s75, v239
	v_med3_f32 v13, v13, s75, v239
	v_mov_b32_e32 v6, v203
	v_cvt_pk_fp8_f32 v6, v12, v13
	v_add_f32_e32 v12, 1.0, v19
	v_med3_f32 v18, v18, s75, v239
	v_med3_f32 v7, v7, s75, v239
	v_cvt_pk_fp8_f32 v6, v18, v7 op_sel:[0,0,1]
	v_mul_f32_e32 v20, 0xbfb8aa3b, v17
	v_exp_f32_e32 v20, v20
	s_nop 0
	v_add_f32_e32 v13, 1.0, v20
	v_pk_mul_f32 v[14:15], v[172:173], s[28:29] op_sel_hi:[1,0]
	v_mul_f32_e32 v18, 0xbfb8aa3b, v14
	v_exp_f32_e32 v18, v18
	v_rcp_f32_e32 v7, v12
	s_nop 0
	v_mul_f32_e32 v7, v16, v7
	v_add_f32_e32 v18, 1.0, v18
	v_rcp_f32_e32 v12, v13
	s_nop 0
	v_mul_f32_e32 v12, v17, v12
	v_mul_f32_e32 v17, 0xbfb8aa3b, v15
	v_exp_f32_e32 v17, v17
	s_nop 0
	v_add_f32_e32 v17, 1.0, v17
	v_rcp_f32_e32 v13, v18
	s_nop 0
	v_mul_f32_e32 v13, v14, v13
	v_pk_mul_f32 v[24:25], v[138:139], s[30:31] op_sel_hi:[1,0]
	v_mul_f32_e32 v7, v7, v24
	v_mul_f32_e32 v12, v12, v25
	v_pk_mul_f32 v[22:23], v[140:141], s[30:31] op_sel_hi:[1,0]
	v_rcp_f32_e32 v14, v17
	s_nop 0
	v_mul_f32_e32 v14, v15, v14
	v_med3_f32 v15, v7, s75, v239
	v_med3_f32 v12, v12, s75, v239
	v_mov_b32_e32 v7, v203
	v_cvt_pk_fp8_f32 v7, v15, v12
	v_mul_f32_e32 v12, v14, v23
	v_pk_mul_f32 v[14:15], v[166:167], s[28:29] op_sel_hi:[1,0]
	v_mul_f32_e32 v13, v13, v22
	v_mul_f32_e32 v16, 0xbfb8aa3b, v14
	v_exp_f32_e32 v22, v16
	v_mul_f32_e32 v33, 0xbfb8aa3b, v15
	v_exp_f32_e32 v33, v33
	v_med3_f32 v13, v13, s75, v239
	v_add_f32_e32 v28, 1.0, v22
	v_med3_f32 v12, v12, s75, v239
	v_cvt_pk_fp8_f32 v7, v13, v12 op_sel:[0,0,1]
	v_pk_mul_f32 v[12:13], v[168:169], s[28:29] op_sel_hi:[1,0]
	s_waitcnt lgkmcnt(0)
	v_add_f32_e32 v31, 1.0, v33
	v_rcp_f32_e32 v29, v28
	s_nop 0
	v_mul_f32_e32 v14, v14, v29
	v_mul_f32_e32 v29, 0xbfb8aa3b, v12
	v_pk_mul_f32 v[22:23], v[134:135], s[30:31] op_sel_hi:[1,0]
	v_exp_f32_e32 v29, v29
	v_mul_f32_e32 v14, v14, v22
	v_add_f32_e32 v29, 1.0, v29
	v_mul_f32_e32 v28, 0xbfb8aa3b, v13
	v_rcp_f32_e32 v22, v31
	s_nop 0
	v_mul_f32_e32 v15, v15, v22
	v_exp_f32_e32 v28, v28
	v_mul_f32_e32 v15, v15, v23
	v_add_f32_e32 v28, 1.0, v28
	v_pk_mul_f32 v[20:21], v[136:137], s[30:31] op_sel_hi:[1,0]
	v_rcp_f32_e32 v22, v29
	s_nop 0
	v_mul_f32_e32 v12, v12, v22
	v_mul_f32_e32 v20, v12, v20
	v_pk_mul_f32 v[18:19], v[162:163], s[28:29] op_sel_hi:[1,0]
	v_rcp_f32_e32 v12, v28
	s_nop 0
	v_mul_f32_e32 v12, v13, v12
	v_mul_f32_e32 v13, v12, v21
	v_mul_f32_e32 v12, 0xbfb8aa3b, v18
	v_exp_f32_e32 v21, v12
	v_med3_f32 v14, v14, s75, v239
	v_med3_f32 v15, v15, s75, v239
	v_mov_b32_e32 v12, v203
	v_cvt_pk_fp8_f32 v12, v14, v15
	v_add_f32_e32 v14, 1.0, v21
	v_med3_f32 v20, v20, s75, v239
	v_med3_f32 v13, v13, s75, v239
	v_cvt_pk_fp8_f32 v12, v20, v13 op_sel:[0,0,1]
	v_mul_f32_e32 v22, 0xbfb8aa3b, v19
	v_exp_f32_e32 v22, v22
	s_nop 0
	v_add_f32_e32 v15, 1.0, v22
	v_pk_mul_f32 v[16:17], v[164:165], s[28:29] op_sel_hi:[1,0]
	v_mul_f32_e32 v20, 0xbfb8aa3b, v16
	v_exp_f32_e32 v20, v20
	v_rcp_f32_e32 v13, v14
	s_nop 0
	v_mul_f32_e32 v13, v18, v13
	v_add_f32_e32 v20, 1.0, v20
	v_rcp_f32_e32 v14, v15
	s_nop 0
	v_mul_f32_e32 v14, v19, v14
	v_mul_f32_e32 v19, 0xbfb8aa3b, v17
	v_exp_f32_e32 v19, v19
	s_nop 0
	v_add_f32_e32 v19, 1.0, v19
	v_rcp_f32_e32 v15, v20
	s_nop 0
	v_mul_f32_e32 v15, v16, v15
	v_pk_mul_f32 v[26:27], v[130:131], s[30:31] op_sel_hi:[1,0]
	v_mul_f32_e32 v13, v13, v26
	v_mul_f32_e32 v14, v14, v27
	v_rcp_f32_e32 v16, v19
	s_nop 0
	v_mul_f32_e32 v16, v17, v16
	v_med3_f32 v17, v13, s75, v239
	v_med3_f32 v14, v14, s75, v239
	v_mov_b32_e32 v13, v203
	v_cvt_pk_fp8_f32 v13, v17, v14
	ds_write_b64 v8, v[2:3]
	ds_write_b64 v8, v[4:5] offset:512
	v_pk_mul_f32 v[24:25], v[132:133], s[30:31] op_sel_hi:[1,0]
	ds_read_b128 v[2:5], v9
	v_mul_f32_e32 v15, v15, v24
	v_mul_f32_e32 v14, v16, v25
	v_med3_f32 v15, v15, s75, v239
	v_med3_f32 v14, v14, s75, v239
	v_cvt_pk_fp8_f32 v13, v15, v14 op_sel:[0,0,1]
	v_lshl_add_u32 v10, v10, 9, v11
	s_waitcnt lgkmcnt(0)
	global_store_dwordx4 v10, v[2:5], s[16:17]
	ds_write_b64 v8, v[6:7] offset:1024
	ds_write_b64 v8, v[12:13] offset:1536
	v_pk_mul_f32 v[12:13], v[126:127], s[28:29] op_sel_hi:[1,0]
	v_pk_mul_f32 v[6:7], v[128:129], s[28:29] op_sel_hi:[1,0]
	v_mul_f32_e32 v11, 0xbfb8aa3b, v12
	v_exp_f32_e32 v11, v11
	v_mul_f32_e32 v30, 0xbfb8aa3b, v13
	v_exp_f32_e32 v30, v30
	v_pk_mul_f32 v[20:21], v[94:95], s[30:31] op_sel_hi:[1,0]
	v_add_f32_e32 v11, 1.0, v11
	v_pk_mul_f32 v[18:19], v[96:97], s[30:31] op_sel_hi:[1,0]
	v_pk_mul_f32 v[16:17], v[122:123], s[28:29] op_sel_hi:[1,0]
	v_pk_mul_f32 v[14:15], v[124:125], s[28:29] op_sel_hi:[1,0]
	v_add_f32_e32 v28, 1.0, v30
	v_rcp_f32_e32 v11, v11
	s_nop 0
	v_mul_f32_e32 v11, v12, v11
	v_mul_f32_e32 v26, 0xbfb8aa3b, v6
	v_exp_f32_e32 v26, v26
	v_mul_f32_e32 v11, v20, v11
	v_add_f32_e32 v26, 1.0, v26
	v_rcp_f32_e32 v12, v28
	s_nop 0
	v_mul_f32_e32 v12, v13, v12
	v_mul_f32_e32 v12, v21, v12
	v_mul_f32_e32 v21, 0xbfb8aa3b, v7
	v_exp_f32_e32 v21, v21
	s_nop 0
	v_add_f32_e32 v21, 1.0, v21
	v_rcp_f32_e32 v13, v26
	s_nop 0
	v_mul_f32_e32 v6, v6, v13
	v_mul_f32_e32 v13, v18, v6
	v_rcp_f32_e32 v6, v21
	s_nop 0
	v_mul_f32_e32 v6, v7, v6
	v_mul_f32_e32 v7, v19, v6
	v_mul_f32_e32 v6, 0xbfb8aa3b, v16
	v_exp_f32_e32 v18, v6
	v_med3_f32 v11, v11, s75, v239
	v_med3_f32 v12, v12, s75, v239
	v_mov_b32_e32 v6, v203
	v_cvt_pk_fp8_f32 v6, v11, v12
	v_add_f32_e32 v11, 1.0, v18
	v_med3_f32 v13, v13, s75, v239
	v_med3_f32 v7, v7, s75, v239
	v_cvt_pk_fp8_f32 v6, v13, v7 op_sel:[0,0,1]
	v_mul_f32_e32 v19, 0xbfb8aa3b, v17
	v_exp_f32_e32 v19, v19
	s_nop 0
	v_add_f32_e32 v12, 1.0, v19
	v_rcp_f32_e32 v7, v11
	s_nop 0
	v_mul_f32_e32 v7, v16, v7
	v_mul_f32_e32 v16, 0xbfb8aa3b, v14
	v_exp_f32_e32 v16, v16
	s_nop 0
	v_add_f32_e32 v16, 1.0, v16
	v_rcp_f32_e32 v11, v12
	s_nop 0
	v_mul_f32_e32 v11, v17, v11
	v_mul_f32_e32 v17, 0xbfb8aa3b, v15
	v_exp_f32_e32 v17, v17
	s_nop 0
	v_add_f32_e32 v17, 1.0, v17
	v_rcp_f32_e32 v12, v16
	s_nop 0
	v_mul_f32_e32 v12, v14, v12
	v_pk_mul_f32 v[24:25], v[90:91], s[30:31] op_sel_hi:[1,0]
	v_mul_f32_e32 v7, v24, v7
	v_mul_f32_e32 v11, v25, v11
	v_med3_f32 v14, v7, s75, v239
	v_med3_f32 v11, v11, s75, v239
	v_mov_b32_e32 v7, v203
	v_cvt_pk_fp8_f32 v7, v14, v11
	v_pk_mul_f32 v[22:23], v[92:93], s[30:31] op_sel_hi:[1,0]
	v_rcp_f32_e32 v13, v17
	s_nop 0
	v_mul_f32_e32 v13, v15, v13
	v_mul_f32_e32 v12, v22, v12
	v_mul_f32_e32 v11, v23, v13
	v_med3_f32 v12, v12, s75, v239
	v_med3_f32 v11, v11, s75, v239
	v_pk_mul_f32 v[14:15], v[118:119], s[28:29] op_sel_hi:[1,0]
	v_cvt_pk_fp8_f32 v7, v12, v11 op_sel:[0,0,1]
	v_mul_f32_e32 v11, 0xbfb8aa3b, v14
	v_exp_f32_e32 v11, v11
	v_mul_f32_e32 v32, 0xbfb8aa3b, v15
	v_exp_f32_e32 v32, v32
	v_pk_mul_f32 v[12:13], v[120:121], s[28:29] op_sel_hi:[1,0]
	v_add_f32_e32 v11, 1.0, v11
	v_pk_mul_f32 v[22:23], v[86:87], s[30:31] op_sel_hi:[1,0]
	v_pk_mul_f32 v[20:21], v[88:89], s[30:31] op_sel_hi:[1,0]
	v_pk_mul_f32 v[18:19], v[114:115], s[28:29] op_sel_hi:[1,0]
	v_add_f32_e32 v30, 1.0, v32
	v_rcp_f32_e32 v11, v11
	s_nop 0
	v_mul_f32_e32 v11, v14, v11
	v_mul_f32_e32 v28, 0xbfb8aa3b, v12
	v_exp_f32_e32 v28, v28
	v_mul_f32_e32 v11, v22, v11
	v_add_f32_e32 v28, 1.0, v28
	v_rcp_f32_e32 v14, v30
	s_nop 0
	v_mul_f32_e32 v14, v15, v14
	v_mul_f32_e32 v14, v23, v14
	v_mul_f32_e32 v23, 0xbfb8aa3b, v13
	v_exp_f32_e32 v23, v23
	s_nop 0
	v_add_f32_e32 v23, 1.0, v23
	v_rcp_f32_e32 v15, v28
	s_nop 0
	v_mul_f32_e32 v12, v12, v15
	v_mul_f32_e32 v15, v20, v12
	v_rcp_f32_e32 v12, v23
	s_nop 0
	v_mul_f32_e32 v12, v13, v12
	v_mul_f32_e32 v13, v21, v12
	v_mul_f32_e32 v12, 0xbfb8aa3b, v18
	v_exp_f32_e32 v20, v12
	v_med3_f32 v11, v11, s75, v239
	v_med3_f32 v14, v14, s75, v239
	v_mov_b32_e32 v12, v203
	v_cvt_pk_fp8_f32 v12, v11, v14
	v_add_f32_e32 v11, 1.0, v20
	v_med3_f32 v15, v15, s75, v239
	v_med3_f32 v13, v13, s75, v239
	v_cvt_pk_fp8_f32 v12, v15, v13 op_sel:[0,0,1]
	v_mul_f32_e32 v21, 0xbfb8aa3b, v19
	v_exp_f32_e32 v21, v21
	s_nop 0
	v_add_f32_e32 v14, 1.0, v21
	v_pk_mul_f32 v[16:17], v[116:117], s[28:29] op_sel_hi:[1,0]
	v_rcp_f32_e32 v11, v11
	s_nop 0
	v_mul_f32_e32 v11, v18, v11
	v_mul_f32_e32 v18, 0xbfb8aa3b, v16
	v_exp_f32_e32 v18, v18
	s_nop 0
	v_add_f32_e32 v18, 1.0, v18
	v_rcp_f32_e32 v13, v14
	s_nop 0
	v_mul_f32_e32 v13, v19, v13
	v_mul_f32_e32 v19, 0xbfb8aa3b, v17
	v_exp_f32_e32 v19, v19
	s_nop 0
	v_add_f32_e32 v19, 1.0, v19
	v_rcp_f32_e32 v14, v18
	s_nop 0
	v_mul_f32_e32 v14, v16, v14
	v_pk_mul_f32 v[26:27], v[82:83], s[30:31] op_sel_hi:[1,0]
	v_mul_f32_e32 v11, v26, v11
	v_mul_f32_e32 v13, v27, v13
	v_med3_f32 v11, v11, s75, v239
	v_med3_f32 v16, v13, s75, v239
	v_mov_b32_e32 v13, v203
	v_cvt_pk_fp8_f32 v13, v11, v16
	v_pk_mul_f32 v[24:25], v[84:85], s[30:31] op_sel_hi:[1,0]
	v_rcp_f32_e32 v15, v19
	s_nop 0
	v_mul_f32_e32 v15, v17, v15
	ds_read_b128 v[2:5], v9 offset:1024
	v_mul_f32_e32 v14, v24, v14
	v_mul_f32_e32 v11, v25, v15
	v_med3_f32 v14, v14, s75, v239
	v_med3_f32 v11, v11, s75, v239
	v_cvt_pk_fp8_f32 v13, v14, v11 op_sel:[0,0,1]
	v_add_u32_e32 v11, 0x4000, v10
	s_waitcnt lgkmcnt(0)
	global_store_dwordx4 v11, v[2:5], s[16:17]
	ds_write_b64 v8, v[6:7]
	ds_write_b64 v8, v[12:13] offset:512
	v_pk_mul_f32 v[12:13], v[110:111], s[28:29] op_sel_hi:[1,0]
	v_pk_mul_f32 v[6:7], v[112:113], s[28:29] op_sel_hi:[1,0]
	v_mul_f32_e32 v11, 0xbfb8aa3b, v12
	v_exp_f32_e32 v11, v11
	v_mul_f32_e32 v30, 0xbfb8aa3b, v13
	v_exp_f32_e32 v30, v30
	v_pk_mul_f32 v[20:21], v[78:79], s[30:31] op_sel_hi:[1,0]
	v_add_f32_e32 v11, 1.0, v11
	v_pk_mul_f32 v[18:19], v[80:81], s[30:31] op_sel_hi:[1,0]
	v_pk_mul_f32 v[16:17], v[106:107], s[28:29] op_sel_hi:[1,0]
	v_pk_mul_f32 v[14:15], v[108:109], s[28:29] op_sel_hi:[1,0]
	v_add_f32_e32 v28, 1.0, v30
	v_rcp_f32_e32 v11, v11
	s_nop 0
	v_mul_f32_e32 v11, v12, v11
	v_mul_f32_e32 v26, 0xbfb8aa3b, v6
	v_exp_f32_e32 v26, v26
	v_mul_f32_e32 v11, v20, v11
	v_add_f32_e32 v26, 1.0, v26
	v_rcp_f32_e32 v12, v28
	s_nop 0
	v_mul_f32_e32 v12, v13, v12
	v_mul_f32_e32 v12, v21, v12
	v_mul_f32_e32 v21, 0xbfb8aa3b, v7
	v_exp_f32_e32 v21, v21
	s_nop 0
	v_add_f32_e32 v21, 1.0, v21
	v_rcp_f32_e32 v13, v26
	s_nop 0
	v_mul_f32_e32 v6, v6, v13
	v_mul_f32_e32 v13, v18, v6
	v_rcp_f32_e32 v6, v21
	s_nop 0
	v_mul_f32_e32 v6, v7, v6
	v_mul_f32_e32 v7, v19, v6
	v_mul_f32_e32 v6, 0xbfb8aa3b, v16
	v_exp_f32_e32 v18, v6
	v_med3_f32 v11, v11, s75, v239
	v_med3_f32 v12, v12, s75, v239
	v_mov_b32_e32 v6, v203
	v_cvt_pk_fp8_f32 v6, v11, v12
	v_add_f32_e32 v11, 1.0, v18
	v_med3_f32 v13, v13, s75, v239
	v_med3_f32 v7, v7, s75, v239
	v_cvt_pk_fp8_f32 v6, v13, v7 op_sel:[0,0,1]
	v_mul_f32_e32 v19, 0xbfb8aa3b, v17
	v_exp_f32_e32 v19, v19
	s_nop 0
	v_add_f32_e32 v12, 1.0, v19
	v_rcp_f32_e32 v7, v11
	s_nop 0
	v_mul_f32_e32 v7, v16, v7
	v_mul_f32_e32 v16, 0xbfb8aa3b, v14
	v_exp_f32_e32 v16, v16
	s_nop 0
	v_add_f32_e32 v16, 1.0, v16
	v_rcp_f32_e32 v11, v12
	s_nop 0
	v_mul_f32_e32 v11, v17, v11
	v_mul_f32_e32 v17, 0xbfb8aa3b, v15
	v_exp_f32_e32 v17, v17
	s_nop 0
	v_add_f32_e32 v17, 1.0, v17
	v_rcp_f32_e32 v12, v16
	s_nop 0
	v_mul_f32_e32 v12, v14, v12
	v_pk_mul_f32 v[24:25], v[74:75], s[30:31] op_sel_hi:[1,0]
	v_mul_f32_e32 v7, v24, v7
	v_mul_f32_e32 v11, v25, v11
	v_med3_f32 v14, v7, s75, v239
	v_med3_f32 v11, v11, s75, v239
	v_mov_b32_e32 v7, v203
	v_cvt_pk_fp8_f32 v7, v14, v11
	v_pk_mul_f32 v[22:23], v[76:77], s[30:31] op_sel_hi:[1,0]
	v_rcp_f32_e32 v13, v17
	s_nop 0
	v_mul_f32_e32 v13, v15, v13
	v_mul_f32_e32 v12, v22, v12
	v_mul_f32_e32 v11, v23, v13
	v_med3_f32 v12, v12, s75, v239
	v_med3_f32 v11, v11, s75, v239
	v_pk_mul_f32 v[14:15], v[102:103], s[28:29] op_sel_hi:[1,0]
	v_cvt_pk_fp8_f32 v7, v12, v11 op_sel:[0,0,1]
	v_mul_f32_e32 v11, 0xbfb8aa3b, v14
	v_exp_f32_e32 v11, v11
	v_mul_f32_e32 v32, 0xbfb8aa3b, v15
	v_exp_f32_e32 v32, v32
	v_pk_mul_f32 v[12:13], v[104:105], s[28:29] op_sel_hi:[1,0]
	v_add_f32_e32 v11, 1.0, v11
	v_pk_mul_f32 v[22:23], v[70:71], s[30:31] op_sel_hi:[1,0]
	v_pk_mul_f32 v[20:21], v[72:73], s[30:31] op_sel_hi:[1,0]
	v_pk_mul_f32 v[18:19], v[98:99], s[28:29] op_sel_hi:[1,0]
	v_add_f32_e32 v30, 1.0, v32
	v_rcp_f32_e32 v11, v11
	s_nop 0
	v_mul_f32_e32 v11, v14, v11
	v_mul_f32_e32 v28, 0xbfb8aa3b, v12
	v_exp_f32_e32 v28, v28
	v_mul_f32_e32 v11, v22, v11
	v_add_f32_e32 v28, 1.0, v28
	v_rcp_f32_e32 v14, v30
	s_nop 0
	v_mul_f32_e32 v14, v15, v14
	v_mul_f32_e32 v14, v23, v14
	v_mul_f32_e32 v23, 0xbfb8aa3b, v13
	v_exp_f32_e32 v23, v23
	s_nop 0
	v_add_f32_e32 v23, 1.0, v23
	v_rcp_f32_e32 v15, v28
	s_nop 0
	v_mul_f32_e32 v12, v12, v15
	v_mul_f32_e32 v15, v20, v12
	v_rcp_f32_e32 v12, v23
	s_nop 0
	v_mul_f32_e32 v12, v13, v12
	v_mul_f32_e32 v13, v21, v12
	v_mul_f32_e32 v12, 0xbfb8aa3b, v18
	v_exp_f32_e32 v20, v12
	v_med3_f32 v11, v11, s75, v239
	v_med3_f32 v14, v14, s75, v239
	v_mov_b32_e32 v12, v203
	v_cvt_pk_fp8_f32 v12, v11, v14
	v_add_f32_e32 v11, 1.0, v20
	v_med3_f32 v15, v15, s75, v239
	v_med3_f32 v13, v13, s75, v239
	v_cvt_pk_fp8_f32 v12, v15, v13 op_sel:[0,0,1]
	v_mul_f32_e32 v21, 0xbfb8aa3b, v19
	v_exp_f32_e32 v21, v21
	s_nop 0
	v_add_f32_e32 v14, 1.0, v21
	v_pk_mul_f32 v[16:17], v[100:101], s[28:29] op_sel_hi:[1,0]
	v_rcp_f32_e32 v11, v11
	s_nop 0
	v_mul_f32_e32 v11, v18, v11
	v_mul_f32_e32 v18, 0xbfb8aa3b, v16
	v_exp_f32_e32 v18, v18
	s_nop 0
	v_add_f32_e32 v18, 1.0, v18
	v_rcp_f32_e32 v13, v14
	s_nop 0
	v_mul_f32_e32 v13, v19, v13
	v_mul_f32_e32 v19, 0xbfb8aa3b, v17
	v_exp_f32_e32 v19, v19
	s_nop 0
	v_add_f32_e32 v19, 1.0, v19
	v_rcp_f32_e32 v14, v18
	s_nop 0
	v_mul_f32_e32 v14, v16, v14
	v_pk_mul_f32 v[26:27], v[66:67], s[30:31] op_sel_hi:[1,0]
	v_mul_f32_e32 v11, v26, v11
	v_mul_f32_e32 v13, v27, v13
	v_med3_f32 v11, v11, s75, v239
	v_med3_f32 v16, v13, s75, v239
	v_mov_b32_e32 v13, v203
	v_cvt_pk_fp8_f32 v13, v11, v16
	v_pk_mul_f32 v[24:25], v[68:69], s[30:31] op_sel_hi:[1,0]
	v_rcp_f32_e32 v15, v19
	s_nop 0
	v_mul_f32_e32 v15, v17, v15
	ds_read_b128 v[2:5], v9
	v_mul_f32_e32 v14, v24, v14
	v_mul_f32_e32 v11, v25, v15
	v_med3_f32 v14, v14, s75, v239
	v_med3_f32 v11, v11, s75, v239
	v_cvt_pk_fp8_f32 v13, v14, v11 op_sel:[0,0,1]
	v_add_u32_e32 v11, 0x10000, v10
	s_waitcnt lgkmcnt(0)
	global_store_dwordx4 v11, v[2:5], s[16:17]
	ds_write_b64 v8, v[6:7] offset:1024
	ds_write_b64 v8, v[12:13] offset:1536
	ds_read_b128 v[2:5], v9 offset:1024
	v_add_u32_e32 v6, 0x14000, v10
	s_andn2_b64 vcc, exec, s[42:43]
	s_waitcnt lgkmcnt(0)
	global_store_dwordx4 v6, v[2:5], s[16:17]
	s_cbranch_vccnz .LBB0_1680
	s_andn2_b64 vcc, exec, s[20:21]
	s_cbranch_vccnz .LBB0_1647
	s_barrier
	s_branch .LBB0_1647

.LBB0_1853:
	v_mov_b32_e32 v2, v232
	s_add_u32 s0, s79, 0xffffff00
	s_nop 15
	s_nop 15
	s_nop 15
	s_addc_u32 s1, s80, -1
	v_lshlrev_b32_e32 v3, 5, v2
	v_ashrrev_i32_e32 v4, 1, v2
	v_and_b32_e32 v3, 0x1e0, v3
	v_and_b32_e32 v5, -8, v4
	s_add_i32 s2, s33, s69
	v_add3_u32 v8, s53, v3, v5
	v_add_u32_e32 v10, s2, v4
	v_pk_mul_f32 v[4:5], v[190:191], s[28:29] op_sel_hi:[1,0]
	v_lshlrev_b32_e32 v2, 4, v2
	v_mul_f32_e32 v6, 0xbfb8aa3b, v4
	v_exp_f32_e32 v16, v6
	v_mul_f32_e32 v27, 0xbfb8aa3b, v5
	v_exp_f32_e32 v27, v27
	v_add_u32_e32 v9, s53, v2
	v_add_f32_e32 v22, 1.0, v16
	v_and_b32_e32 v11, 16, v2
	v_pk_mul_f32 v[2:3], v[192:193], s[28:29] op_sel_hi:[1,0]
	v_pk_mul_f32 v[16:17], v[158:159], s[30:31] op_sel_hi:[1,0]
	v_add_f32_e32 v25, 1.0, v27
	v_rcp_f32_e32 v23, v22
	s_nop 0
	v_mul_f32_e32 v4, v4, v23
	v_mul_f32_e32 v23, 0xbfb8aa3b, v2
	v_exp_f32_e32 v23, v23
	v_mul_f32_e32 v4, v4, v16
	v_add_f32_e32 v23, 1.0, v23
	v_mul_f32_e32 v22, 0xbfb8aa3b, v3
	v_rcp_f32_e32 v16, v25
	s_nop 0
	v_mul_f32_e32 v5, v5, v16
	v_exp_f32_e32 v22, v22
	v_mul_f32_e32 v5, v5, v17
	v_add_f32_e32 v22, 1.0, v22
	v_pk_mul_f32 v[14:15], v[160:161], s[30:31] op_sel_hi:[1,0]
	v_rcp_f32_e32 v16, v23
	s_nop 0
	v_mul_f32_e32 v2, v2, v16
	v_mul_f32_e32 v14, v2, v14
	v_pk_mul_f32 v[12:13], v[186:187], s[28:29] op_sel_hi:[1,0]
	v_rcp_f32_e32 v2, v22
	s_nop 0
	v_mul_f32_e32 v2, v3, v2
	v_mul_f32_e32 v3, v2, v15
	v_mul_f32_e32 v2, 0xbfb8aa3b, v12
	v_exp_f32_e32 v15, v2
	v_med3_f32 v4, v4, s75, v233
	v_med3_f32 v5, v5, s75, v233
	v_mov_b32_e32 v2, v203
	v_cvt_pk_fp8_f32 v2, v4, v5
	v_add_f32_e32 v4, 1.0, v15
	v_med3_f32 v14, v14, s75, v233
	v_med3_f32 v3, v3, s75, v233
	v_cvt_pk_fp8_f32 v2, v14, v3 op_sel:[0,0,1]
	v_mul_f32_e32 v16, 0xbfb8aa3b, v13
	v_exp_f32_e32 v16, v16
	s_nop 0
	v_add_f32_e32 v5, 1.0, v16
	v_pk_mul_f32 v[6:7], v[188:189], s[28:29] op_sel_hi:[1,0]
	v_mul_f32_e32 v14, 0xbfb8aa3b, v6
	v_exp_f32_e32 v14, v14
	v_rcp_f32_e32 v3, v4
	s_nop 0
	v_mul_f32_e32 v3, v12, v3
	v_add_f32_e32 v14, 1.0, v14
	v_rcp_f32_e32 v4, v5
	s_nop 0
	v_mul_f32_e32 v4, v13, v4
	v_mul_f32_e32 v13, 0xbfb8aa3b, v7
	v_exp_f32_e32 v13, v13
	s_nop 0
	v_add_f32_e32 v13, 1.0, v13
	v_rcp_f32_e32 v5, v14
	s_nop 0
	v_mul_f32_e32 v5, v6, v5
	v_pk_mul_f32 v[20:21], v[154:155], s[30:31] op_sel_hi:[1,0]
	v_mul_f32_e32 v3, v3, v20
	v_mul_f32_e32 v4, v4, v21
	v_pk_mul_f32 v[18:19], v[156:157], s[30:31] op_sel_hi:[1,0]
	v_rcp_f32_e32 v6, v13
	s_nop 0
	v_mul_f32_e32 v6, v7, v6
	v_med3_f32 v7, v3, s75, v233
	v_med3_f32 v4, v4, s75, v233
	v_mov_b32_e32 v3, v203
	v_cvt_pk_fp8_f32 v3, v7, v4
	v_mul_f32_e32 v4, v6, v19
	v_pk_mul_f32 v[6:7], v[182:183], s[28:29] op_sel_hi:[1,0]
	v_mul_f32_e32 v5, v5, v18
	v_mul_f32_e32 v12, 0xbfb8aa3b, v6
	v_exp_f32_e32 v18, v12
	v_mul_f32_e32 v29, 0xbfb8aa3b, v7
	v_exp_f32_e32 v29, v29
	v_med3_f32 v5, v5, s75, v233
	v_add_f32_e32 v24, 1.0, v18
	v_med3_f32 v4, v4, s75, v233
	v_cvt_pk_fp8_f32 v3, v5, v4 op_sel:[0,0,1]
	v_pk_mul_f32 v[4:5], v[184:185], s[28:29] op_sel_hi:[1,0]
	v_add_f32_e32 v27, 1.0, v29
	v_rcp_f32_e32 v25, v24
	s_nop 0
	v_mul_f32_e32 v6, v6, v25
	v_mul_f32_e32 v25, 0xbfb8aa3b, v4
	v_pk_mul_f32 v[18:19], v[150:151], s[30:31] op_sel_hi:[1,0]
	v_exp_f32_e32 v25, v25
	v_mul_f32_e32 v6, v6, v18
	v_add_f32_e32 v25, 1.0, v25
	v_mul_f32_e32 v24, 0xbfb8aa3b, v5
	v_rcp_f32_e32 v18, v27
	s_nop 0
	v_mul_f32_e32 v7, v7, v18
	v_exp_f32_e32 v24, v24
	v_mul_f32_e32 v7, v7, v19
	v_add_f32_e32 v24, 1.0, v24
	v_pk_mul_f32 v[16:17], v[152:153], s[30:31] op_sel_hi:[1,0]
	v_rcp_f32_e32 v18, v25
	s_nop 0
	v_mul_f32_e32 v4, v4, v18
	v_mul_f32_e32 v16, v4, v16
	v_pk_mul_f32 v[14:15], v[178:179], s[28:29] op_sel_hi:[1,0]
	v_rcp_f32_e32 v4, v24
	s_nop 0
	v_mul_f32_e32 v4, v5, v4
	v_mul_f32_e32 v5, v4, v17
	v_mul_f32_e32 v4, 0xbfb8aa3b, v14
	v_exp_f32_e32 v17, v4
	v_med3_f32 v6, v6, s75, v233
	v_med3_f32 v7, v7, s75, v233
	v_mov_b32_e32 v4, v203
	v_cvt_pk_fp8_f32 v4, v6, v7
	v_add_f32_e32 v6, 1.0, v17
	v_med3_f32 v16, v16, s75, v233
	v_med3_f32 v5, v5, s75, v233
	v_cvt_pk_fp8_f32 v4, v16, v5 op_sel:[0,0,1]
	v_mul_f32_e32 v18, 0xbfb8aa3b, v15
	v_exp_f32_e32 v18, v18
	s_nop 0
	v_add_f32_e32 v7, 1.0, v18
	v_pk_mul_f32 v[12:13], v[180:181], s[28:29] op_sel_hi:[1,0]
	v_mul_f32_e32 v16, 0xbfb8aa3b, v12
	v_exp_f32_e32 v16, v16
	v_rcp_f32_e32 v5, v6
	s_nop 0
	v_mul_f32_e32 v5, v14, v5
	v_add_f32_e32 v16, 1.0, v16
	v_rcp_f32_e32 v6, v7
	s_nop 0
	v_mul_f32_e32 v6, v15, v6
	v_mul_f32_e32 v15, 0xbfb8aa3b, v13
	v_exp_f32_e32 v15, v15
	s_nop 0
	v_add_f32_e32 v15, 1.0, v15
	v_rcp_f32_e32 v7, v16
	s_nop 0
	v_mul_f32_e32 v7, v12, v7
	v_pk_mul_f32 v[22:23], v[146:147], s[30:31] op_sel_hi:[1,0]
	v_mul_f32_e32 v5, v5, v22
	v_mul_f32_e32 v6, v6, v23
	v_pk_mul_f32 v[20:21], v[148:149], s[30:31] op_sel_hi:[1,0]
	v_rcp_f32_e32 v12, v15
	s_nop 0
	v_mul_f32_e32 v12, v13, v12
	v_med3_f32 v13, v5, s75, v233
	v_med3_f32 v6, v6, s75, v233
	v_mov_b32_e32 v5, v203
	v_cvt_pk_fp8_f32 v5, v13, v6
	v_mul_f32_e32 v6, v12, v21
	v_pk_mul_f32 v[12:13], v[174:175], s[28:29] op_sel_hi:[1,0]
	v_mul_f32_e32 v7, v7, v20
	v_mul_f32_e32 v14, 0xbfb8aa3b, v12
	v_exp_f32_e32 v20, v14
	v_mul_f32_e32 v31, 0xbfb8aa3b, v13
	v_exp_f32_e32 v31, v31
	v_med3_f32 v7, v7, s75, v233
	v_add_f32_e32 v26, 1.0, v20
	v_med3_f32 v6, v6, s75, v233
	v_cvt_pk_fp8_f32 v5, v7, v6 op_sel:[0,0,1]
	v_lshl_or_b32 v6, s18, 7, v11
	v_add_f32_e32 v29, 1.0, v31
	v_or_b32_e32 v11, s70, v6
	v_pk_mul_f32 v[6:7], v[176:177], s[28:29] op_sel_hi:[1,0]
	v_rcp_f32_e32 v27, v26
	s_nop 0
	v_mul_f32_e32 v12, v12, v27
	v_mul_f32_e32 v27, 0xbfb8aa3b, v6
	v_pk_mul_f32 v[20:21], v[142:143], s[30:31] op_sel_hi:[1,0]
	v_exp_f32_e32 v27, v27
	v_mul_f32_e32 v12, v12, v20
	v_add_f32_e32 v27, 1.0, v27
	v_mul_f32_e32 v26, 0xbfb8aa3b, v7
	v_rcp_f32_e32 v20, v29
	s_nop 0
	v_mul_f32_e32 v13, v13, v20
	v_exp_f32_e32 v26, v26
	v_mul_f32_e32 v13, v13, v21
	v_add_f32_e32 v26, 1.0, v26
	v_pk_mul_f32 v[18:19], v[144:145], s[30:31] op_sel_hi:[1,0]
	v_rcp_f32_e32 v20, v27
	s_nop 0
	v_mul_f32_e32 v6, v6, v20
	v_mul_f32_e32 v18, v6, v18
	v_pk_mul_f32 v[16:17], v[170:171], s[28:29] op_sel_hi:[1,0]
	v_rcp_f32_e32 v6, v26
	s_nop 0
	v_mul_f32_e32 v6, v7, v6
	v_mul_f32_e32 v7, v6, v19
	v_mul_f32_e32 v6, 0xbfb8aa3b, v16
	v_exp_f32_e32 v19, v6
	v_med3_f32 v12, v12, s75, v233
	v_med3_f32 v13, v13, s75, v233
	v_mov_b32_e32 v6, v203
	v_cvt_pk_fp8_f32 v6, v12, v13
	v_add_f32_e32 v12, 1.0, v19
	v_med3_f32 v18, v18, s75, v233
	v_med3_f32 v7, v7, s75, v233
	v_cvt_pk_fp8_f32 v6, v18, v7 op_sel:[0,0,1]
	v_mul_f32_e32 v20, 0xbfb8aa3b, v17
	v_exp_f32_e32 v20, v20
	s_nop 0
	v_add_f32_e32 v13, 1.0, v20
	v_pk_mul_f32 v[14:15], v[172:173], s[28:29] op_sel_hi:[1,0]
	v_mul_f32_e32 v18, 0xbfb8aa3b, v14
	v_exp_f32_e32 v18, v18
	v_rcp_f32_e32 v7, v12
	s_nop 0
	v_mul_f32_e32 v7, v16, v7
	v_add_f32_e32 v18, 1.0, v18
	v_rcp_f32_e32 v12, v13
	s_nop 0
	v_mul_f32_e32 v12, v17, v12
	v_mul_f32_e32 v17, 0xbfb8aa3b, v15
	v_exp_f32_e32 v17, v17
	s_nop 0
	v_add_f32_e32 v17, 1.0, v17
	v_rcp_f32_e32 v13, v18
	s_nop 0
	v_mul_f32_e32 v13, v14, v13
	v_pk_mul_f32 v[24:25], v[138:139], s[30:31] op_sel_hi:[1,0]
	v_mul_f32_e32 v7, v7, v24
	v_mul_f32_e32 v12, v12, v25
	v_pk_mul_f32 v[22:23], v[140:141], s[30:31] op_sel_hi:[1,0]
	v_rcp_f32_e32 v14, v17
	s_nop 0
	v_mul_f32_e32 v14, v15, v14
	v_med3_f32 v15, v7, s75, v233
	v_med3_f32 v12, v12, s75, v233
	v_mov_b32_e32 v7, v203
	v_cvt_pk_fp8_f32 v7, v15, v12
	v_mul_f32_e32 v12, v14, v23
	v_pk_mul_f32 v[14:15], v[166:167], s[28:29] op_sel_hi:[1,0]
	v_mul_f32_e32 v13, v13, v22
	v_mul_f32_e32 v16, 0xbfb8aa3b, v14
	v_exp_f32_e32 v22, v16
	v_mul_f32_e32 v33, 0xbfb8aa3b, v15
	v_exp_f32_e32 v33, v33
	v_med3_f32 v13, v13, s75, v233
	v_add_f32_e32 v28, 1.0, v22
	v_med3_f32 v12, v12, s75, v233
	v_cvt_pk_fp8_f32 v7, v13, v12 op_sel:[0,0,1]
	v_pk_mul_f32 v[12:13], v[168:169], s[28:29] op_sel_hi:[1,0]
	s_waitcnt lgkmcnt(0)
	v_add_f32_e32 v31, 1.0, v33
	v_rcp_f32_e32 v29, v28
	s_nop 0
	v_mul_f32_e32 v14, v14, v29
	v_mul_f32_e32 v29, 0xbfb8aa3b, v12
	v_pk_mul_f32 v[22:23], v[134:135], s[30:31] op_sel_hi:[1,0]
	v_exp_f32_e32 v29, v29
	v_mul_f32_e32 v14, v14, v22
	v_add_f32_e32 v29, 1.0, v29
	v_mul_f32_e32 v28, 0xbfb8aa3b, v13
	v_rcp_f32_e32 v22, v31
	s_nop 0
	v_mul_f32_e32 v15, v15, v22
	v_exp_f32_e32 v28, v28
	v_mul_f32_e32 v15, v15, v23
	v_add_f32_e32 v28, 1.0, v28
	v_pk_mul_f32 v[20:21], v[136:137], s[30:31] op_sel_hi:[1,0]
	v_rcp_f32_e32 v22, v29
	s_nop 0
	v_mul_f32_e32 v12, v12, v22
	v_mul_f32_e32 v20, v12, v20
	v_pk_mul_f32 v[18:19], v[162:163], s[28:29] op_sel_hi:[1,0]
	v_rcp_f32_e32 v12, v28
	s_nop 0
	v_mul_f32_e32 v12, v13, v12
	v_mul_f32_e32 v13, v12, v21
	v_mul_f32_e32 v12, 0xbfb8aa3b, v18
	v_exp_f32_e32 v21, v12
	v_med3_f32 v14, v14, s75, v233
	v_med3_f32 v15, v15, s75, v233
	v_mov_b32_e32 v12, v203
	v_cvt_pk_fp8_f32 v12, v14, v15
	v_add_f32_e32 v14, 1.0, v21
	v_med3_f32 v20, v20, s75, v233
	v_med3_f32 v13, v13, s75, v233
	v_cvt_pk_fp8_f32 v12, v20, v13 op_sel:[0,0,1]
	v_mul_f32_e32 v22, 0xbfb8aa3b, v19
	v_exp_f32_e32 v22, v22
	s_nop 0
	v_add_f32_e32 v15, 1.0, v22
	v_pk_mul_f32 v[16:17], v[164:165], s[28:29] op_sel_hi:[1,0]
	v_mul_f32_e32 v20, 0xbfb8aa3b, v16
	v_exp_f32_e32 v20, v20
	v_rcp_f32_e32 v13, v14
	s_nop 0
	v_mul_f32_e32 v13, v18, v13
	v_add_f32_e32 v20, 1.0, v20
	v_rcp_f32_e32 v14, v15
	s_nop 0
	v_mul_f32_e32 v14, v19, v14
	v_mul_f32_e32 v19, 0xbfb8aa3b, v17
	v_exp_f32_e32 v19, v19
	s_nop 0
	v_add_f32_e32 v19, 1.0, v19
	v_rcp_f32_e32 v15, v20
	s_nop 0
	v_mul_f32_e32 v15, v16, v15
	v_pk_mul_f32 v[26:27], v[130:131], s[30:31] op_sel_hi:[1,0]
	v_mul_f32_e32 v13, v13, v26
	v_mul_f32_e32 v14, v14, v27
	v_rcp_f32_e32 v16, v19
	s_nop 0
	v_mul_f32_e32 v16, v17, v16
	v_med3_f32 v17, v13, s75, v233
	v_med3_f32 v14, v14, s75, v233
	v_mov_b32_e32 v13, v203
	v_cvt_pk_fp8_f32 v13, v17, v14
	ds_write_b64 v8, v[2:3]
	ds_write_b64 v8, v[4:5] offset:512
	v_pk_mul_f32 v[24:25], v[132:133], s[30:31] op_sel_hi:[1,0]
	ds_read_b128 v[2:5], v9
	v_mul_f32_e32 v15, v15, v24
	v_mul_f32_e32 v14, v16, v25
	v_med3_f32 v15, v15, s75, v233
	v_med3_f32 v14, v14, s75, v233
	v_cvt_pk_fp8_f32 v13, v15, v14 op_sel:[0,0,1]
	v_lshl_add_u32 v10, v10, 9, v11
	s_waitcnt lgkmcnt(0)
	global_store_dwordx4 v10, v[2:5], s[16:17]
	ds_write_b64 v8, v[6:7] offset:1024
	ds_write_b64 v8, v[12:13] offset:1536
	v_pk_mul_f32 v[12:13], v[126:127], s[28:29] op_sel_hi:[1,0]
	v_pk_mul_f32 v[6:7], v[128:129], s[28:29] op_sel_hi:[1,0]
	v_mul_f32_e32 v11, 0xbfb8aa3b, v12
	v_exp_f32_e32 v11, v11
	v_mul_f32_e32 v30, 0xbfb8aa3b, v13
	v_exp_f32_e32 v30, v30
	v_pk_mul_f32 v[20:21], v[94:95], s[30:31] op_sel_hi:[1,0]
	v_add_f32_e32 v11, 1.0, v11
	v_pk_mul_f32 v[18:19], v[96:97], s[30:31] op_sel_hi:[1,0]
	v_pk_mul_f32 v[16:17], v[122:123], s[28:29] op_sel_hi:[1,0]
	v_pk_mul_f32 v[14:15], v[124:125], s[28:29] op_sel_hi:[1,0]
	v_add_f32_e32 v28, 1.0, v30
	v_rcp_f32_e32 v11, v11
	s_nop 0
	v_mul_f32_e32 v11, v12, v11
	v_mul_f32_e32 v26, 0xbfb8aa3b, v6
	v_exp_f32_e32 v26, v26
	v_mul_f32_e32 v11, v20, v11
	v_add_f32_e32 v26, 1.0, v26
	v_rcp_f32_e32 v12, v28
	s_nop 0
	v_mul_f32_e32 v12, v13, v12
	v_mul_f32_e32 v12, v21, v12
	v_mul_f32_e32 v21, 0xbfb8aa3b, v7
	v_exp_f32_e32 v21, v21
	s_nop 0
	v_add_f32_e32 v21, 1.0, v21
	v_rcp_f32_e32 v13, v26
	s_nop 0
	v_mul_f32_e32 v6, v6, v13
	v_mul_f32_e32 v13, v18, v6
	v_rcp_f32_e32 v6, v21
	s_nop 0
	v_mul_f32_e32 v6, v7, v6
	v_mul_f32_e32 v7, v19, v6
	v_mul_f32_e32 v6, 0xbfb8aa3b, v16
	v_exp_f32_e32 v18, v6
	v_med3_f32 v11, v11, s75, v233
	v_med3_f32 v12, v12, s75, v233
	v_mov_b32_e32 v6, v203
	v_cvt_pk_fp8_f32 v6, v11, v12
	v_add_f32_e32 v11, 1.0, v18
	v_med3_f32 v13, v13, s75, v233
	v_med3_f32 v7, v7, s75, v233
	v_cvt_pk_fp8_f32 v6, v13, v7 op_sel:[0,0,1]
	v_mul_f32_e32 v19, 0xbfb8aa3b, v17
	v_exp_f32_e32 v19, v19
	s_nop 0
	v_add_f32_e32 v12, 1.0, v19
	v_rcp_f32_e32 v7, v11
	s_nop 0
	v_mul_f32_e32 v7, v16, v7
	v_mul_f32_e32 v16, 0xbfb8aa3b, v14
	v_exp_f32_e32 v16, v16
	s_nop 0
	v_add_f32_e32 v16, 1.0, v16
	v_rcp_f32_e32 v11, v12
	s_nop 0
	v_mul_f32_e32 v11, v17, v11
	v_mul_f32_e32 v17, 0xbfb8aa3b, v15
	v_exp_f32_e32 v17, v17
	s_nop 0
	v_add_f32_e32 v17, 1.0, v17
	v_rcp_f32_e32 v12, v16
	s_nop 0
	v_mul_f32_e32 v12, v14, v12
	v_pk_mul_f32 v[24:25], v[90:91], s[30:31] op_sel_hi:[1,0]
	v_mul_f32_e32 v7, v24, v7
	v_mul_f32_e32 v11, v25, v11
	v_med3_f32 v14, v7, s75, v233
	v_med3_f32 v11, v11, s75, v233
	v_mov_b32_e32 v7, v203
	v_cvt_pk_fp8_f32 v7, v14, v11
	v_pk_mul_f32 v[22:23], v[92:93], s[30:31] op_sel_hi:[1,0]
	v_rcp_f32_e32 v13, v17
	s_nop 0
	v_mul_f32_e32 v13, v15, v13
	v_mul_f32_e32 v12, v22, v12
	v_mul_f32_e32 v11, v23, v13
	v_med3_f32 v12, v12, s75, v233
	v_med3_f32 v11, v11, s75, v233
	v_pk_mul_f32 v[14:15], v[118:119], s[28:29] op_sel_hi:[1,0]
	v_cvt_pk_fp8_f32 v7, v12, v11 op_sel:[0,0,1]
	v_mul_f32_e32 v11, 0xbfb8aa3b, v14
	v_exp_f32_e32 v11, v11
	v_mul_f32_e32 v32, 0xbfb8aa3b, v15
	v_exp_f32_e32 v32, v32
	v_pk_mul_f32 v[12:13], v[120:121], s[28:29] op_sel_hi:[1,0]
	v_add_f32_e32 v11, 1.0, v11
	v_pk_mul_f32 v[22:23], v[86:87], s[30:31] op_sel_hi:[1,0]
	v_pk_mul_f32 v[20:21], v[88:89], s[30:31] op_sel_hi:[1,0]
	v_pk_mul_f32 v[18:19], v[114:115], s[28:29] op_sel_hi:[1,0]
	v_add_f32_e32 v30, 1.0, v32
	v_rcp_f32_e32 v11, v11
	s_nop 0
	v_mul_f32_e32 v11, v14, v11
	v_mul_f32_e32 v28, 0xbfb8aa3b, v12
	v_exp_f32_e32 v28, v28
	v_mul_f32_e32 v11, v22, v11
	v_add_f32_e32 v28, 1.0, v28
	v_rcp_f32_e32 v14, v30
	s_nop 0
	v_mul_f32_e32 v14, v15, v14
	v_mul_f32_e32 v14, v23, v14
	v_mul_f32_e32 v23, 0xbfb8aa3b, v13
	v_exp_f32_e32 v23, v23
	s_nop 0
	v_add_f32_e32 v23, 1.0, v23
	v_rcp_f32_e32 v15, v28
	s_nop 0
	v_mul_f32_e32 v12, v12, v15
	v_mul_f32_e32 v15, v20, v12
	v_rcp_f32_e32 v12, v23
	s_nop 0
	v_mul_f32_e32 v12, v13, v12
	v_mul_f32_e32 v13, v21, v12
	v_mul_f32_e32 v12, 0xbfb8aa3b, v18
	v_exp_f32_e32 v20, v12
	v_med3_f32 v11, v11, s75, v233
	v_med3_f32 v14, v14, s75, v233
	v_mov_b32_e32 v12, v203
	v_cvt_pk_fp8_f32 v12, v11, v14
	v_add_f32_e32 v11, 1.0, v20
	v_med3_f32 v15, v15, s75, v233
	v_med3_f32 v13, v13, s75, v233
	v_cvt_pk_fp8_f32 v12, v15, v13 op_sel:[0,0,1]
	v_mul_f32_e32 v21, 0xbfb8aa3b, v19
	v_exp_f32_e32 v21, v21
	s_nop 0
	v_add_f32_e32 v14, 1.0, v21
	v_pk_mul_f32 v[16:17], v[116:117], s[28:29] op_sel_hi:[1,0]
	v_rcp_f32_e32 v11, v11
	s_nop 0
	v_mul_f32_e32 v11, v18, v11
	v_mul_f32_e32 v18, 0xbfb8aa3b, v16
	v_exp_f32_e32 v18, v18
	s_nop 0
	v_add_f32_e32 v18, 1.0, v18
	v_rcp_f32_e32 v13, v14
	s_nop 0
	v_mul_f32_e32 v13, v19, v13
	v_mul_f32_e32 v19, 0xbfb8aa3b, v17
	v_exp_f32_e32 v19, v19
	s_nop 0
	v_add_f32_e32 v19, 1.0, v19
	v_rcp_f32_e32 v14, v18
	s_nop 0
	v_mul_f32_e32 v14, v16, v14
	v_pk_mul_f32 v[26:27], v[82:83], s[30:31] op_sel_hi:[1,0]
	v_mul_f32_e32 v11, v26, v11
	v_mul_f32_e32 v13, v27, v13
	v_med3_f32 v11, v11, s75, v233
	v_med3_f32 v16, v13, s75, v233
	v_mov_b32_e32 v13, v203
	v_cvt_pk_fp8_f32 v13, v11, v16
	v_pk_mul_f32 v[24:25], v[84:85], s[30:31] op_sel_hi:[1,0]
	v_rcp_f32_e32 v15, v19
	s_nop 0
	v_mul_f32_e32 v15, v17, v15
	ds_read_b128 v[2:5], v9 offset:1024
	v_mul_f32_e32 v14, v24, v14
	v_mul_f32_e32 v11, v25, v15
	v_med3_f32 v14, v14, s75, v233
	v_med3_f32 v11, v11, s75, v233
	v_cvt_pk_fp8_f32 v13, v14, v11 op_sel:[0,0,1]
	v_add_u32_e32 v11, 0x4000, v10
	s_waitcnt lgkmcnt(0)
	global_store_dwordx4 v11, v[2:5], s[16:17]
	ds_write_b64 v8, v[6:7]
	ds_write_b64 v8, v[12:13] offset:512
	v_pk_mul_f32 v[12:13], v[110:111], s[28:29] op_sel_hi:[1,0]
	v_pk_mul_f32 v[6:7], v[112:113], s[28:29] op_sel_hi:[1,0]
	v_mul_f32_e32 v11, 0xbfb8aa3b, v12
	v_exp_f32_e32 v11, v11
	v_mul_f32_e32 v30, 0xbfb8aa3b, v13
	v_exp_f32_e32 v30, v30
	v_pk_mul_f32 v[20:21], v[78:79], s[30:31] op_sel_hi:[1,0]
	v_add_f32_e32 v11, 1.0, v11
	v_pk_mul_f32 v[18:19], v[80:81], s[30:31] op_sel_hi:[1,0]
	v_pk_mul_f32 v[16:17], v[106:107], s[28:29] op_sel_hi:[1,0]
	v_pk_mul_f32 v[14:15], v[108:109], s[28:29] op_sel_hi:[1,0]
	v_add_f32_e32 v28, 1.0, v30
	v_rcp_f32_e32 v11, v11
	s_nop 0
	v_mul_f32_e32 v11, v12, v11
	v_mul_f32_e32 v26, 0xbfb8aa3b, v6
	v_exp_f32_e32 v26, v26
	v_mul_f32_e32 v11, v20, v11
	v_add_f32_e32 v26, 1.0, v26
	v_rcp_f32_e32 v12, v28
	s_nop 0
	v_mul_f32_e32 v12, v13, v12
	v_mul_f32_e32 v12, v21, v12
	v_mul_f32_e32 v21, 0xbfb8aa3b, v7
	v_exp_f32_e32 v21, v21
	s_nop 0
	v_add_f32_e32 v21, 1.0, v21
	v_rcp_f32_e32 v13, v26
	s_nop 0
	v_mul_f32_e32 v6, v6, v13
	v_mul_f32_e32 v13, v18, v6
	v_rcp_f32_e32 v6, v21
	s_nop 0
	v_mul_f32_e32 v6, v7, v6
	v_mul_f32_e32 v7, v19, v6
	v_mul_f32_e32 v6, 0xbfb8aa3b, v16
	v_exp_f32_e32 v18, v6
	v_med3_f32 v11, v11, s75, v233
	v_med3_f32 v12, v12, s75, v233
	v_mov_b32_e32 v6, v203
	v_cvt_pk_fp8_f32 v6, v11, v12
	v_add_f32_e32 v11, 1.0, v18
	v_med3_f32 v13, v13, s75, v233
	v_med3_f32 v7, v7, s75, v233
	v_cvt_pk_fp8_f32 v6, v13, v7 op_sel:[0,0,1]
	v_mul_f32_e32 v19, 0xbfb8aa3b, v17
	v_exp_f32_e32 v19, v19
	s_nop 0
	v_add_f32_e32 v12, 1.0, v19
	v_rcp_f32_e32 v7, v11
	s_nop 0
	v_mul_f32_e32 v7, v16, v7
	v_mul_f32_e32 v16, 0xbfb8aa3b, v14
	v_exp_f32_e32 v16, v16
	s_nop 0
	v_add_f32_e32 v16, 1.0, v16
	v_rcp_f32_e32 v11, v12
	s_nop 0
	v_mul_f32_e32 v11, v17, v11
	v_mul_f32_e32 v17, 0xbfb8aa3b, v15
	v_exp_f32_e32 v17, v17
	s_nop 0
	v_add_f32_e32 v17, 1.0, v17
	v_rcp_f32_e32 v12, v16
	s_nop 0
	v_mul_f32_e32 v12, v14, v12
	v_pk_mul_f32 v[24:25], v[74:75], s[30:31] op_sel_hi:[1,0]
	v_mul_f32_e32 v7, v24, v7
	v_mul_f32_e32 v11, v25, v11
	v_med3_f32 v14, v7, s75, v233
	v_med3_f32 v11, v11, s75, v233
	v_mov_b32_e32 v7, v203
	v_cvt_pk_fp8_f32 v7, v14, v11
	v_pk_mul_f32 v[22:23], v[76:77], s[30:31] op_sel_hi:[1,0]
	v_rcp_f32_e32 v13, v17
	s_nop 0
	v_mul_f32_e32 v13, v15, v13
	v_mul_f32_e32 v12, v22, v12
	v_mul_f32_e32 v11, v23, v13
	v_med3_f32 v12, v12, s75, v233
	v_med3_f32 v11, v11, s75, v233
	v_pk_mul_f32 v[14:15], v[102:103], s[28:29] op_sel_hi:[1,0]
	v_cvt_pk_fp8_f32 v7, v12, v11 op_sel:[0,0,1]
	v_mul_f32_e32 v11, 0xbfb8aa3b, v14
	v_exp_f32_e32 v11, v11
	v_mul_f32_e32 v32, 0xbfb8aa3b, v15
	v_exp_f32_e32 v32, v32
	v_pk_mul_f32 v[12:13], v[104:105], s[28:29] op_sel_hi:[1,0]
	v_add_f32_e32 v11, 1.0, v11
	v_pk_mul_f32 v[22:23], v[70:71], s[30:31] op_sel_hi:[1,0]
	v_pk_mul_f32 v[20:21], v[72:73], s[30:31] op_sel_hi:[1,0]
	v_pk_mul_f32 v[18:19], v[98:99], s[28:29] op_sel_hi:[1,0]
	v_add_f32_e32 v30, 1.0, v32
	v_rcp_f32_e32 v11, v11
	s_nop 0
	v_mul_f32_e32 v11, v14, v11
	v_mul_f32_e32 v28, 0xbfb8aa3b, v12
	v_exp_f32_e32 v28, v28
	v_mul_f32_e32 v11, v22, v11
	v_add_f32_e32 v28, 1.0, v28
	v_rcp_f32_e32 v14, v30
	s_nop 0
	v_mul_f32_e32 v14, v15, v14
	v_mul_f32_e32 v14, v23, v14
	v_mul_f32_e32 v23, 0xbfb8aa3b, v13
	v_exp_f32_e32 v23, v23
	s_nop 0
	v_add_f32_e32 v23, 1.0, v23
	v_rcp_f32_e32 v15, v28
	s_nop 0
	v_mul_f32_e32 v12, v12, v15
	v_mul_f32_e32 v15, v20, v12
	v_rcp_f32_e32 v12, v23
	s_nop 0
	v_mul_f32_e32 v12, v13, v12
	v_mul_f32_e32 v13, v21, v12
	v_mul_f32_e32 v12, 0xbfb8aa3b, v18
	v_exp_f32_e32 v20, v12
	v_med3_f32 v11, v11, s75, v233
	v_med3_f32 v14, v14, s75, v233
	v_mov_b32_e32 v12, v203
	v_cvt_pk_fp8_f32 v12, v11, v14
	v_add_f32_e32 v11, 1.0, v20
	v_med3_f32 v15, v15, s75, v233
	v_med3_f32 v13, v13, s75, v233
	v_cvt_pk_fp8_f32 v12, v15, v13 op_sel:[0,0,1]
	v_mul_f32_e32 v21, 0xbfb8aa3b, v19
	v_exp_f32_e32 v21, v21
	s_nop 0
	v_add_f32_e32 v14, 1.0, v21
	v_pk_mul_f32 v[16:17], v[100:101], s[28:29] op_sel_hi:[1,0]
	v_rcp_f32_e32 v11, v11
	s_nop 0
	v_mul_f32_e32 v11, v18, v11
	v_mul_f32_e32 v18, 0xbfb8aa3b, v16
	v_exp_f32_e32 v18, v18
	s_nop 0
	v_add_f32_e32 v18, 1.0, v18
	v_rcp_f32_e32 v13, v14
	s_nop 0
	v_mul_f32_e32 v13, v19, v13
	v_mul_f32_e32 v19, 0xbfb8aa3b, v17
	v_exp_f32_e32 v19, v19
	s_nop 0
	v_add_f32_e32 v19, 1.0, v19
	v_rcp_f32_e32 v14, v18
	s_nop 0
	v_mul_f32_e32 v14, v16, v14
	v_pk_mul_f32 v[26:27], v[66:67], s[30:31] op_sel_hi:[1,0]
	v_mul_f32_e32 v11, v26, v11
	v_mul_f32_e32 v13, v27, v13
	v_med3_f32 v11, v11, s75, v233
	v_med3_f32 v16, v13, s75, v233
	v_mov_b32_e32 v13, v203
	v_cvt_pk_fp8_f32 v13, v11, v16
	v_pk_mul_f32 v[24:25], v[68:69], s[30:31] op_sel_hi:[1,0]
	v_rcp_f32_e32 v15, v19
	s_nop 0
	v_mul_f32_e32 v15, v17, v15
	ds_read_b128 v[2:5], v9
	v_mul_f32_e32 v14, v24, v14
	v_mul_f32_e32 v11, v25, v15
	v_med3_f32 v14, v14, s75, v233
	v_med3_f32 v11, v11, s75, v233
	v_cvt_pk_fp8_f32 v13, v14, v11 op_sel:[0,0,1]
	v_add_u32_e32 v11, 0x10000, v10
	s_waitcnt lgkmcnt(0)
	global_store_dwordx4 v11, v[2:5], s[16:17]
	ds_write_b64 v8, v[6:7] offset:1024
	ds_write_b64 v8, v[12:13] offset:1536
	ds_read_b128 v[2:5], v9 offset:1024
	v_add_u32_e32 v6, 0x14000, v10
	s_andn2_b64 vcc, exec, s[42:43]
	s_waitcnt lgkmcnt(0)
	global_store_dwordx4 v6, v[2:5], s[16:17]
	s_cbranch_vccnz .LBB0_1856
	s_andn2_b64 vcc, exec, s[20:21]
	s_cbranch_vccnz .LBB0_1823
	s_barrier
	s_branch .LBB0_1823

.LBB0_1974:
	v_pk_mul_f32 v[4:5], v[186:187], v[0:1] op_sel_hi:[1,0]
	v_pk_mul_f32 v[6:7], v[184:185], v[0:1] op_sel_hi:[1,0]
	v_pk_mul_f32 v[10:11], v[180:181], v[0:1] op_sel_hi:[1,0]
	v_med3_f32 v3, v6, s74, v250
	v_med3_f32 v6, v7, s74, v250
	v_med3_f32 v7, v4, s74, v250
	v_mov_b32_e32 v4, v207
	v_med3_f32 v18, v5, s74, v250
	v_cvt_pk_fp8_f32 v4, v3, v6
	v_med3_f32 v3, v10, s74, v250
	v_med3_f32 v6, v11, s74, v250
	v_mov_b32_e32 v5, v207
	v_cvt_pk_fp8_f32 v5, v3, v6
	v_pk_mul_f32 v[8:9], v[182:183], v[0:1] op_sel_hi:[1,0]
	v_pk_mul_f32 v[14:15], v[192:193], v[0:1] op_sel_hi:[1,0]
	v_med3_f32 v3, v8, s74, v250
	v_med3_f32 v6, v9, s74, v250
	v_pk_mul_f32 v[12:13], v[194:195], v[0:1] op_sel_hi:[1,0]
	v_pk_mul_f32 v[16:17], v[190:191], v[0:1] op_sel_hi:[1,0]
	v_pk_mul_f32 v[0:1], v[188:189], v[0:1] op_sel_hi:[1,0]
	v_cvt_pk_fp8_f32 v4, v7, v18 op_sel:[0,0,1]
	v_cvt_pk_fp8_f32 v5, v3, v6 op_sel:[0,0,1]
	v_med3_f32 v3, v14, s74, v250
	v_med3_f32 v7, v15, s74, v250
	v_mov_b32_e32 v6, v207
	v_cvt_pk_fp8_f32 v6, v3, v7
	v_med3_f32 v0, v0, s74, v250
	v_med3_f32 v1, v1, s74, v250
	v_mov_b32_e32 v7, v207
	v_cvt_pk_fp8_f32 v7, v0, v1
	v_med3_f32 v8, v12, s74, v250
	v_med3_f32 v9, v13, s74, v250
	v_med3_f32 v0, v16, s74, v250
	v_med3_f32 v1, v17, s74, v250
	v_cvt_pk_fp8_f32 v6, v8, v9 op_sel:[0,0,1]
	v_cvt_pk_fp8_f32 v7, v0, v1 op_sel:[0,0,1]
	v_add_u32_e32 v0, v232, v236
	v_ashrrev_i32_e32 v1, 31, v0
	v_lshlrev_b64 v[8:9], 11, v[0:1]
	ds_write_b128 v251, v[4:7]
	ds_read_b128 v[4:7], v252
	s_lshl_b32 s40, s40, 8
	v_lshl_add_u64 v[8:9], s[16:17], 0, v[8:9]
	s_ashr_i32 s41, s40, 31
	v_lshl_add_u64 v[8:9], v[8:9], 0, s[40:41]
	v_lshl_add_u64 v[8:9], v[8:9], 0, s[12:13]
	v_cndmask_b32_e64 v1, 0, 1, s[46:47]
	v_lshl_add_u64 v[8:9], v[8:9], 0, v[214:215]
	v_cmp_ne_u32_e64 s[2:3], 1, v1
	s_andn2_b64 vcc, exec, s[46:47]
	s_waitcnt lgkmcnt(0)
	global_store_dwordx4 v[8:9], v[4:7], off
	s_cbranch_vccnz .LBB0_1978
	v_or_b32_e32 v1, 16, v234
	v_cmp_lt_i32_e32 vcc, v1, v233
	s_waitcnt vmcnt(6)
	v_mul_f32_e32 v2, 0.5, v25
	v_cndmask_b32_e32 v2, 0, v2, vcc
.LBB0_1978:
	s_nop 0
	v_pk_mul_f32 v[6:7], v[168:169], v[2:3] op_sel_hi:[1,0]
	v_pk_mul_f32 v[4:5], v[170:171], v[2:3] op_sel_hi:[1,0]
	v_pk_mul_f32 v[8:9], v[166:167], v[2:3] op_sel_hi:[1,0]
	v_pk_mul_f32 v[10:11], v[164:165], v[2:3] op_sel_hi:[1,0]
	v_pk_mul_f32 v[12:13], v[178:179], v[2:3] op_sel_hi:[1,0]
	v_pk_mul_f32 v[14:15], v[176:177], v[2:3] op_sel_hi:[1,0]
	v_pk_mul_f32 v[16:17], v[174:175], v[2:3] op_sel_hi:[1,0]
	v_pk_mul_f32 v[18:19], v[172:173], v[2:3] op_sel_hi:[1,0]
	v_med3_f32 v1, v6, s74, v250
	v_med3_f32 v3, v7, s74, v250
	v_mov_b32_e32 v2, v207
	v_cvt_pk_fp8_f32 v2, v1, v3
	v_med3_f32 v1, v10, s74, v250
	v_med3_f32 v6, v11, s74, v250
	v_mov_b32_e32 v3, v207
	v_cvt_pk_fp8_f32 v3, v1, v6
	v_med3_f32 v4, v4, s74, v250
	v_med3_f32 v5, v5, s74, v250
	v_cvt_pk_fp8_f32 v2, v4, v5 op_sel:[0,0,1]
	v_med3_f32 v1, v8, s74, v250
	v_med3_f32 v4, v9, s74, v250
	v_cvt_pk_fp8_f32 v3, v1, v4 op_sel:[0,0,1]
	v_med3_f32 v1, v14, s74, v250
	v_med3_f32 v5, v15, s74, v250
	v_mov_b32_e32 v4, v207
	v_cvt_pk_fp8_f32 v4, v1, v5
	v_med3_f32 v1, v18, s74, v250
	v_med3_f32 v8, v19, s74, v250
	v_mov_b32_e32 v5, v207
	v_cvt_pk_fp8_f32 v5, v1, v8
	v_med3_f32 v6, v12, s74, v250
	v_med3_f32 v7, v13, s74, v250
	v_cvt_pk_fp8_f32 v4, v6, v7 op_sel:[0,0,1]
	v_med3_f32 v1, v16, s74, v250
	v_med3_f32 v6, v17, s74, v250
	v_cvt_pk_fp8_f32 v5, v1, v6 op_sel:[0,0,1]
	v_or_b32_e32 v1, 16, v236
	v_add_u32_e32 v6, v1, v232
	v_ashrrev_i32_e32 v7, 31, v6
	ds_write_b128 v251, v[2:5] offset:1024
	ds_read_b128 v[2:5], v252 offset:1024
	v_lshlrev_b64 v[6:7], 11, v[6:7]
	v_lshl_add_u64 v[6:7], s[16:17], 0, v[6:7]
	v_lshl_add_u64 v[6:7], v[6:7], 0, s[40:41]
	v_lshl_add_u64 v[6:7], v[6:7], 0, s[12:13]
	v_lshl_add_u64 v[6:7], v[6:7], 0, v[214:215]
	s_waitcnt lgkmcnt(0)
	global_store_dwordx4 v[6:7], v[2:5], off
	s_and_b64 vcc, exec, s[2:3]
	s_nop 0
	v_mov_b32_e32 v2, 0.5
	v_mov_b32_e32 v4, 0.5
	s_cbranch_vccnz .LBB0_1982
	v_or_b32_e32 v1, 32, v234
	v_cmp_lt_i32_e32 vcc, v1, v233
	s_waitcnt vmcnt(5)
	v_mul_f32_e32 v4, 0.5, v26
	v_cndmask_b32_e32 v4, 0, v4, vcc
.LBB0_1982:
	v_pk_mul_f32 v[8:9], v[152:153], v[4:5] op_sel_hi:[1,0]
	v_pk_mul_f32 v[6:7], v[154:155], v[4:5] op_sel_hi:[1,0]
	v_pk_mul_f32 v[10:11], v[150:151], v[4:5] op_sel_hi:[1,0]
	v_pk_mul_f32 v[12:13], v[148:149], v[4:5] op_sel_hi:[1,0]
	v_pk_mul_f32 v[14:15], v[162:163], v[4:5] op_sel_hi:[1,0]
	v_pk_mul_f32 v[16:17], v[160:161], v[4:5] op_sel_hi:[1,0]
	v_pk_mul_f32 v[18:19], v[158:159], v[4:5] op_sel_hi:[1,0]
	v_pk_mul_f32 v[20:21], v[156:157], v[4:5] op_sel_hi:[1,0]
	v_med3_f32 v1, v8, s74, v250
	v_med3_f32 v3, v9, s74, v250
	v_mov_b32_e32 v4, v207
	v_cvt_pk_fp8_f32 v4, v1, v3
	v_med3_f32 v1, v12, s74, v250
	v_med3_f32 v3, v13, s74, v250
	v_mov_b32_e32 v5, v207
	v_cvt_pk_fp8_f32 v5, v1, v3
	v_med3_f32 v6, v6, s74, v250
	v_med3_f32 v7, v7, s74, v250
	v_med3_f32 v1, v10, s74, v250
	v_med3_f32 v3, v11, s74, v250
	v_cvt_pk_fp8_f32 v4, v6, v7 op_sel:[0,0,1]
	v_cvt_pk_fp8_f32 v5, v1, v3 op_sel:[0,0,1]
	v_med3_f32 v1, v16, s74, v250
	v_med3_f32 v3, v17, s74, v250
	v_mov_b32_e32 v6, v207
	v_cvt_pk_fp8_f32 v6, v1, v3
	v_med3_f32 v1, v20, s74, v250
	v_med3_f32 v3, v21, s74, v250
	v_mov_b32_e32 v7, v207
	v_cvt_pk_fp8_f32 v7, v1, v3
	v_med3_f32 v8, v14, s74, v250
	v_med3_f32 v9, v15, s74, v250
	v_med3_f32 v1, v18, s74, v250
	v_med3_f32 v3, v19, s74, v250
	v_cvt_pk_fp8_f32 v6, v8, v9 op_sel:[0,0,1]
	v_cvt_pk_fp8_f32 v7, v1, v3 op_sel:[0,0,1]
	v_add_u32_e32 v8, v239, v232
	v_ashrrev_i32_e32 v9, 31, v8
	v_lshlrev_b64 v[8:9], 11, v[8:9]
	ds_write_b128 v251, v[4:7]
	ds_read_b128 v[4:7], v252
	v_lshl_add_u64 v[8:9], s[16:17], 0, v[8:9]
	v_lshl_add_u64 v[8:9], v[8:9], 0, s[40:41]
	v_lshl_add_u64 v[8:9], v[8:9], 0, s[12:13]
	v_lshl_add_u64 v[8:9], v[8:9], 0, v[214:215]
	s_and_b64 vcc, exec, s[2:3]
	s_waitcnt lgkmcnt(0)
	global_store_dwordx4 v[8:9], v[4:7], off
	s_cbranch_vccnz .LBB0_1986
	v_or_b32_e32 v1, 48, v234
	v_cmp_lt_i32_e32 vcc, v1, v233
	s_waitcnt vmcnt(4)
	v_mul_f32_e32 v2, 0.5, v27
	v_cndmask_b32_e32 v2, 0, v2, vcc
.LBB0_1986:
	s_nop 0
	v_pk_mul_f32 v[6:7], v[120:121], v[2:3] op_sel_hi:[1,0]
	v_pk_mul_f32 v[4:5], v[122:123], v[2:3] op_sel_hi:[1,0]
	v_pk_mul_f32 v[8:9], v[118:119], v[2:3] op_sel_hi:[1,0]
	v_pk_mul_f32 v[10:11], v[116:117], v[2:3] op_sel_hi:[1,0]
	v_pk_mul_f32 v[12:13], v[130:131], v[2:3] op_sel_hi:[1,0]
	v_pk_mul_f32 v[14:15], v[128:129], v[2:3] op_sel_hi:[1,0]
	v_pk_mul_f32 v[16:17], v[126:127], v[2:3] op_sel_hi:[1,0]
	v_pk_mul_f32 v[18:19], v[124:125], v[2:3] op_sel_hi:[1,0]
	v_med3_f32 v1, v6, s74, v250
	v_med3_f32 v3, v7, s74, v250
	v_mov_b32_e32 v2, v207
	v_cvt_pk_fp8_f32 v2, v1, v3
	v_med3_f32 v1, v10, s74, v250
	v_med3_f32 v6, v11, s74, v250
	v_mov_b32_e32 v3, v207
	v_cvt_pk_fp8_f32 v3, v1, v6
	v_med3_f32 v4, v4, s74, v250
	v_med3_f32 v5, v5, s74, v250
	v_cvt_pk_fp8_f32 v2, v4, v5 op_sel:[0,0,1]
	v_med3_f32 v1, v8, s74, v250
	v_med3_f32 v4, v9, s74, v250
	v_cvt_pk_fp8_f32 v3, v1, v4 op_sel:[0,0,1]
	v_med3_f32 v1, v14, s74, v250
	v_med3_f32 v5, v15, s74, v250
	v_mov_b32_e32 v4, v207
	v_cvt_pk_fp8_f32 v4, v1, v5
	v_med3_f32 v1, v18, s74, v250
	v_med3_f32 v8, v19, s74, v250
	v_mov_b32_e32 v5, v207
	v_cvt_pk_fp8_f32 v5, v1, v8
	v_med3_f32 v6, v12, s74, v250
	v_med3_f32 v7, v13, s74, v250
	v_cvt_pk_fp8_f32 v4, v6, v7 op_sel:[0,0,1]
	v_med3_f32 v1, v16, s74, v250
	v_med3_f32 v6, v17, s74, v250
	v_cvt_pk_fp8_f32 v5, v1, v6 op_sel:[0,0,1]
	v_add_u32_e32 v6, v241, v232
	v_ashrrev_i32_e32 v7, 31, v6
	v_lshlrev_b64 v[6:7], 11, v[6:7]
	ds_write_b128 v251, v[2:5] offset:1024
	ds_read_b128 v[2:5], v252 offset:1024
	v_lshl_add_u64 v[6:7], s[16:17], 0, v[6:7]
	v_lshl_add_u64 v[6:7], v[6:7], 0, s[40:41]
	v_lshl_add_u64 v[6:7], v[6:7], 0, s[12:13]
	v_lshl_add_u64 v[6:7], v[6:7], 0, v[214:215]
	s_waitcnt lgkmcnt(0)
	global_store_dwordx4 v[6:7], v[2:5], off
	s_and_b64 vcc, exec, s[2:3]
	s_nop 0
	v_mov_b32_e32 v2, 0.5
	v_mov_b32_e32 v4, 0.5
	s_cbranch_vccnz .LBB0_1990
	v_add_u32_e32 v1, 0x80, v234
	v_cmp_lt_i32_e32 vcc, v1, v233
	s_waitcnt vmcnt(3)
	v_mul_f32_e32 v4, 0.5, v28
	v_cndmask_b32_e32 v4, 0, v4, vcc
.LBB0_1990:
	v_pk_mul_f32 v[8:9], v[136:137], v[4:5] op_sel_hi:[1,0]
	v_pk_mul_f32 v[6:7], v[138:139], v[4:5] op_sel_hi:[1,0]
	v_pk_mul_f32 v[10:11], v[134:135], v[4:5] op_sel_hi:[1,0]
	v_pk_mul_f32 v[12:13], v[132:133], v[4:5] op_sel_hi:[1,0]
	v_pk_mul_f32 v[14:15], v[146:147], v[4:5] op_sel_hi:[1,0]
	v_pk_mul_f32 v[16:17], v[144:145], v[4:5] op_sel_hi:[1,0]
	v_pk_mul_f32 v[18:19], v[142:143], v[4:5] op_sel_hi:[1,0]
	v_pk_mul_f32 v[20:21], v[140:141], v[4:5] op_sel_hi:[1,0]
	v_med3_f32 v1, v8, s74, v250
	v_med3_f32 v3, v9, s74, v250
	v_mov_b32_e32 v4, v207
	v_cvt_pk_fp8_f32 v4, v1, v3
	v_med3_f32 v1, v12, s74, v250
	v_med3_f32 v3, v13, s74, v250
	v_mov_b32_e32 v5, v207
	v_cvt_pk_fp8_f32 v5, v1, v3
	v_med3_f32 v6, v6, s74, v250
	v_med3_f32 v7, v7, s74, v250
	v_med3_f32 v1, v10, s74, v250
	v_med3_f32 v3, v11, s74, v250
	v_cvt_pk_fp8_f32 v4, v6, v7 op_sel:[0,0,1]
	v_cvt_pk_fp8_f32 v5, v1, v3 op_sel:[0,0,1]
	v_med3_f32 v1, v16, s74, v250
	v_med3_f32 v3, v17, s74, v250
	v_mov_b32_e32 v6, v207
	v_cvt_pk_fp8_f32 v6, v1, v3
	v_med3_f32 v1, v20, s74, v250
	v_med3_f32 v3, v21, s74, v250
	v_mov_b32_e32 v7, v207
	v_cvt_pk_fp8_f32 v7, v1, v3
	v_med3_f32 v8, v14, s74, v250
	v_med3_f32 v9, v15, s74, v250
	v_med3_f32 v1, v18, s74, v250
	v_med3_f32 v3, v19, s74, v250
	v_cvt_pk_fp8_f32 v6, v8, v9 op_sel:[0,0,1]
	v_cvt_pk_fp8_f32 v7, v1, v3 op_sel:[0,0,1]
	v_add_u32_e32 v8, 0x80, v0
	v_ashrrev_i32_e32 v9, 31, v8
	v_lshlrev_b64 v[8:9], 11, v[8:9]
	ds_write_b128 v251, v[4:7]
	ds_read_b128 v[4:7], v252
	v_lshl_add_u64 v[8:9], s[16:17], 0, v[8:9]
	v_lshl_add_u64 v[8:9], v[8:9], 0, s[40:41]
	v_lshl_add_u64 v[8:9], v[8:9], 0, s[12:13]
	v_lshl_add_u64 v[8:9], v[8:9], 0, v[214:215]
	s_and_b64 vcc, exec, s[2:3]
	s_waitcnt lgkmcnt(0)
	global_store_dwordx4 v[8:9], v[4:7], off
	s_cbranch_vccnz .LBB0_1994
	v_add_u32_e32 v1, 0x90, v234
	v_cmp_lt_i32_e32 vcc, v1, v233
	s_waitcnt vmcnt(2)
	v_mul_f32_e32 v2, 0.5, v29
	v_cndmask_b32_e32 v2, 0, v2, vcc
.LBB0_1994:
	s_nop 0
	v_pk_mul_f32 v[6:7], v[104:105], v[2:3] op_sel_hi:[1,0]
	v_pk_mul_f32 v[4:5], v[106:107], v[2:3] op_sel_hi:[1,0]
	v_pk_mul_f32 v[8:9], v[102:103], v[2:3] op_sel_hi:[1,0]
	v_pk_mul_f32 v[10:11], v[100:101], v[2:3] op_sel_hi:[1,0]
	v_pk_mul_f32 v[12:13], v[114:115], v[2:3] op_sel_hi:[1,0]
	v_pk_mul_f32 v[14:15], v[112:113], v[2:3] op_sel_hi:[1,0]
	v_pk_mul_f32 v[16:17], v[110:111], v[2:3] op_sel_hi:[1,0]
	v_pk_mul_f32 v[18:19], v[108:109], v[2:3] op_sel_hi:[1,0]
	v_med3_f32 v1, v6, s74, v250
	v_med3_f32 v3, v7, s74, v250
	v_mov_b32_e32 v2, v207
	v_cvt_pk_fp8_f32 v2, v1, v3
	v_med3_f32 v1, v10, s74, v250
	v_med3_f32 v6, v11, s74, v250
	v_mov_b32_e32 v3, v207
	v_cvt_pk_fp8_f32 v3, v1, v6
	v_med3_f32 v4, v4, s74, v250
	v_med3_f32 v5, v5, s74, v250
	v_cvt_pk_fp8_f32 v2, v4, v5 op_sel:[0,0,1]
	v_med3_f32 v1, v8, s74, v250
	v_med3_f32 v4, v9, s74, v250
	v_cvt_pk_fp8_f32 v3, v1, v4 op_sel:[0,0,1]
	v_med3_f32 v1, v14, s74, v250
	v_med3_f32 v5, v15, s74, v250
	v_mov_b32_e32 v4, v207
	v_cvt_pk_fp8_f32 v4, v1, v5
	v_med3_f32 v1, v18, s74, v250
	v_med3_f32 v8, v19, s74, v250
	v_mov_b32_e32 v5, v207
	v_cvt_pk_fp8_f32 v5, v1, v8
	v_med3_f32 v6, v12, s74, v250
	v_med3_f32 v7, v13, s74, v250
	v_cvt_pk_fp8_f32 v4, v6, v7 op_sel:[0,0,1]
	v_med3_f32 v1, v16, s74, v250
	v_med3_f32 v6, v17, s74, v250
	v_cvt_pk_fp8_f32 v5, v1, v6 op_sel:[0,0,1]
	v_add_u32_e32 v6, 0x90, v0
	v_ashrrev_i32_e32 v7, 31, v6
	v_lshlrev_b64 v[6:7], 11, v[6:7]
	ds_write_b128 v251, v[2:5] offset:1024
	ds_read_b128 v[2:5], v252 offset:1024
	v_lshl_add_u64 v[6:7], s[16:17], 0, v[6:7]
	v_lshl_add_u64 v[6:7], v[6:7], 0, s[40:41]
	v_lshl_add_u64 v[6:7], v[6:7], 0, s[12:13]
	v_lshl_add_u64 v[6:7], v[6:7], 0, v[214:215]
	s_waitcnt lgkmcnt(0)
	global_store_dwordx4 v[6:7], v[2:5], off
	s_and_b64 vcc, exec, s[2:3]
	s_nop 0
	v_mov_b32_e32 v2, 0.5
	v_mov_b32_e32 v4, 0.5
	s_cbranch_vccnz .LBB0_1998
	v_cmp_lt_i32_e32 vcc, v244, v233
	s_waitcnt vmcnt(1)
	v_mul_f32_e32 v4, 0.5, v30
	v_cndmask_b32_e32 v4, 0, v4, vcc
.LBB0_1998:
	v_pk_mul_f32 v[8:9], v[88:89], v[4:5] op_sel_hi:[1,0]
	v_pk_mul_f32 v[6:7], v[90:91], v[4:5] op_sel_hi:[1,0]
	v_pk_mul_f32 v[10:11], v[86:87], v[4:5] op_sel_hi:[1,0]
	v_pk_mul_f32 v[12:13], v[84:85], v[4:5] op_sel_hi:[1,0]
	v_pk_mul_f32 v[14:15], v[98:99], v[4:5] op_sel_hi:[1,0]
	v_pk_mul_f32 v[16:17], v[96:97], v[4:5] op_sel_hi:[1,0]
	v_pk_mul_f32 v[18:19], v[94:95], v[4:5] op_sel_hi:[1,0]
	v_pk_mul_f32 v[20:21], v[92:93], v[4:5] op_sel_hi:[1,0]
	v_med3_f32 v1, v8, s74, v250
	v_med3_f32 v3, v9, s74, v250
	v_mov_b32_e32 v4, v207
	v_cvt_pk_fp8_f32 v4, v1, v3
	v_med3_f32 v1, v12, s74, v250
	v_med3_f32 v3, v13, s74, v250
	v_mov_b32_e32 v5, v207
	v_cvt_pk_fp8_f32 v5, v1, v3
	v_med3_f32 v6, v6, s74, v250
	v_med3_f32 v7, v7, s74, v250
	v_med3_f32 v1, v10, s74, v250
	v_med3_f32 v3, v11, s74, v250
	v_cvt_pk_fp8_f32 v4, v6, v7 op_sel:[0,0,1]
	v_cvt_pk_fp8_f32 v5, v1, v3 op_sel:[0,0,1]
	v_med3_f32 v1, v16, s74, v250
	v_med3_f32 v3, v17, s74, v250
	v_mov_b32_e32 v6, v207
	v_cvt_pk_fp8_f32 v6, v1, v3
	v_med3_f32 v1, v20, s74, v250
	v_med3_f32 v3, v21, s74, v250
	v_mov_b32_e32 v7, v207
	v_cvt_pk_fp8_f32 v7, v1, v3
	v_med3_f32 v8, v14, s74, v250
	v_med3_f32 v9, v15, s74, v250
	v_med3_f32 v1, v18, s74, v250
	v_med3_f32 v3, v19, s74, v250
	v_cvt_pk_fp8_f32 v6, v8, v9 op_sel:[0,0,1]
	v_cvt_pk_fp8_f32 v7, v1, v3 op_sel:[0,0,1]
	v_add_u32_e32 v8, 0xa0, v0
	v_ashrrev_i32_e32 v9, 31, v8
	v_lshlrev_b64 v[8:9], 11, v[8:9]
	ds_write_b128 v251, v[4:7]
	ds_read_b128 v[4:7], v252
	v_lshl_add_u64 v[8:9], s[16:17], 0, v[8:9]
	v_lshl_add_u64 v[8:9], v[8:9], 0, s[40:41]
	v_lshl_add_u64 v[8:9], v[8:9], 0, s[12:13]
	v_lshl_add_u64 v[8:9], v[8:9], 0, v[214:215]
	s_and_b64 vcc, exec, s[2:3]
	s_waitcnt lgkmcnt(0)
	global_store_dwordx4 v[8:9], v[4:7], off
	s_cbranch_vccnz .LBB0_2002
	v_cmp_lt_i32_e32 vcc, v245, v233
	s_waitcnt vmcnt(0)
	v_mul_f32_e32 v2, 0.5, v31
	v_cndmask_b32_e32 v2, 0, v2, vcc
